# K loops: fragment-load segment at priority 1, MFMA segment at priority 0 (swapped)
# baseline (speedup 1.0000x reference)
; #define GAS __attribute__((address_space(1)))
; #define PG8_STAGE(bufoff, gbase, voff) do { _Pragma("unroll") for (int _i = 0; _i < 2; ++_i) \
;         __builtin_amdgcn_global_load_lds((const GAS unsigned*)((const GAS char*)(gbase) + (voff)[_i]), (LAS unsigned*)(lds + (bufoff) + ldsw + _i * 8192), 16, 0, 0); } while (0)
; #define PG8_LDA(dst, b, h) do { _Pragma("unroll") for (int m = 0; m < 4; ++m) { dst[m].lo = *(const LAS i32x4v*)(lds + PG8_SA(b, h) + (FP8 ? aoff8[0] : aoff) + m * 2048); dst[m].hi = *(const LAS i32x4v*)(lds + PG8_SA(b, h) + (FP8 ? aoff8[1] : aoff + 1024) + m * 2048); } } while (0)
; #define PG8_LDB(dst, b, h) do { _Pragma("unroll") for (int n = 0; n < 2; ++n) { dst[n].lo = *(const LAS i32x4v*)(lds + PG8_SB(b, h) + (FP8 ? boff8[0] : boff) + n * 2048); dst[n].hi = *(const LAS i32x4v*)(lds + PG8_SB(b, h) + (FP8 ? boff8[1] : boff + 1024) + n * 2048); } } while (0)
; #define PG8_WAIT_V(n) asm volatile("s_waitcnt vmcnt(" #n ")" ::: "memory")
; template <class Epi, class Sched, bool GATHER, bool FP8 = false, bool UNI = false>
; __device__ __forceinline__ void gemm_phase(LAS unsigned char* lds, const Sched& S, const Epi& E) {
;     ...
;         for (int t = 0; t < nt; t += 2) {
;             const bool last = (t == nt - 2);
;             const GAS char* a1 = cA + (size_t)(t + 1) * 128;
;             const GAS char* a2 = last ? nA : cA + (size_t)(t + 2) * 128; const GAS char* b2 = last ? nB : cB + (size_t)(t + 2) * 128;
;             const GAS char* a3 = a2 + 128; const GAS char* b3 = b2 + 128;
;             const size_t hB2 = last ? hBn : hBc;
;             unsigned oa0[2], oa1[2], ob[2];
; #pragma unroll
;             for (int i = 0; i < 2; ++i) { if constexpr (UNI) { oa0[i] = aoc[0][i]; oa1[i] = aoc[1][i]; ob[i] = boc[i]; } else { oa0[i] = last ? aon[0][i] : aoc[0][i]; oa1[i] = last ? aon[1][i] : aoc[1][i]; ob[i] = last ? bon[i] : boc[i]; } }
;             PG8_LDB(B0, 0, 0); PG8_LDB(B1, 0, 1); PG8_SCHED; PG8_LDA(At, 0, 0); PG8_STAGE(PG8_SA(1, 1), a1, aoc[1]);
;             PG8_WAIT_V(8); PG8_WAIT_L(0); PG8_BAR; PG8_MMA(0, 0, At, B0); PG8_MMA(0, 1, At, B1); PG8_BAR; PG8_SCHED;
;             PG8_LDA(At, 0, 1); PG8_STAGE(PG8_SB(0, 0), b2, ob); PG8_STAGE(PG8_SB(0, 1), b2 + hB2, ob); PG8_STAGE(PG8_SA(0, 0), a2, oa0);
;             PG8_WAIT_V(8); PG8_WAIT_L(0); PG8_BAR; PG8_MMA(1, 0, At, B0); PG8_MMA(1, 1, At, B1); PG8_BAR; PG8_SCHED;
.LBB0_244:
	ds_read_b128 v[130:133], v161
	ds_read_b128 v[134:137], v161 offset:1024
	ds_read_b128 v[138:141], v161 offset:2048
	ds_read_b128 v[142:145], v161 offset:3072
	ds_read_b128 v[174:177], v182
	ds_read_b128 v[178:181], v182 offset:1024
	ds_read_b128 v[188:191], v182 offset:2048
	ds_read_b128 v[192:195], v182 offset:3072
	s_add_u32 s8, s6, 0x80
	s_addc_u32 s9, s7, 0
	s_cmp_eq_u32 s64, 28
	s_cselect_b32 s61, s49, s9
	s_cselect_b32 s60, s48, s8
	s_cselect_b32 s9, s59, s63
	s_cselect_b32 s8, s58, s62
	v_lshl_add_u64 v[228:229], s[6:7], 0, v[168:169]
	s_add_i32 m0, s29, 0xc000
	ds_read_b128 v[196:199], v183
	ds_read_b128 v[200:203], v183 offset:1024
	ds_read_b128 v[204:207], v183 offset:2048
	ds_read_b128 v[208:211], v183 offset:3072
	ds_read_b128 v[212:215], v183 offset:4096
	ds_read_b128 v[216:219], v183 offset:5120
	ds_read_b128 v[220:223], v183 offset:6144
	ds_read_b128 v[224:227], v183 offset:7168
	global_load_lds_dwordx4 v[228:229], off
	v_lshl_add_u64 v[228:229], s[6:7], 0, v[166:167]
	s_add_i32 m0, s29, 0xe000
	s_nop 0
	global_load_lds_dwordx4 v[228:229], off
	s_waitcnt vmcnt(8)
	s_waitcnt lgkmcnt(0)
	s_barrier
	s_setprio 0
	s_waitcnt lgkmcnt(0)
	v_mfma_f32_16x16x32_bf16 v[126:129], v[130:133], v[196:199], v[126:129]
	v_mfma_f32_16x16x32_bf16 v[122:125], v[138:141], v[196:199], v[122:125]
	v_mfma_f32_16x16x32_bf16 v[110:113], v[130:133], v[204:207], v[110:113]
	v_mfma_f32_16x16x32_bf16 v[106:109], v[138:141], v[204:207], v[106:109]
	v_mfma_f32_16x16x32_bf16 v[94:97], v[130:133], v[212:215], v[94:97]
	v_mfma_f32_16x16x32_bf16 v[90:93], v[138:141], v[212:215], v[90:93]
	v_mfma_f32_16x16x32_bf16 v[78:81], v[130:133], v[220:223], v[78:81]
	v_mfma_f32_16x16x32_bf16 v[74:77], v[138:141], v[220:223], v[74:77]
	v_mfma_f32_16x16x32_bf16 v[126:129], v[134:137], v[200:203], v[126:129]
	v_mfma_f32_16x16x32_bf16 v[122:125], v[142:145], v[200:203], v[122:125]
	v_mfma_f32_16x16x32_bf16 v[110:113], v[134:137], v[208:211], v[110:113]
	v_mfma_f32_16x16x32_bf16 v[106:109], v[142:145], v[208:211], v[106:109]
	v_mfma_f32_16x16x32_bf16 v[94:97], v[134:137], v[216:219], v[94:97]
	v_mfma_f32_16x16x32_bf16 v[90:93], v[142:145], v[216:219], v[90:93]
	v_mfma_f32_16x16x32_bf16 v[78:81], v[134:137], v[224:227], v[78:81]
	v_mfma_f32_16x16x32_bf16 v[74:77], v[142:145], v[224:227], v[74:77]
	s_nop 0
	s_setprio 0
	v_mfma_f32_16x16x32_bf16 v[118:121], v[174:177], v[196:199], v[118:121]
	v_mfma_f32_16x16x32_bf16 v[114:117], v[188:191], v[196:199], v[114:117]
	v_mfma_f32_16x16x32_bf16 v[102:105], v[174:177], v[204:207], v[102:105]
	v_mfma_f32_16x16x32_bf16 v[98:101], v[188:191], v[204:207], v[98:101]
	v_mfma_f32_16x16x32_bf16 v[86:89], v[174:177], v[212:215], v[86:89]
	v_mfma_f32_16x16x32_bf16 v[82:85], v[188:191], v[212:215], v[82:85]
	v_mfma_f32_16x16x32_bf16 v[70:73], v[174:177], v[220:223], v[70:73]
	v_mfma_f32_16x16x32_bf16 v[66:69], v[188:191], v[220:223], v[66:69]
	v_mfma_f32_16x16x32_bf16 v[118:121], v[178:181], v[200:203], v[118:121]
	v_mfma_f32_16x16x32_bf16 v[114:117], v[192:195], v[200:203], v[114:117]
	v_mfma_f32_16x16x32_bf16 v[102:105], v[178:181], v[208:211], v[102:105]
	v_mfma_f32_16x16x32_bf16 v[98:101], v[192:195], v[208:211], v[98:101]
	v_mfma_f32_16x16x32_bf16 v[86:89], v[178:181], v[216:219], v[86:89]
	v_mfma_f32_16x16x32_bf16 v[82:85], v[192:195], v[216:219], v[82:85]
	v_mfma_f32_16x16x32_bf16 v[70:73], v[178:181], v[224:227], v[70:73]
	v_mfma_f32_16x16x32_bf16 v[66:69], v[192:195], v[224:227], v[66:69]
	s_setprio 1
	s_barrier
	s_mov_b32 m0, s25
	v_lshl_add_u64 v[228:229], s[8:9], 0, v[146:147]
	s_add_u32 s80, s8, 0x80000
	ds_read_b128 v[196:199], v183 offset:16384
	ds_read_b128 v[200:203], v183 offset:17408
	ds_read_b128 v[204:207], v183 offset:18432
	ds_read_b128 v[208:211], v183 offset:19456
	ds_read_b128 v[212:215], v183 offset:20480
	ds_read_b128 v[216:219], v183 offset:21504
	ds_read_b128 v[220:223], v183 offset:22528
	ds_read_b128 v[224:227], v183 offset:23552
	global_load_lds_dwordx4 v[228:229], off
	v_lshl_add_u64 v[230:231], s[8:9], 0, v[152:153]
	s_mov_b32 m0, s26
	s_addc_u32 s81, s9, 0
	global_load_lds_dwordx4 v[230:231], off
	v_lshl_add_u64 v[232:233], s[80:81], 0, v[146:147]
	s_mov_b32 m0, s27
	v_lshl_add_u64 v[234:235], s[60:61], 0, v[154:155]
	global_load_lds_dwordx4 v[232:233], off
	v_lshl_add_u64 v[232:233], s[80:81], 0, v[152:153]
	s_mov_b32 m0, s28
	s_nop 0
	global_load_lds_dwordx4 v[232:233], off
	v_lshl_add_u64 v[232:233], s[60:61], 0, v[148:149]
	s_mov_b32 m0, s29
	s_nop 0
	global_load_lds_dwordx4 v[232:233], off
	s_mov_b32 m0, s50
	s_nop 0
	global_load_lds_dwordx4 v[234:235], off
	s_waitcnt vmcnt(8)
	s_waitcnt lgkmcnt(0)
	s_barrier
; #define PG8_STAGE(bufoff, gbase, voff) do { _Pragma("unroll") for (int _i = 0; _i < 2; ++_i) \
;         __builtin_amdgcn_global_load_lds((const GAS unsigned*)((const GAS char*)(gbase) + (voff)[_i]), (LAS unsigned*)(lds + (bufoff) + ldsw + _i * 8192), 16, 0, 0); } while (0)
; #define PG8_LDA(dst, b, h) do { _Pragma("unroll") for (int m = 0; m < 4; ++m) { dst[m].lo = *(const LAS i32x4v*)(lds + PG8_SA(b, h) + (FP8 ? aoff8[0] : aoff) + m * 2048); dst[m].hi = *(const LAS i32x4v*)(lds + PG8_SA(b, h) + (FP8 ? aoff8[1] : aoff + 1024) + m * 2048); } } while (0)
; #define PG8_LDB(dst, b, h) do { _Pragma("unroll") for (int n = 0; n < 2; ++n) { dst[n].lo = *(const LAS i32x4v*)(lds + PG8_SB(b, h) + (FP8 ? boff8[0] : boff) + n * 2048); dst[n].hi = *(const LAS i32x4v*)(lds + PG8_SB(b, h) + (FP8 ? boff8[1] : boff + 1024) + n * 2048); } } while (0)
; #define PG8_WAIT_V(n) asm volatile("s_waitcnt vmcnt(" #n ")" ::: "memory")
; #define PG8_WAIT_L(n) asm volatile("s_waitcnt lgkmcnt(" #n ")" ::: "memory")
; #define PG8_BAR __builtin_amdgcn_s_barrier()
; #define PG8_SCHED __builtin_amdgcn_sched_barrier(0)
; template <class Epi, class Sched, bool GATHER, bool FP8 = false, bool UNI = false>
; __device__ __forceinline__ void gemm_phase(LAS unsigned char* lds, const Sched& S, const Epi& E) {
;     ...
;             PG8_WAIT_V(8); PG8_WAIT_L(0); PG8_BAR; PG8_MMA(1, 0, At, B0); PG8_MMA(1, 1, At, B1); PG8_BAR; PG8_SCHED;
;             PG8_LDB(B0, 1, 0); PG8_LDB(B1, 1, 1); PG8_SCHED; PG8_LDA(At, 1, 0); PG8_STAGE(PG8_SA(0, 1), a2, oa1);
;             PG8_WAIT_V(8); PG8_WAIT_L(0); PG8_BAR; PG8_MMA(0, 0, At, B0); PG8_MMA(0, 1, At, B1); PG8_BAR; PG8_SCHED;
	s_setprio 0
	s_waitcnt lgkmcnt(0)
	v_mfma_f32_16x16x32_bf16 v[54:57], v[130:133], v[196:199], v[54:57]
	v_mfma_f32_16x16x32_bf16 v[50:53], v[138:141], v[196:199], v[50:53]
	v_mfma_f32_16x16x32_bf16 v[38:41], v[130:133], v[204:207], v[38:41]
	v_mfma_f32_16x16x32_bf16 v[34:37], v[138:141], v[204:207], v[34:37]
	v_mfma_f32_16x16x32_bf16 v[18:21], v[130:133], v[212:215], v[18:21]
	v_mfma_f32_16x16x32_bf16 v[22:25], v[138:141], v[212:215], v[22:25]
	v_mfma_f32_16x16x32_bf16 v[2:5], v[130:133], v[220:223], v[2:5]
	v_mfma_f32_16x16x32_bf16 v[6:9], v[138:141], v[220:223], v[6:9]
	v_mfma_f32_16x16x32_bf16 v[54:57], v[134:137], v[200:203], v[54:57]
	v_mfma_f32_16x16x32_bf16 v[50:53], v[142:145], v[200:203], v[50:53]
	v_mfma_f32_16x16x32_bf16 v[38:41], v[134:137], v[208:211], v[38:41]
	v_mfma_f32_16x16x32_bf16 v[34:37], v[142:145], v[208:211], v[34:37]
	v_mfma_f32_16x16x32_bf16 v[18:21], v[134:137], v[216:219], v[18:21]
	v_mfma_f32_16x16x32_bf16 v[22:25], v[142:145], v[216:219], v[22:25]
	v_mfma_f32_16x16x32_bf16 v[2:5], v[134:137], v[224:227], v[2:5]
	v_mfma_f32_16x16x32_bf16 v[6:9], v[142:145], v[224:227], v[6:9]
	s_nop 0
	s_setprio 0
	v_mfma_f32_16x16x32_bf16 v[58:61], v[174:177], v[196:199], v[58:61]
	v_mfma_f32_16x16x32_bf16 v[62:65], v[188:191], v[196:199], v[62:65]
	v_mfma_f32_16x16x32_bf16 v[42:45], v[174:177], v[204:207], v[42:45]
	v_mfma_f32_16x16x32_bf16 v[46:49], v[188:191], v[204:207], v[46:49]
	v_mfma_f32_16x16x32_bf16 v[26:29], v[174:177], v[212:215], v[26:29]
	v_mfma_f32_16x16x32_bf16 v[30:33], v[188:191], v[212:215], v[30:33]
	v_mfma_f32_16x16x32_bf16 v[10:13], v[174:177], v[220:223], v[10:13]
	v_mfma_f32_16x16x32_bf16 v[14:17], v[188:191], v[220:223], v[14:17]
	v_mfma_f32_16x16x32_bf16 v[58:61], v[178:181], v[200:203], v[58:61]
	v_mfma_f32_16x16x32_bf16 v[62:65], v[192:195], v[200:203], v[62:65]
	v_mfma_f32_16x16x32_bf16 v[42:45], v[178:181], v[208:211], v[42:45]
	v_mfma_f32_16x16x32_bf16 v[46:49], v[192:195], v[208:211], v[46:49]
	v_mfma_f32_16x16x32_bf16 v[26:29], v[178:181], v[216:219], v[26:29]
	v_mfma_f32_16x16x32_bf16 v[30:33], v[192:195], v[216:219], v[30:33]
	v_mfma_f32_16x16x32_bf16 v[10:13], v[178:181], v[224:227], v[10:13]
	v_mfma_f32_16x16x32_bf16 v[14:17], v[192:195], v[224:227], v[14:17]
	s_setprio 1
	s_barrier
	ds_read_b128 v[130:133], v184
	ds_read_b128 v[134:137], v184 offset:1024
	ds_read_b128 v[138:141], v184 offset:2048
	ds_read_b128 v[142:145], v184 offset:3072
	ds_read_b128 v[174:177], v185
	ds_read_b128 v[178:181], v185 offset:1024
	ds_read_b128 v[188:191], v185 offset:2048
	ds_read_b128 v[192:195], v185 offset:3072
	s_mov_b32 m0, s51
	v_lshl_add_u64 v[236:237], s[60:61], 0, v[150:151]
	ds_read_b128 v[196:199], v183 offset:32768
	ds_read_b128 v[200:203], v183 offset:33792
	ds_read_b128 v[204:207], v183 offset:34816
	ds_read_b128 v[208:211], v183 offset:35840
	ds_read_b128 v[212:215], v183 offset:36864
	ds_read_b128 v[216:219], v183 offset:37888
	ds_read_b128 v[220:223], v183 offset:38912
	ds_read_b128 v[224:227], v183 offset:39936
	global_load_lds_dwordx4 v[236:237], off
	v_lshl_add_u64 v[236:237], s[60:61], 0, v[156:157]
	s_mov_b32 m0, s56
	s_nop 0
	global_load_lds_dwordx4 v[236:237], off
	s_waitcnt vmcnt(8)
	s_waitcnt lgkmcnt(0)
	s_barrier
	s_setprio 0
	s_waitcnt lgkmcnt(0)
	v_mfma_f32_16x16x32_bf16 v[126:129], v[130:133], v[196:199], v[126:129]
	v_mfma_f32_16x16x32_bf16 v[122:125], v[138:141], v[196:199], v[122:125]
	v_mfma_f32_16x16x32_bf16 v[110:113], v[130:133], v[204:207], v[110:113]
	v_mfma_f32_16x16x32_bf16 v[106:109], v[138:141], v[204:207], v[106:109]
	v_mfma_f32_16x16x32_bf16 v[94:97], v[130:133], v[212:215], v[94:97]
	v_mfma_f32_16x16x32_bf16 v[90:93], v[138:141], v[212:215], v[90:93]
	v_mfma_f32_16x16x32_bf16 v[78:81], v[130:133], v[220:223], v[78:81]
	v_mfma_f32_16x16x32_bf16 v[74:77], v[138:141], v[220:223], v[74:77]
	v_mfma_f32_16x16x32_bf16 v[126:129], v[134:137], v[200:203], v[126:129]
	v_mfma_f32_16x16x32_bf16 v[122:125], v[142:145], v[200:203], v[122:125]
	v_mfma_f32_16x16x32_bf16 v[110:113], v[134:137], v[208:211], v[110:113]
	v_mfma_f32_16x16x32_bf16 v[106:109], v[142:145], v[208:211], v[106:109]
	v_mfma_f32_16x16x32_bf16 v[94:97], v[134:137], v[216:219], v[94:97]
	v_mfma_f32_16x16x32_bf16 v[90:93], v[142:145], v[216:219], v[90:93]
	v_mfma_f32_16x16x32_bf16 v[78:81], v[134:137], v[224:227], v[78:81]
	v_mfma_f32_16x16x32_bf16 v[74:77], v[142:145], v[224:227], v[74:77]
	s_nop 0
	s_setprio 0
	v_mfma_f32_16x16x32_bf16 v[118:121], v[174:177], v[196:199], v[118:121]
	v_mfma_f32_16x16x32_bf16 v[114:117], v[188:191], v[196:199], v[114:117]
	v_mfma_f32_16x16x32_bf16 v[102:105], v[174:177], v[204:207], v[102:105]
	v_mfma_f32_16x16x32_bf16 v[98:101], v[188:191], v[204:207], v[98:101]
	v_mfma_f32_16x16x32_bf16 v[86:89], v[174:177], v[212:215], v[86:89]
	v_mfma_f32_16x16x32_bf16 v[82:85], v[188:191], v[212:215], v[82:85]
	v_mfma_f32_16x16x32_bf16 v[70:73], v[174:177], v[220:223], v[70:73]
	v_mfma_f32_16x16x32_bf16 v[66:69], v[188:191], v[220:223], v[66:69]
	v_mfma_f32_16x16x32_bf16 v[118:121], v[178:181], v[200:203], v[118:121]
	v_mfma_f32_16x16x32_bf16 v[114:117], v[192:195], v[200:203], v[114:117]
	v_mfma_f32_16x16x32_bf16 v[102:105], v[178:181], v[208:211], v[102:105]
	v_mfma_f32_16x16x32_bf16 v[98:101], v[192:195], v[208:211], v[98:101]
	v_mfma_f32_16x16x32_bf16 v[86:89], v[178:181], v[216:219], v[86:89]
	v_mfma_f32_16x16x32_bf16 v[82:85], v[192:195], v[216:219], v[82:85]
	v_mfma_f32_16x16x32_bf16 v[70:73], v[178:181], v[224:227], v[70:73]
	v_mfma_f32_16x16x32_bf16 v[66:69], v[192:195], v[224:227], v[66:69]
	s_setprio 1
	s_barrier
; #define PG8_STAGE(bufoff, gbase, voff) do { _Pragma("unroll") for (int _i = 0; _i < 2; ++_i) \
;         __builtin_amdgcn_global_load_lds((const GAS unsigned*)((const GAS char*)(gbase) + (voff)[_i]), (LAS unsigned*)(lds + (bufoff) + ldsw + _i * 8192), 16, 0, 0); } while (0)
; #define PG8_LDA(dst, b, h) do { _Pragma("unroll") for (int m = 0; m < 4; ++m) { dst[m].lo = *(const LAS i32x4v*)(lds + PG8_SA(b, h) + (FP8 ? aoff8[0] : aoff) + m * 2048); dst[m].hi = *(const LAS i32x4v*)(lds + PG8_SA(b, h) + (FP8 ? aoff8[1] : aoff + 1024) + m * 2048); } } while (0)
; #define PG8_WAIT_V(n) asm volatile("s_waitcnt vmcnt(" #n ")" ::: "memory")
; #define PG8_WAIT_L(n) asm volatile("s_waitcnt lgkmcnt(" #n ")" ::: "memory")
; #define PG8_BAR __builtin_amdgcn_s_barrier()
; #define PG8_SCHED __builtin_amdgcn_sched_barrier(0)
; template <class Epi, class Sched, bool GATHER, bool FP8 = false, bool UNI = false>
; __device__ __forceinline__ void gemm_phase(LAS unsigned char* lds, const Sched& S, const Epi& E) {
;     ...
;             PG8_LDA(At, 1, 1); PG8_STAGE(PG8_SB(1, 0), b3, ob); PG8_STAGE(PG8_SB(1, 1), b3 + hB2, ob); PG8_STAGE(PG8_SA(1, 0), a3, oa0);
;             PG8_WAIT_V(8); PG8_WAIT_L(0); PG8_BAR; PG8_MMA(1, 0, At, B0); PG8_MMA(1, 1, At, B1); PG8_BAR; PG8_SCHED;
;         }
;         if (wr == 0) PG8_BAR;
	s_mov_b32 m0, s57
	v_lshl_add_u64 v[228:229], v[228:229], 0, s[16:17]
	s_add_u32 s8, s8, 0x80080
	ds_read_b128 v[196:199], v183 offset:49152
	ds_read_b128 v[200:203], v183 offset:50176
	ds_read_b128 v[204:207], v183 offset:51200
	ds_read_b128 v[208:211], v183 offset:52224
	ds_read_b128 v[212:215], v183 offset:53248
	ds_read_b128 v[216:219], v183 offset:54272
	ds_read_b128 v[220:223], v183 offset:55296
	ds_read_b128 v[224:227], v183 offset:56320
	global_load_lds_dwordx4 v[228:229], off
	v_lshl_add_u64 v[228:229], v[230:231], 0, s[16:17]
	s_mov_b32 m0, s66
	s_addc_u32 s9, s9, 0
	global_load_lds_dwordx4 v[228:229], off
	v_lshl_add_u64 v[228:229], s[8:9], 0, v[146:147]
	s_mov_b32 m0, s69
	s_nop 0
	global_load_lds_dwordx4 v[228:229], off
	v_lshl_add_u64 v[228:229], s[8:9], 0, v[152:153]
	s_mov_b32 m0, s70
	s_nop 0
	global_load_lds_dwordx4 v[228:229], off
	v_lshl_add_u64 v[228:229], v[232:233], 0, s[16:17]
	s_mov_b32 m0, s67
	s_nop 0
	global_load_lds_dwordx4 v[228:229], off
	v_lshl_add_u64 v[228:229], v[234:235], 0, s[16:17]
	s_mov_b32 m0, s68
	s_nop 0
	global_load_lds_dwordx4 v[228:229], off
	s_waitcnt vmcnt(8)
	s_waitcnt lgkmcnt(0)
	s_barrier
	s_setprio 0
	s_waitcnt lgkmcnt(0)
	v_mfma_f32_16x16x32_bf16 v[54:57], v[130:133], v[196:199], v[54:57]
	v_mfma_f32_16x16x32_bf16 v[50:53], v[138:141], v[196:199], v[50:53]
	v_mfma_f32_16x16x32_bf16 v[38:41], v[130:133], v[204:207], v[38:41]
	v_mfma_f32_16x16x32_bf16 v[34:37], v[138:141], v[204:207], v[34:37]
	v_mfma_f32_16x16x32_bf16 v[18:21], v[130:133], v[212:215], v[18:21]
	v_mfma_f32_16x16x32_bf16 v[22:25], v[138:141], v[212:215], v[22:25]
	v_mfma_f32_16x16x32_bf16 v[2:5], v[130:133], v[220:223], v[2:5]
	v_mfma_f32_16x16x32_bf16 v[6:9], v[138:141], v[220:223], v[6:9]
	v_mfma_f32_16x16x32_bf16 v[54:57], v[134:137], v[200:203], v[54:57]
	v_mfma_f32_16x16x32_bf16 v[50:53], v[142:145], v[200:203], v[50:53]
	v_mfma_f32_16x16x32_bf16 v[38:41], v[134:137], v[208:211], v[38:41]
	v_mfma_f32_16x16x32_bf16 v[34:37], v[142:145], v[208:211], v[34:37]
	v_mfma_f32_16x16x32_bf16 v[18:21], v[134:137], v[216:219], v[18:21]
	v_mfma_f32_16x16x32_bf16 v[22:25], v[142:145], v[216:219], v[22:25]
	v_mfma_f32_16x16x32_bf16 v[2:5], v[134:137], v[224:227], v[2:5]
	v_mfma_f32_16x16x32_bf16 v[6:9], v[142:145], v[224:227], v[6:9]
	s_nop 0
	s_setprio 0
	v_mfma_f32_16x16x32_bf16 v[58:61], v[174:177], v[196:199], v[58:61]
	v_mfma_f32_16x16x32_bf16 v[62:65], v[188:191], v[196:199], v[62:65]
	v_mfma_f32_16x16x32_bf16 v[42:45], v[174:177], v[204:207], v[42:45]
	v_mfma_f32_16x16x32_bf16 v[46:49], v[188:191], v[204:207], v[46:49]
	v_mfma_f32_16x16x32_bf16 v[26:29], v[174:177], v[212:215], v[26:29]
	v_mfma_f32_16x16x32_bf16 v[30:33], v[188:191], v[212:215], v[30:33]
	v_mfma_f32_16x16x32_bf16 v[10:13], v[174:177], v[220:223], v[10:13]
	v_mfma_f32_16x16x32_bf16 v[14:17], v[188:191], v[220:223], v[14:17]
	v_mfma_f32_16x16x32_bf16 v[58:61], v[178:181], v[200:203], v[58:61]
	v_mfma_f32_16x16x32_bf16 v[62:65], v[192:195], v[200:203], v[62:65]
	v_mfma_f32_16x16x32_bf16 v[42:45], v[178:181], v[208:211], v[42:45]
	v_mfma_f32_16x16x32_bf16 v[46:49], v[192:195], v[208:211], v[46:49]
	v_mfma_f32_16x16x32_bf16 v[26:29], v[178:181], v[216:219], v[26:29]
	v_mfma_f32_16x16x32_bf16 v[30:33], v[192:195], v[216:219], v[30:33]
	v_mfma_f32_16x16x32_bf16 v[10:13], v[178:181], v[224:227], v[10:13]
	v_mfma_f32_16x16x32_bf16 v[14:17], v[192:195], v[224:227], v[14:17]
	s_setprio 1
	s_barrier
	s_add_i32 s64, s64, 2
	s_add_u32 s62, s62, 0x100
	s_addc_u32 s63, s63, 0
	s_add_u32 s6, s6, 0x100
	s_addc_u32 s7, s7, 0
	s_cmp_gt_u32 s64, 29
	s_cbranch_scc0 .LBB0_244
	s_setprio 0
	s_and_b64 vcc, exec, s[18:19]
	s_cbranch_vccz .LBB0_247
	s_barrier

; #define PG8_STAGE(bufoff, gbase, voff) do { _Pragma("unroll") for (int _i = 0; _i < 2; ++_i) \
;         __builtin_amdgcn_global_load_lds((const GAS unsigned*)((const GAS char*)(gbase) + (voff)[_i]), (LAS unsigned*)(lds + (bufoff) + ldsw + _i * 8192), 16, 0, 0); } while (0)
; #define PG8_LDA(dst, b, h) do { _Pragma("unroll") for (int m = 0; m < 4; ++m) { dst[m].lo = *(const LAS i32x4v*)(lds + PG8_SA(b, h) + (FP8 ? aoff8[0] : aoff) + m * 2048); dst[m].hi = *(const LAS i32x4v*)(lds + PG8_SA(b, h) + (FP8 ? aoff8[1] : aoff + 1024) + m * 2048); } } while (0)
; #define PG8_LDB(dst, b, h) do { _Pragma("unroll") for (int n = 0; n < 2; ++n) { dst[n].lo = *(const LAS i32x4v*)(lds + PG8_SB(b, h) + (FP8 ? boff8[0] : boff) + n * 2048); dst[n].hi = *(const LAS i32x4v*)(lds + PG8_SB(b, h) + (FP8 ? boff8[1] : boff + 1024) + n * 2048); } } while (0)
; #define PG8_WAIT_V(n) asm volatile("s_waitcnt vmcnt(" #n ")" ::: "memory")
; #define PG8_WAIT_L(n) asm volatile("s_waitcnt lgkmcnt(" #n ")" ::: "memory")
; #define PG8_BAR __builtin_amdgcn_s_barrier()
; #define PG8_SCHED __builtin_amdgcn_sched_barrier(0)
; template <class Epi, class Sched, bool GATHER, bool FP8 = false, bool UNI = false>
; __device__ __forceinline__ void gemm_phase(LAS unsigned char* lds, const Sched& S, const Epi& E) {
;     ...
;             PG8_LDB(B0, 0, 0); PG8_LDB(B1, 0, 1); PG8_SCHED; PG8_LDA(At, 0, 0); PG8_STAGE(PG8_SA(1, 1), a1, aoc[1]);
;             PG8_WAIT_V(8); PG8_WAIT_L(0); PG8_BAR; PG8_MMA(0, 0, At, B0); PG8_MMA(0, 1, At, B1); PG8_BAR; PG8_SCHED;
;             PG8_LDA(At, 0, 1); PG8_STAGE(PG8_SB(0, 0), b2, ob); PG8_STAGE(PG8_SB(0, 1), b2 + hB2, ob); PG8_STAGE(PG8_SA(0, 0), a2, oa0);
;             PG8_WAIT_V(8); PG8_WAIT_L(0); PG8_BAR; PG8_MMA(1, 0, At, B0); PG8_MMA(1, 1, At, B1); PG8_BAR; PG8_SCHED;
;             PG8_LDB(B0, 1, 0); PG8_LDB(B1, 1, 1); PG8_SCHED; PG8_LDA(At, 1, 0); PG8_STAGE(PG8_SA(0, 1), a2, oa1);
;             PG8_WAIT_V(8); PG8_WAIT_L(0); PG8_BAR; PG8_MMA(0, 0, At, B0); PG8_MMA(0, 1, At, B1); PG8_BAR; PG8_SCHED;
.LBB0_321:
	v_add_u32_e32 v2, s70, v199
	v_add_u32_e32 v3, s70, v200
	v_add_u32_e32 v6, s71, v199
	v_add_u32_e32 v14, s71, v200
	ds_read_b128 v[18:21], v2
	ds_read_b128 v[26:29], v2 offset:2048
	ds_read_b128 v[22:25], v3
	ds_read_b128 v[30:33], v3 offset:2048
	ds_read_b128 v[2:5], v6
	ds_read_b128 v[10:13], v6 offset:2048
	ds_read_b128 v[6:9], v14
	ds_read_b128 v[14:17], v14 offset:2048
	s_add_u32 s8, s6, 0x80
	s_addc_u32 s9, s7, 0
	s_cmp_eq_u32 s78, 12
	s_cselect_b32 s23, s17, s9
	s_cselect_b32 s22, s16, s8
	s_cselect_b32 s9, s19, s77
	s_cselect_b32 s8, s18, s76
	v_lshl_add_u64 v[228:229], s[6:7], 0, v[186:187]
	s_add_i32 m0, s86, 0xc000
	ds_read_b128 v[188:191], v201
	ds_read_b128 v[204:207], v201 offset:2048
	ds_read_b128 v[192:195], v202
	ds_read_b128 v[208:211], v202 offset:2048
	ds_read_b128 v[212:215], v201 offset:4096
	ds_read_b128 v[220:223], v201 offset:6144
	ds_read_b128 v[216:219], v202 offset:4096
	ds_read_b128 v[224:227], v202 offset:6144
	global_load_lds_dwordx4 v[228:229], off
	v_lshl_add_u64 v[228:229], s[6:7], 0, v[184:185]
	s_add_i32 m0, s86, 0xe000
	s_nop 0
	global_load_lds_dwordx4 v[228:229], off
	s_waitcnt vmcnt(8)
	s_waitcnt lgkmcnt(0)
	s_barrier
	s_setprio 0
	s_waitcnt lgkmcnt(0)
	v_mfma_scale_f32_16x16x128_f8f6f4 v[158:161], v[18:25], v[188:195], v[158:161], v1, v179 op_sel_hi:[0,0,0]
	v_mfma_scale_f32_16x16x128_f8f6f4 v[154:157], v[26:33], v[188:195], v[154:157], v1, v179 op_sel_hi:[0,0,0]
	v_mfma_scale_f32_16x16x128_f8f6f4 v[142:145], v[18:25], v[204:211], v[142:145], v1, v179 op_sel_hi:[0,0,0]
	v_mfma_scale_f32_16x16x128_f8f6f4 v[138:141], v[26:33], v[204:211], v[138:141], v1, v179 op_sel_hi:[0,0,0]
	v_mfma_scale_f32_16x16x128_f8f6f4 v[126:129], v[18:25], v[212:219], v[126:129], v1, v179 op_sel_hi:[0,0,0]
	v_mfma_scale_f32_16x16x128_f8f6f4 v[122:125], v[26:33], v[212:219], v[122:125], v1, v179 op_sel_hi:[0,0,0]
	v_mfma_scale_f32_16x16x128_f8f6f4 v[110:113], v[18:25], v[220:227], v[110:113], v1, v179 op_sel_hi:[0,0,0]
	v_mfma_scale_f32_16x16x128_f8f6f4 v[106:109], v[26:33], v[220:227], v[106:109], v1, v179 op_sel_hi:[0,0,0]
	s_nop 0
	s_setprio 0
	v_mfma_scale_f32_16x16x128_f8f6f4 v[150:153], v[2:9], v[188:195], v[150:153], v1, v179 op_sel_hi:[0,0,0]
	v_mfma_scale_f32_16x16x128_f8f6f4 v[146:149], v[10:17], v[188:195], v[146:149], v1, v179 op_sel_hi:[0,0,0]
	v_mfma_scale_f32_16x16x128_f8f6f4 v[134:137], v[2:9], v[204:211], v[134:137], v1, v179 op_sel_hi:[0,0,0]
	v_mfma_scale_f32_16x16x128_f8f6f4 v[130:133], v[10:17], v[204:211], v[130:133], v1, v179 op_sel_hi:[0,0,0]
	v_mfma_scale_f32_16x16x128_f8f6f4 v[118:121], v[2:9], v[212:219], v[118:121], v1, v179 op_sel_hi:[0,0,0]
	v_mfma_scale_f32_16x16x128_f8f6f4 v[114:117], v[10:17], v[212:219], v[114:117], v1, v179 op_sel_hi:[0,0,0]
	v_mfma_scale_f32_16x16x128_f8f6f4 v[102:105], v[2:9], v[220:227], v[102:105], v1, v179 op_sel_hi:[0,0,0]
	v_mfma_scale_f32_16x16x128_f8f6f4 v[98:101], v[10:17], v[220:227], v[98:101], v1, v179 op_sel_hi:[0,0,0]
	s_setprio 1
	s_barrier
	s_mov_b32 m0, s82
	v_lshl_add_u64 v[188:189], s[8:9], 0, v[166:167]
	s_add_u32 vcc_lo, s8, 0x40000
	ds_read_b128 v[204:207], v201 offset:16384
	ds_read_b128 v[212:215], v201 offset:18432
	ds_read_b128 v[208:211], v202 offset:16384
	ds_read_b128 v[216:219], v202 offset:18432
	ds_read_b128 v[220:223], v201 offset:20480
	ds_read_b128 v[228:231], v201 offset:22528
	ds_read_b128 v[224:227], v202 offset:20480
	ds_read_b128 v[232:235], v202 offset:22528
	global_load_lds_dwordx4 v[188:189], off
	v_lshl_add_u64 v[190:191], s[8:9], 0, v[172:173]
	s_mov_b32 m0, s83
	s_addc_u32 vcc_hi, s9, 0
	global_load_lds_dwordx4 v[190:191], off
	v_lshl_add_u64 v[192:193], vcc, 0, v[166:167]
	s_mov_b32 m0, s84
	v_lshl_add_u64 v[194:195], s[22:23], 0, v[174:175]
	global_load_lds_dwordx4 v[192:193], off
	v_lshl_add_u64 v[192:193], vcc, 0, v[172:173]
	s_mov_b32 m0, s85
	s_nop 0
	global_load_lds_dwordx4 v[192:193], off
	v_lshl_add_u64 v[192:193], s[22:23], 0, v[168:169]
	s_mov_b32 m0, s86
	s_nop 0
	global_load_lds_dwordx4 v[192:193], off
	s_mov_b32 m0, s87
	s_nop 0
	global_load_lds_dwordx4 v[194:195], off
	s_waitcnt vmcnt(8)
	s_waitcnt lgkmcnt(0)
	s_barrier
	s_setprio 0
	s_waitcnt lgkmcnt(0)
	v_mfma_scale_f32_16x16x128_f8f6f4 v[86:89], v[18:25], v[204:211], v[86:89], v1, v179 op_sel_hi:[0,0,0]
	v_mfma_scale_f32_16x16x128_f8f6f4 v[82:85], v[26:33], v[204:211], v[82:85], v1, v179 op_sel_hi:[0,0,0]
	v_mfma_scale_f32_16x16x128_f8f6f4 v[70:73], v[18:25], v[212:219], v[70:73], v1, v179 op_sel_hi:[0,0,0]
	v_mfma_scale_f32_16x16x128_f8f6f4 v[66:69], v[26:33], v[212:219], v[66:69], v1, v179 op_sel_hi:[0,0,0]
	v_mfma_scale_f32_16x16x128_f8f6f4 v[58:61], v[18:25], v[220:227], v[58:61], v1, v179 op_sel_hi:[0,0,0]
	v_mfma_scale_f32_16x16x128_f8f6f4 v[50:53], v[26:33], v[220:227], v[50:53], v1, v179 op_sel_hi:[0,0,0]
	v_mfma_scale_f32_16x16x128_f8f6f4 v[42:45], v[18:25], v[228:235], v[42:45], v1, v179 op_sel_hi:[0,0,0]
	v_mfma_scale_f32_16x16x128_f8f6f4 v[34:37], v[26:33], v[228:235], v[34:37], v1, v179 op_sel_hi:[0,0,0]
	s_nop 0
	s_setprio 0
	v_mfma_scale_f32_16x16x128_f8f6f4 v[94:97], v[2:9], v[204:211], v[94:97], v1, v179 op_sel_hi:[0,0,0]
	v_mfma_scale_f32_16x16x128_f8f6f4 v[90:93], v[10:17], v[204:211], v[90:93], v1, v179 op_sel_hi:[0,0,0]
	v_mfma_scale_f32_16x16x128_f8f6f4 v[78:81], v[2:9], v[212:219], v[78:81], v1, v179 op_sel_hi:[0,0,0]
	v_mfma_scale_f32_16x16x128_f8f6f4 v[74:77], v[10:17], v[212:219], v[74:77], v1, v179 op_sel_hi:[0,0,0]
	v_mfma_scale_f32_16x16x128_f8f6f4 v[62:65], v[2:9], v[220:227], v[62:65], v1, v179 op_sel_hi:[0,0,0]
	v_mfma_scale_f32_16x16x128_f8f6f4 v[54:57], v[10:17], v[220:227], v[54:57], v1, v179 op_sel_hi:[0,0,0]
	v_mfma_scale_f32_16x16x128_f8f6f4 v[46:49], v[2:9], v[228:235], v[46:49], v1, v179 op_sel_hi:[0,0,0]
	v_mfma_scale_f32_16x16x128_f8f6f4 v[38:41], v[10:17], v[228:235], v[38:41], v1, v179 op_sel_hi:[0,0,0]
	s_setprio 1
	s_barrier
; #define PG8_STAGE(bufoff, gbase, voff) do { _Pragma("unroll") for (int _i = 0; _i < 2; ++_i) \
;         __builtin_amdgcn_global_load_lds((const GAS unsigned*)((const GAS char*)(gbase) + (voff)[_i]), (LAS unsigned*)(lds + (bufoff) + ldsw + _i * 8192), 16, 0, 0); } while (0)
; #define PG8_LDA(dst, b, h) do { _Pragma("unroll") for (int m = 0; m < 4; ++m) { dst[m].lo = *(const LAS i32x4v*)(lds + PG8_SA(b, h) + (FP8 ? aoff8[0] : aoff) + m * 2048); dst[m].hi = *(const LAS i32x4v*)(lds + PG8_SA(b, h) + (FP8 ? aoff8[1] : aoff + 1024) + m * 2048); } } while (0)
; #define PG8_LDB(dst, b, h) do { _Pragma("unroll") for (int n = 0; n < 2; ++n) { dst[n].lo = *(const LAS i32x4v*)(lds + PG8_SB(b, h) + (FP8 ? boff8[0] : boff) + n * 2048); dst[n].hi = *(const LAS i32x4v*)(lds + PG8_SB(b, h) + (FP8 ? boff8[1] : boff + 1024) + n * 2048); } } while (0)
; #define PG8_WAIT_V(n) asm volatile("s_waitcnt vmcnt(" #n ")" ::: "memory")
; #define PG8_WAIT_L(n) asm volatile("s_waitcnt lgkmcnt(" #n ")" ::: "memory")
; #define PG8_BAR __builtin_amdgcn_s_barrier()
; #define PG8_SCHED __builtin_amdgcn_sched_barrier(0)
; template <class Epi, class Sched, bool GATHER, bool FP8 = false, bool UNI = false>
; __device__ __forceinline__ void gemm_phase(LAS unsigned char* lds, const Sched& S, const Epi& E) {
;     ...
;             PG8_LDB(B0, 1, 0); PG8_LDB(B1, 1, 1); PG8_SCHED; PG8_LDA(At, 1, 0); PG8_STAGE(PG8_SA(0, 1), a2, oa1);
;             PG8_WAIT_V(8); PG8_WAIT_L(0); PG8_BAR; PG8_MMA(0, 0, At, B0); PG8_MMA(0, 1, At, B1); PG8_BAR; PG8_SCHED;
;             PG8_LDA(At, 1, 1); PG8_STAGE(PG8_SB(1, 0), b3, ob); PG8_STAGE(PG8_SB(1, 1), b3 + hB2, ob); PG8_STAGE(PG8_SA(1, 0), a3, oa0);
;             PG8_WAIT_V(8); PG8_WAIT_L(0); PG8_BAR; PG8_MMA(1, 0, At, B0); PG8_MMA(1, 1, At, B1); PG8_BAR; PG8_SCHED;
;         }
;         if (wr == 0) PG8_BAR;
	v_add_u32_e32 v6, s56, v199
	v_add_u32_e32 v14, s56, v200
	v_add_u32_e32 v22, s57, v199
	v_add_u32_e32 v30, s57, v200
	ds_read_b128 v[2:5], v6
	ds_read_b128 v[10:13], v6 offset:2048
	ds_read_b128 v[6:9], v14
	ds_read_b128 v[14:17], v14 offset:2048
	ds_read_b128 v[18:21], v22
	ds_read_b128 v[26:29], v22 offset:2048
	ds_read_b128 v[22:25], v30
	ds_read_b128 v[30:33], v30 offset:2048
	s_mov_b32 m0, s88
	v_lshl_add_u64 v[236:237], s[22:23], 0, v[170:171]
	ds_read_b128 v[204:207], v201 offset:32768
	ds_read_b128 v[212:215], v201 offset:34816
	ds_read_b128 v[208:211], v202 offset:32768
	ds_read_b128 v[216:219], v202 offset:34816
	ds_read_b128 v[220:223], v201 offset:36864
	ds_read_b128 v[228:231], v201 offset:38912
	ds_read_b128 v[224:227], v202 offset:36864
	ds_read_b128 v[232:235], v202 offset:38912
	global_load_lds_dwordx4 v[236:237], off
	v_lshl_add_u64 v[236:237], s[22:23], 0, v[176:177]
	s_mov_b32 m0, s50
	s_nop 0
	global_load_lds_dwordx4 v[236:237], off
	s_waitcnt vmcnt(8)
	s_waitcnt lgkmcnt(0)
	s_barrier
	s_setprio 0
	s_waitcnt lgkmcnt(0)
	v_mfma_scale_f32_16x16x128_f8f6f4 v[158:161], v[2:9], v[204:211], v[158:161], v1, v179 op_sel_hi:[0,0,0]
	v_mfma_scale_f32_16x16x128_f8f6f4 v[154:157], v[10:17], v[204:211], v[154:157], v1, v179 op_sel_hi:[0,0,0]
	v_mfma_scale_f32_16x16x128_f8f6f4 v[142:145], v[2:9], v[212:219], v[142:145], v1, v179 op_sel_hi:[0,0,0]
	v_mfma_scale_f32_16x16x128_f8f6f4 v[138:141], v[10:17], v[212:219], v[138:141], v1, v179 op_sel_hi:[0,0,0]
	v_mfma_scale_f32_16x16x128_f8f6f4 v[126:129], v[2:9], v[220:227], v[126:129], v1, v179 op_sel_hi:[0,0,0]
	v_mfma_scale_f32_16x16x128_f8f6f4 v[122:125], v[10:17], v[220:227], v[122:125], v1, v179 op_sel_hi:[0,0,0]
	v_mfma_scale_f32_16x16x128_f8f6f4 v[110:113], v[2:9], v[228:235], v[110:113], v1, v179 op_sel_hi:[0,0,0]
	v_mfma_scale_f32_16x16x128_f8f6f4 v[106:109], v[10:17], v[228:235], v[106:109], v1, v179 op_sel_hi:[0,0,0]
	s_nop 0
	s_setprio 0
	v_mfma_scale_f32_16x16x128_f8f6f4 v[150:153], v[18:25], v[204:211], v[150:153], v1, v179 op_sel_hi:[0,0,0]
	v_mfma_scale_f32_16x16x128_f8f6f4 v[146:149], v[26:33], v[204:211], v[146:149], v1, v179 op_sel_hi:[0,0,0]
	v_mfma_scale_f32_16x16x128_f8f6f4 v[134:137], v[18:25], v[212:219], v[134:137], v1, v179 op_sel_hi:[0,0,0]
	v_mfma_scale_f32_16x16x128_f8f6f4 v[130:133], v[26:33], v[212:219], v[130:133], v1, v179 op_sel_hi:[0,0,0]
	v_mfma_scale_f32_16x16x128_f8f6f4 v[118:121], v[18:25], v[220:227], v[118:121], v1, v179 op_sel_hi:[0,0,0]
	v_mfma_scale_f32_16x16x128_f8f6f4 v[114:117], v[26:33], v[220:227], v[114:117], v1, v179 op_sel_hi:[0,0,0]
	v_mfma_scale_f32_16x16x128_f8f6f4 v[102:105], v[18:25], v[228:235], v[102:105], v1, v179 op_sel_hi:[0,0,0]
	v_mfma_scale_f32_16x16x128_f8f6f4 v[98:101], v[26:33], v[228:235], v[98:101], v1, v179 op_sel_hi:[0,0,0]
	s_setprio 1
	s_barrier
	s_mov_b32 m0, s51
	v_lshl_add_u64 v[188:189], v[188:189], 0, s[74:75]
	s_add_u32 s8, s8, 0x40080
	ds_read_b128 v[204:207], v201 offset:49152
	ds_read_b128 v[212:215], v201 offset:51200
	ds_read_b128 v[208:211], v202 offset:49152
	ds_read_b128 v[216:219], v202 offset:51200
	ds_read_b128 v[220:223], v201 offset:53248
	ds_read_b128 v[228:231], v201 offset:55296
	ds_read_b128 v[224:227], v202 offset:53248
	ds_read_b128 v[232:235], v202 offset:55296
	global_load_lds_dwordx4 v[188:189], off
	v_lshl_add_u64 v[188:189], v[190:191], 0, s[74:75]
	s_mov_b32 m0, s24
	s_addc_u32 s9, s9, 0
	global_load_lds_dwordx4 v[188:189], off
	v_lshl_add_u64 v[188:189], s[8:9], 0, v[166:167]
	s_mov_b32 m0, s61
	s_nop 0
	global_load_lds_dwordx4 v[188:189], off
	v_lshl_add_u64 v[188:189], s[8:9], 0, v[172:173]
	s_mov_b32 m0, s58
	s_nop 0
	global_load_lds_dwordx4 v[188:189], off
	v_lshl_add_u64 v[188:189], v[192:193], 0, s[74:75]
	s_mov_b32 m0, s25
	s_nop 0
	global_load_lds_dwordx4 v[188:189], off
	v_lshl_add_u64 v[188:189], v[194:195], 0, s[74:75]
	s_mov_b32 m0, s60
	s_nop 0
	global_load_lds_dwordx4 v[188:189], off
	s_waitcnt vmcnt(8)
	s_waitcnt lgkmcnt(0)
	s_barrier
	s_setprio 0
	s_waitcnt lgkmcnt(0)
	v_mfma_scale_f32_16x16x128_f8f6f4 v[86:89], v[2:9], v[204:211], v[86:89], v1, v179 op_sel_hi:[0,0,0]
	v_mfma_scale_f32_16x16x128_f8f6f4 v[82:85], v[10:17], v[204:211], v[82:85], v1, v179 op_sel_hi:[0,0,0]
	v_mfma_scale_f32_16x16x128_f8f6f4 v[70:73], v[2:9], v[212:219], v[70:73], v1, v179 op_sel_hi:[0,0,0]
	v_mfma_scale_f32_16x16x128_f8f6f4 v[66:69], v[10:17], v[212:219], v[66:69], v1, v179 op_sel_hi:[0,0,0]
	v_mfma_scale_f32_16x16x128_f8f6f4 v[58:61], v[2:9], v[220:227], v[58:61], v1, v179 op_sel_hi:[0,0,0]
	v_mfma_scale_f32_16x16x128_f8f6f4 v[50:53], v[10:17], v[220:227], v[50:53], v1, v179 op_sel_hi:[0,0,0]
	v_mfma_scale_f32_16x16x128_f8f6f4 v[42:45], v[2:9], v[228:235], v[42:45], v1, v179 op_sel_hi:[0,0,0]
	v_mfma_scale_f32_16x16x128_f8f6f4 v[34:37], v[10:17], v[228:235], v[34:37], v1, v179 op_sel_hi:[0,0,0]
	s_nop 0
	s_setprio 0
	v_mfma_scale_f32_16x16x128_f8f6f4 v[94:97], v[18:25], v[204:211], v[94:97], v1, v179 op_sel_hi:[0,0,0]
	v_mfma_scale_f32_16x16x128_f8f6f4 v[90:93], v[26:33], v[204:211], v[90:93], v1, v179 op_sel_hi:[0,0,0]
	v_mfma_scale_f32_16x16x128_f8f6f4 v[78:81], v[18:25], v[212:219], v[78:81], v1, v179 op_sel_hi:[0,0,0]
	v_mfma_scale_f32_16x16x128_f8f6f4 v[74:77], v[26:33], v[212:219], v[74:77], v1, v179 op_sel_hi:[0,0,0]
	v_mfma_scale_f32_16x16x128_f8f6f4 v[62:65], v[18:25], v[220:227], v[62:65], v1, v179 op_sel_hi:[0,0,0]
	v_mfma_scale_f32_16x16x128_f8f6f4 v[54:57], v[26:33], v[220:227], v[54:57], v1, v179 op_sel_hi:[0,0,0]
	v_mfma_scale_f32_16x16x128_f8f6f4 v[46:49], v[18:25], v[228:235], v[46:49], v1, v179 op_sel_hi:[0,0,0]
	v_mfma_scale_f32_16x16x128_f8f6f4 v[38:41], v[26:33], v[228:235], v[38:41], v1, v179 op_sel_hi:[0,0,0]
	s_setprio 1
	s_barrier
	s_add_i32 s78, s78, 2
	s_add_u32 s76, s76, 0x100
	s_addc_u32 s77, s77, 0
	s_add_u32 s6, s6, 0x100
	s_addc_u32 s7, s7, 0
	s_cmp_gt_u32 s78, 13
	s_cbranch_scc0 .LBB0_321
	s_setprio 0
	s_and_b64 vcc, exec, s[14:15]
	s_cbranch_vccz .LBB0_324
	s_barrier

; #define GAS __attribute__((address_space(1)))
; #define PG8_STAGE(bufoff, gbase, voff) do { _Pragma("unroll") for (int _i = 0; _i < 2; ++_i) \
;         __builtin_amdgcn_global_load_lds((const GAS unsigned*)((const GAS char*)(gbase) + (voff)[_i]), (LAS unsigned*)(lds + (bufoff) + ldsw + _i * 8192), 16, 0, 0); } while (0)
; #define PG8_LDA(dst, b, h) do { _Pragma("unroll") for (int m = 0; m < 4; ++m) { dst[m].lo = *(const LAS i32x4v*)(lds + PG8_SA(b, h) + (FP8 ? aoff8[0] : aoff) + m * 2048); dst[m].hi = *(const LAS i32x4v*)(lds + PG8_SA(b, h) + (FP8 ? aoff8[1] : aoff + 1024) + m * 2048); } } while (0)
; #define PG8_WAIT_V(n) asm volatile("s_waitcnt vmcnt(" #n ")" ::: "memory")
; template <class Epi, class Sched, bool GATHER, bool FP8 = false, bool UNI = false>
; __device__ __forceinline__ void gemm_phase(LAS unsigned char* lds, const Sched& S, const Epi& E) {
;     ...
;         const GAS char* cA = cur.a; const GAS char* cB = cur.b; const GAS char* nA = nxt.a; const GAS char* nB = nxt.b;
;         const size_t hBc = (size_t)(Epi::WIDE ? 32 : HALF) * cur.ldb, hBn = (size_t)(Epi::WIDE ? 32 : HALF) * nxt.ldb;
;         const int nt = cur.nt;
;         for (int t = 0; t < nt; t += 2) {
;             const bool last = (t == nt - 2);
;             const GAS char* a1 = cA + (size_t)(t + 1) * 128;
;             const GAS char* a2 = last ? nA : cA + (size_t)(t + 2) * 128; const GAS char* b2 = last ? nB : cB + (size_t)(t + 2) * 128;
;             const GAS char* a3 = a2 + 128; const GAS char* b3 = b2 + 128;
;             const size_t hB2 = last ? hBn : hBc;
;             unsigned oa0[2], oa1[2], ob[2];
; #pragma unroll
;             for (int i = 0; i < 2; ++i) { if constexpr (UNI) { oa0[i] = aoc[0][i]; oa1[i] = aoc[1][i]; ob[i] = boc[i]; } else { oa0[i] = last ? aon[0][i] : aoc[0][i]; oa1[i] = last ? aon[1][i] : aoc[1][i]; ob[i] = last ? bon[i] : boc[i]; } }
;             PG8_LDB(B0, 0, 0); PG8_LDB(B1, 0, 1); PG8_SCHED; PG8_LDA(At, 0, 0); PG8_STAGE(PG8_SA(1, 1), a1, aoc[1]);
;             PG8_WAIT_V(8); PG8_WAIT_L(0); PG8_BAR; PG8_MMA(0, 0, At, B0); PG8_MMA(0, 1, At, B1); PG8_BAR; PG8_SCHED;
;             PG8_LDA(At, 0, 1); PG8_STAGE(PG8_SB(0, 0), b2, ob); PG8_STAGE(PG8_SB(0, 1), b2 + hB2, ob); PG8_STAGE(PG8_SA(0, 0), a2, oa0);
;             PG8_WAIT_V(8); PG8_WAIT_L(0); PG8_BAR; PG8_MMA(1, 0, At, B0); PG8_MMA(1, 1, At, B1); PG8_BAR; PG8_SCHED;
.LBB0_1047:
	s_add_i32 s81, s28, 2
	s_add_u32 s29, s8, s6
	s_addc_u32 s30, s9, s7
	v_add_u32_e32 v135, s43, v183
	s_add_u32 s31, s29, 0x100
	ds_read_b128 v[144:147], v135
	ds_read_b128 v[148:151], v135 offset:1024
	ds_read_b128 v[190:193], v135 offset:2048
	ds_read_b128 v[194:197], v135 offset:3072
	v_add_u32_e32 v135, s46, v183
	s_addc_u32 s30, s30, 0
	ds_read_b128 v[198:201], v135
	ds_read_b128 v[202:205], v135 offset:1024
	ds_read_b128 v[206:209], v135 offset:2048
	ds_read_b128 v[210:213], v135 offset:3072
	s_add_u32 s35, s40, s6
	s_addc_u32 s82, s41, s7
	s_cmp_eq_u32 s39, s28
	s_cselect_b64 vcc, -1, 0
	s_and_b64 s[28:29], vcc, exec
	s_cselect_b32 s28, s26, s31
	s_cselect_b32 s34, s80, s38
	v_cndmask_b32_e32 v152, v132, v174, vcc
	s_cselect_b32 s29, s27, s30
	s_cselect_b32 s31, s23, s82
	s_cselect_b32 s30, s22, s35
	s_ashr_i32 s35, s34, 31
	v_cndmask_b32_e32 v131, v130, v173, vcc
	v_cndmask_b32_e32 v158, v133, v172, vcc
	v_cndmask_b32_e32 v180, v136, v178, vcc
	v_cndmask_b32_e32 v135, v134, v175, vcc
	v_cndmask_b32_e32 v246, v138, v176, vcc
	v_lshl_add_u64 v[248:249], v[142:143], 0, s[6:7]
	s_add_i32 m0, s49, 0xc000
	ds_read_b128 v[214:217], v185
	ds_read_b128 v[218:221], v185 offset:1024
	ds_read_b128 v[222:225], v185 offset:2048
	ds_read_b128 v[226:229], v185 offset:3072
	ds_read_b128 v[230:233], v185 offset:4096
	ds_read_b128 v[234:237], v185 offset:5120
	ds_read_b128 v[238:241], v185 offset:6144
	ds_read_b128 v[242:245], v185 offset:7168
	global_load_lds_dwordx4 v[248:249], off
	v_lshl_add_u64 v[248:249], v[140:141], 0, s[6:7]
	s_add_i32 m0, s49, 0xe000
	s_nop 0
	global_load_lds_dwordx4 v[248:249], off
	s_waitcnt vmcnt(8)
	s_waitcnt lgkmcnt(0)
	s_barrier
	s_setprio 0
	s_waitcnt lgkmcnt(0)
	v_mfma_f32_16x16x32_bf16 v[110:113], v[144:147], v[214:217], v[110:113]
	v_mfma_f32_16x16x32_bf16 v[102:105], v[190:193], v[214:217], v[102:105]
	v_mfma_f32_16x16x32_bf16 v[94:97], v[144:147], v[222:225], v[94:97]
	v_mfma_f32_16x16x32_bf16 v[90:93], v[190:193], v[222:225], v[90:93]
	v_mfma_f32_16x16x32_bf16 v[86:89], v[144:147], v[230:233], v[86:89]
	v_mfma_f32_16x16x32_bf16 v[82:85], v[190:193], v[230:233], v[82:85]
	v_mfma_f32_16x16x32_bf16 v[78:81], v[144:147], v[238:241], v[78:81]
	v_mfma_f32_16x16x32_bf16 v[74:77], v[190:193], v[238:241], v[74:77]
	v_mfma_f32_16x16x32_bf16 v[110:113], v[148:151], v[218:221], v[110:113]
	v_mfma_f32_16x16x32_bf16 v[102:105], v[194:197], v[218:221], v[102:105]
	v_mfma_f32_16x16x32_bf16 v[94:97], v[148:151], v[226:229], v[94:97]
	v_mfma_f32_16x16x32_bf16 v[90:93], v[194:197], v[226:229], v[90:93]
	v_mfma_f32_16x16x32_bf16 v[86:89], v[148:151], v[234:237], v[86:89]
	v_mfma_f32_16x16x32_bf16 v[82:85], v[194:197], v[234:237], v[82:85]
	v_mfma_f32_16x16x32_bf16 v[78:81], v[148:151], v[242:245], v[78:81]
	v_mfma_f32_16x16x32_bf16 v[74:77], v[194:197], v[242:245], v[74:77]
	s_nop 0
	s_setprio 0
	v_mfma_f32_16x16x32_bf16 v[70:73], v[198:201], v[214:217], v[70:73]
	v_mfma_f32_16x16x32_bf16 v[66:69], v[206:209], v[214:217], v[66:69]
	v_mfma_f32_16x16x32_bf16 v[62:65], v[198:201], v[222:225], v[62:65]
	v_mfma_f32_16x16x32_bf16 v[58:61], v[206:209], v[222:225], v[58:61]
	v_mfma_f32_16x16x32_bf16 v[54:57], v[198:201], v[230:233], v[54:57]
	v_mfma_f32_16x16x32_bf16 v[50:53], v[206:209], v[230:233], v[50:53]
	v_mfma_f32_16x16x32_bf16 v[46:49], v[198:201], v[238:241], v[46:49]
	v_mfma_f32_16x16x32_bf16 v[42:45], v[206:209], v[238:241], v[42:45]
	v_mfma_f32_16x16x32_bf16 v[70:73], v[202:205], v[218:221], v[70:73]
	v_mfma_f32_16x16x32_bf16 v[66:69], v[210:213], v[218:221], v[66:69]
	v_mfma_f32_16x16x32_bf16 v[62:65], v[202:205], v[226:229], v[62:65]
	v_mfma_f32_16x16x32_bf16 v[58:61], v[210:213], v[226:229], v[58:61]
	v_mfma_f32_16x16x32_bf16 v[54:57], v[202:205], v[234:237], v[54:57]
	v_mfma_f32_16x16x32_bf16 v[50:53], v[210:213], v[234:237], v[50:53]
	v_mfma_f32_16x16x32_bf16 v[46:49], v[202:205], v[242:245], v[46:49]
	v_mfma_f32_16x16x32_bf16 v[42:45], v[210:213], v[242:245], v[42:45]
	s_setprio 1
	s_barrier
	s_mov_b32 m0, s44
	s_lshl_b64 s[34:35], s[34:35], 5
	ds_read_b128 v[214:217], v185 offset:16384
	ds_read_b128 v[218:221], v185 offset:17408
	ds_read_b128 v[222:225], v185 offset:18432
	ds_read_b128 v[226:229], v185 offset:19456
	ds_read_b128 v[230:233], v185 offset:20480
	ds_read_b128 v[234:237], v185 offset:21504
	ds_read_b128 v[238:241], v185 offset:22528
	ds_read_b128 v[242:245], v185 offset:23552
	global_load_lds_dwordx4 v158, s[30:31]
	s_mov_b32 m0, s45
	s_add_u32 s34, s30, s34
	global_load_lds_dwordx4 v246, s[30:31]
	s_addc_u32 s35, s31, s35
	s_mov_b32 m0, s47
	v_mov_b32_e32 v247, v159
	global_load_lds_dwordx4 v158, s[34:35]
	s_mov_b32 m0, s48
	v_mov_b32_e32 v153, v159
	global_load_lds_dwordx4 v246, s[34:35]
	s_mov_b32 m0, s49
	v_mov_b32_e32 v181, v159
	global_load_lds_dwordx4 v152, s[28:29]
	s_mov_b32 m0, s50
	v_lshl_add_u64 v[248:249], s[30:31], 0, v[158:159]
	global_load_lds_dwordx4 v180, s[28:29]
	s_waitcnt vmcnt(8)
	s_waitcnt lgkmcnt(0)
	v_lshl_add_u64 v[250:251], s[30:31], 0, v[246:247]
	v_lshl_add_u64 v[252:253], s[34:35], 0, v[158:159]
	v_lshl_add_u64 v[246:247], s[34:35], 0, v[246:247]
	v_lshl_add_u64 v[152:153], s[28:29], 0, v[152:153]
	v_lshl_add_u64 v[180:181], s[28:29], 0, v[180:181]
	s_barrier
; #define PG8_STAGE(bufoff, gbase, voff) do { _Pragma("unroll") for (int _i = 0; _i < 2; ++_i) \
;         __builtin_amdgcn_global_load_lds((const GAS unsigned*)((const GAS char*)(gbase) + (voff)[_i]), (LAS unsigned*)(lds + (bufoff) + ldsw + _i * 8192), 16, 0, 0); } while (0)
; #define PG8_LDA(dst, b, h) do { _Pragma("unroll") for (int m = 0; m < 4; ++m) { dst[m].lo = *(const LAS i32x4v*)(lds + PG8_SA(b, h) + (FP8 ? aoff8[0] : aoff) + m * 2048); dst[m].hi = *(const LAS i32x4v*)(lds + PG8_SA(b, h) + (FP8 ? aoff8[1] : aoff + 1024) + m * 2048); } } while (0)
; #define PG8_LDB(dst, b, h) do { _Pragma("unroll") for (int n = 0; n < 2; ++n) { dst[n].lo = *(const LAS i32x4v*)(lds + PG8_SB(b, h) + (FP8 ? boff8[0] : boff) + n * 2048); dst[n].hi = *(const LAS i32x4v*)(lds + PG8_SB(b, h) + (FP8 ? boff8[1] : boff + 1024) + n * 2048); } } while (0)
; #define PG8_WAIT_V(n) asm volatile("s_waitcnt vmcnt(" #n ")" ::: "memory")
; #define PG8_WAIT_L(n) asm volatile("s_waitcnt lgkmcnt(" #n ")" ::: "memory")
; #define PG8_BAR __builtin_amdgcn_s_barrier()
; #define PG8_SCHED __builtin_amdgcn_sched_barrier(0)
; template <class Epi, class Sched, bool GATHER, bool FP8 = false, bool UNI = false>
; __device__ __forceinline__ void gemm_phase(LAS unsigned char* lds, const Sched& S, const Epi& E) {
;     ...
;             PG8_WAIT_V(8); PG8_WAIT_L(0); PG8_BAR; PG8_MMA(1, 0, At, B0); PG8_MMA(1, 1, At, B1); PG8_BAR; PG8_SCHED;
;             PG8_LDB(B0, 1, 0); PG8_LDB(B1, 1, 1); PG8_SCHED; PG8_LDA(At, 1, 0); PG8_STAGE(PG8_SA(0, 1), a2, oa1);
;             PG8_WAIT_V(8); PG8_WAIT_L(0); PG8_BAR; PG8_MMA(0, 0, At, B0); PG8_MMA(0, 1, At, B1); PG8_BAR; PG8_SCHED;
	s_setprio 0
	s_waitcnt lgkmcnt(0)
	v_mfma_f32_16x16x32_bf16 v[38:41], v[144:147], v[214:217], v[38:41]
	v_mfma_f32_16x16x32_bf16 v[34:37], v[190:193], v[214:217], v[34:37]
	v_mfma_f32_16x16x32_bf16 v[30:33], v[144:147], v[222:225], v[30:33]
	v_mfma_f32_16x16x32_bf16 v[26:29], v[190:193], v[222:225], v[26:29]
	v_mfma_f32_16x16x32_bf16 v[22:25], v[144:147], v[230:233], v[22:25]
	v_mfma_f32_16x16x32_bf16 v[18:21], v[190:193], v[230:233], v[18:21]
	v_mfma_f32_16x16x32_bf16 v[14:17], v[144:147], v[238:241], v[14:17]
	v_mfma_f32_16x16x32_bf16 v[10:13], v[190:193], v[238:241], v[10:13]
	v_mfma_f32_16x16x32_bf16 v[38:41], v[148:151], v[218:221], v[38:41]
	v_mfma_f32_16x16x32_bf16 v[34:37], v[194:197], v[218:221], v[34:37]
	v_mfma_f32_16x16x32_bf16 v[30:33], v[148:151], v[226:229], v[30:33]
	v_mfma_f32_16x16x32_bf16 v[26:29], v[194:197], v[226:229], v[26:29]
	v_mfma_f32_16x16x32_bf16 v[22:25], v[148:151], v[234:237], v[22:25]
	v_mfma_f32_16x16x32_bf16 v[18:21], v[194:197], v[234:237], v[18:21]
	v_mfma_f32_16x16x32_bf16 v[14:17], v[148:151], v[242:245], v[14:17]
	v_mfma_f32_16x16x32_bf16 v[10:13], v[194:197], v[242:245], v[10:13]
	s_nop 0
	s_setprio 0
	v_mfma_f32_16x16x32_bf16 v[6:9], v[198:201], v[214:217], v[6:9]
	v_mfma_f32_16x16x32_bf16 v[2:5], v[206:209], v[214:217], v[2:5]
	v_mfma_f32_16x16x32_bf16 v[98:101], v[198:201], v[222:225], v[98:101]
	v_mfma_f32_16x16x32_bf16 v[106:109], v[206:209], v[222:225], v[106:109]
	v_mfma_f32_16x16x32_bf16 v[114:117], v[198:201], v[230:233], v[114:117]
	v_mfma_f32_16x16x32_bf16 v[118:121], v[206:209], v[230:233], v[118:121]
	v_mfma_f32_16x16x32_bf16 v[122:125], v[198:201], v[238:241], v[122:125]
	v_mfma_f32_16x16x32_bf16 v[126:129], v[206:209], v[238:241], v[126:129]
	v_mfma_f32_16x16x32_bf16 v[6:9], v[202:205], v[218:221], v[6:9]
	v_mfma_f32_16x16x32_bf16 v[2:5], v[210:213], v[218:221], v[2:5]
	v_mfma_f32_16x16x32_bf16 v[98:101], v[202:205], v[226:229], v[98:101]
	v_mfma_f32_16x16x32_bf16 v[106:109], v[210:213], v[226:229], v[106:109]
	v_mfma_f32_16x16x32_bf16 v[114:117], v[202:205], v[234:237], v[114:117]
	v_mfma_f32_16x16x32_bf16 v[118:121], v[210:213], v[234:237], v[118:121]
	v_mfma_f32_16x16x32_bf16 v[122:125], v[202:205], v[242:245], v[122:125]
	v_mfma_f32_16x16x32_bf16 v[126:129], v[210:213], v[242:245], v[126:129]
	s_setprio 1
	s_barrier
	v_add_u32_e32 v137, s64, v183
	ds_read_b128 v[144:147], v137
	ds_read_b128 v[148:151], v137 offset:1024
	ds_read_b128 v[190:193], v137 offset:2048
	ds_read_b128 v[194:197], v137 offset:3072
	v_add_u32_e32 v137, s69, v183
	ds_read_b128 v[198:201], v137
	ds_read_b128 v[202:205], v137 offset:1024
	ds_read_b128 v[206:209], v137 offset:2048
	ds_read_b128 v[210:213], v137 offset:3072
	s_mov_b32 m0, s51
	ds_read_b128 v[214:217], v185 offset:32768
	ds_read_b128 v[218:221], v185 offset:33792
	ds_read_b128 v[222:225], v185 offset:34816
	ds_read_b128 v[226:229], v185 offset:35840
	ds_read_b128 v[230:233], v185 offset:36864
	ds_read_b128 v[234:237], v185 offset:37888
	ds_read_b128 v[238:241], v185 offset:38912
	ds_read_b128 v[242:245], v185 offset:39936
	global_load_lds_dwordx4 v131, s[28:29]
	s_mov_b32 m0, s56
	s_nop 0
	global_load_lds_dwordx4 v135, s[28:29]
	s_waitcnt vmcnt(8)
	s_waitcnt lgkmcnt(0)
	s_barrier
	s_setprio 0
	s_waitcnt lgkmcnt(0)
	v_mfma_f32_16x16x32_bf16 v[110:113], v[144:147], v[214:217], v[110:113]
	v_mfma_f32_16x16x32_bf16 v[102:105], v[190:193], v[214:217], v[102:105]
	v_mfma_f32_16x16x32_bf16 v[94:97], v[144:147], v[222:225], v[94:97]
	v_mfma_f32_16x16x32_bf16 v[90:93], v[190:193], v[222:225], v[90:93]
	v_mfma_f32_16x16x32_bf16 v[86:89], v[144:147], v[230:233], v[86:89]
	v_mfma_f32_16x16x32_bf16 v[82:85], v[190:193], v[230:233], v[82:85]
	v_mfma_f32_16x16x32_bf16 v[78:81], v[144:147], v[238:241], v[78:81]
	v_mfma_f32_16x16x32_bf16 v[74:77], v[190:193], v[238:241], v[74:77]
	v_mfma_f32_16x16x32_bf16 v[110:113], v[148:151], v[218:221], v[110:113]
	v_mfma_f32_16x16x32_bf16 v[102:105], v[194:197], v[218:221], v[102:105]
	v_mfma_f32_16x16x32_bf16 v[94:97], v[148:151], v[226:229], v[94:97]
	v_mfma_f32_16x16x32_bf16 v[90:93], v[194:197], v[226:229], v[90:93]
	v_mfma_f32_16x16x32_bf16 v[86:89], v[148:151], v[234:237], v[86:89]
	v_mfma_f32_16x16x32_bf16 v[82:85], v[194:197], v[234:237], v[82:85]
	v_mfma_f32_16x16x32_bf16 v[78:81], v[148:151], v[242:245], v[78:81]
	v_mfma_f32_16x16x32_bf16 v[74:77], v[194:197], v[242:245], v[74:77]
	s_nop 0
	s_setprio 0
	v_mfma_f32_16x16x32_bf16 v[70:73], v[198:201], v[214:217], v[70:73]
	v_mfma_f32_16x16x32_bf16 v[66:69], v[206:209], v[214:217], v[66:69]
	v_mfma_f32_16x16x32_bf16 v[62:65], v[198:201], v[222:225], v[62:65]
	v_mfma_f32_16x16x32_bf16 v[58:61], v[206:209], v[222:225], v[58:61]
	v_mfma_f32_16x16x32_bf16 v[54:57], v[198:201], v[230:233], v[54:57]
	v_mfma_f32_16x16x32_bf16 v[50:53], v[206:209], v[230:233], v[50:53]
	v_mfma_f32_16x16x32_bf16 v[46:49], v[198:201], v[238:241], v[46:49]
	v_mfma_f32_16x16x32_bf16 v[42:45], v[206:209], v[238:241], v[42:45]
	v_mfma_f32_16x16x32_bf16 v[70:73], v[202:205], v[218:221], v[70:73]
	v_mfma_f32_16x16x32_bf16 v[66:69], v[210:213], v[218:221], v[66:69]
	v_mfma_f32_16x16x32_bf16 v[62:65], v[202:205], v[226:229], v[62:65]
	v_mfma_f32_16x16x32_bf16 v[58:61], v[210:213], v[226:229], v[58:61]
	v_mfma_f32_16x16x32_bf16 v[54:57], v[202:205], v[234:237], v[54:57]
	v_mfma_f32_16x16x32_bf16 v[50:53], v[210:213], v[234:237], v[50:53]
	v_mfma_f32_16x16x32_bf16 v[46:49], v[202:205], v[242:245], v[46:49]
	v_mfma_f32_16x16x32_bf16 v[42:45], v[210:213], v[242:245], v[42:45]
	s_setprio 1
	s_barrier
; #define PG8_STAGE(bufoff, gbase, voff) do { _Pragma("unroll") for (int _i = 0; _i < 2; ++_i) \
;         __builtin_amdgcn_global_load_lds((const GAS unsigned*)((const GAS char*)(gbase) + (voff)[_i]), (LAS unsigned*)(lds + (bufoff) + ldsw + _i * 8192), 16, 0, 0); } while (0)
; #define PG8_LDA(dst, b, h) do { _Pragma("unroll") for (int m = 0; m < 4; ++m) { dst[m].lo = *(const LAS i32x4v*)(lds + PG8_SA(b, h) + (FP8 ? aoff8[0] : aoff) + m * 2048); dst[m].hi = *(const LAS i32x4v*)(lds + PG8_SA(b, h) + (FP8 ? aoff8[1] : aoff + 1024) + m * 2048); } } while (0)
; #define PG8_WAIT_V(n) asm volatile("s_waitcnt vmcnt(" #n ")" ::: "memory")
; #define PG8_WAIT_L(n) asm volatile("s_waitcnt lgkmcnt(" #n ")" ::: "memory")
; #define PG8_BAR __builtin_amdgcn_s_barrier()
; #define PG8_SCHED __builtin_amdgcn_sched_barrier(0)
; template <class Epi, class Sched, bool GATHER, bool FP8 = false, bool UNI = false>
; __device__ __forceinline__ void gemm_phase(LAS unsigned char* lds, const Sched& S, const Epi& E) {
;     ...
;             PG8_LDA(At, 1, 1); PG8_STAGE(PG8_SB(1, 0), b3, ob); PG8_STAGE(PG8_SB(1, 1), b3 + hB2, ob); PG8_STAGE(PG8_SA(1, 0), a3, oa0);
;             PG8_WAIT_V(8); PG8_WAIT_L(0); PG8_BAR; PG8_MMA(1, 0, At, B0); PG8_MMA(1, 1, At, B1); PG8_BAR; PG8_SCHED;
;         }
;         if (wr == 0) PG8_BAR;
	s_mov_b32 m0, s65
	v_lshl_add_u64 v[248:249], v[248:249], 0, s[16:17]
	ds_read_b128 v[214:217], v185 offset:49152
	ds_read_b128 v[218:221], v185 offset:50176
	ds_read_b128 v[222:225], v185 offset:51200
	ds_read_b128 v[226:229], v185 offset:52224
	ds_read_b128 v[230:233], v185 offset:53248
	ds_read_b128 v[234:237], v185 offset:54272
	ds_read_b128 v[238:241], v185 offset:55296
	ds_read_b128 v[242:245], v185 offset:56320
	global_load_lds_dwordx4 v[248:249], off
	v_lshl_add_u64 v[248:249], v[250:251], 0, s[16:17]
	s_mov_b32 m0, s66
	v_lshl_add_u64 v[246:247], v[246:247], 0, s[16:17]
	global_load_lds_dwordx4 v[248:249], off
	v_lshl_add_u64 v[248:249], v[252:253], 0, s[16:17]
	s_mov_b32 m0, s70
	v_lshl_add_u64 v[152:153], v[152:153], 0, s[16:17]
	global_load_lds_dwordx4 v[248:249], off
	s_mov_b32 m0, s71
	s_nop 0
	global_load_lds_dwordx4 v[246:247], off
	s_mov_b32 m0, s67
	s_nop 0
	global_load_lds_dwordx4 v[152:153], off
	v_lshl_add_u64 v[152:153], v[180:181], 0, s[16:17]
	s_mov_b32 m0, s68
	s_nop 0
	global_load_lds_dwordx4 v[152:153], off
	s_waitcnt vmcnt(8)
	s_waitcnt lgkmcnt(0)
	s_barrier
	s_setprio 0
	s_waitcnt lgkmcnt(0)
	v_mfma_f32_16x16x32_bf16 v[38:41], v[144:147], v[214:217], v[38:41]
	v_mfma_f32_16x16x32_bf16 v[34:37], v[190:193], v[214:217], v[34:37]
	v_mfma_f32_16x16x32_bf16 v[30:33], v[144:147], v[222:225], v[30:33]
	v_mfma_f32_16x16x32_bf16 v[26:29], v[190:193], v[222:225], v[26:29]
	v_mfma_f32_16x16x32_bf16 v[22:25], v[144:147], v[230:233], v[22:25]
	v_mfma_f32_16x16x32_bf16 v[18:21], v[190:193], v[230:233], v[18:21]
	v_mfma_f32_16x16x32_bf16 v[14:17], v[144:147], v[238:241], v[14:17]
	v_mfma_f32_16x16x32_bf16 v[10:13], v[190:193], v[238:241], v[10:13]
	v_mfma_f32_16x16x32_bf16 v[38:41], v[148:151], v[218:221], v[38:41]
	v_mfma_f32_16x16x32_bf16 v[34:37], v[194:197], v[218:221], v[34:37]
	v_mfma_f32_16x16x32_bf16 v[30:33], v[148:151], v[226:229], v[30:33]
	v_mfma_f32_16x16x32_bf16 v[26:29], v[194:197], v[226:229], v[26:29]
	v_mfma_f32_16x16x32_bf16 v[22:25], v[148:151], v[234:237], v[22:25]
	v_mfma_f32_16x16x32_bf16 v[18:21], v[194:197], v[234:237], v[18:21]
	v_mfma_f32_16x16x32_bf16 v[14:17], v[148:151], v[242:245], v[14:17]
	v_mfma_f32_16x16x32_bf16 v[10:13], v[194:197], v[242:245], v[10:13]
	s_nop 0
	s_setprio 0
	v_mfma_f32_16x16x32_bf16 v[6:9], v[198:201], v[214:217], v[6:9]
	v_mfma_f32_16x16x32_bf16 v[2:5], v[206:209], v[214:217], v[2:5]
	v_mfma_f32_16x16x32_bf16 v[98:101], v[198:201], v[222:225], v[98:101]
	v_mfma_f32_16x16x32_bf16 v[106:109], v[206:209], v[222:225], v[106:109]
	v_mfma_f32_16x16x32_bf16 v[114:117], v[198:201], v[230:233], v[114:117]
	v_mfma_f32_16x16x32_bf16 v[118:121], v[206:209], v[230:233], v[118:121]
	v_mfma_f32_16x16x32_bf16 v[122:125], v[198:201], v[238:241], v[122:125]
	v_mfma_f32_16x16x32_bf16 v[126:129], v[206:209], v[238:241], v[126:129]
	v_mfma_f32_16x16x32_bf16 v[6:9], v[202:205], v[218:221], v[6:9]
	v_mfma_f32_16x16x32_bf16 v[2:5], v[210:213], v[218:221], v[2:5]
	v_mfma_f32_16x16x32_bf16 v[98:101], v[202:205], v[226:229], v[98:101]
	v_mfma_f32_16x16x32_bf16 v[106:109], v[210:213], v[226:229], v[106:109]
	v_mfma_f32_16x16x32_bf16 v[114:117], v[202:205], v[234:237], v[114:117]
	v_mfma_f32_16x16x32_bf16 v[118:121], v[210:213], v[234:237], v[118:121]
	v_mfma_f32_16x16x32_bf16 v[122:125], v[202:205], v[242:245], v[122:125]
	v_mfma_f32_16x16x32_bf16 v[126:129], v[210:213], v[242:245], v[126:129]
	s_setprio 1
	s_barrier
	s_add_u32 s6, s6, 0x100
	s_addc_u32 s7, s7, 0
	s_cmp_ge_i32 s81, s36
	s_mov_b32 s28, s81
	s_cbranch_scc0 .LBB0_1047
	s_setprio 0
	s_and_b64 vcc, exec, s[18:19]
	s_cbranch_vccz .LBB0_1050
	s_barrier

; #define PG8_STAGE(bufoff, gbase, voff) do { _Pragma("unroll") for (int _i = 0; _i < 2; ++_i) \
;         __builtin_amdgcn_global_load_lds((const GAS unsigned*)((const GAS char*)(gbase) + (voff)[_i]), (LAS unsigned*)(lds + (bufoff) + ldsw + _i * 8192), 16, 0, 0); } while (0)
; #define PG8_LDA(dst, b, h) do { _Pragma("unroll") for (int m = 0; m < 4; ++m) { dst[m].lo = *(const LAS i32x4v*)(lds + PG8_SA(b, h) + (FP8 ? aoff8[0] : aoff) + m * 2048); dst[m].hi = *(const LAS i32x4v*)(lds + PG8_SA(b, h) + (FP8 ? aoff8[1] : aoff + 1024) + m * 2048); } } while (0)
; #define PG8_LDB(dst, b, h) do { _Pragma("unroll") for (int n = 0; n < 2; ++n) { dst[n].lo = *(const LAS i32x4v*)(lds + PG8_SB(b, h) + (FP8 ? boff8[0] : boff) + n * 2048); dst[n].hi = *(const LAS i32x4v*)(lds + PG8_SB(b, h) + (FP8 ? boff8[1] : boff + 1024) + n * 2048); } } while (0)
; #define PG8_WAIT_V(n) asm volatile("s_waitcnt vmcnt(" #n ")" ::: "memory")
; #define PG8_WAIT_L(n) asm volatile("s_waitcnt lgkmcnt(" #n ")" ::: "memory")
; #define PG8_BAR __builtin_amdgcn_s_barrier()
; #define PG8_SCHED __builtin_amdgcn_sched_barrier(0)
; template <class Epi, class Sched, bool GATHER, bool FP8 = false, bool UNI = false>
; __device__ __forceinline__ void gemm_phase(LAS unsigned char* lds, const Sched& S, const Epi& E) {
;     ...
;             PG8_LDB(B0, 0, 0); PG8_LDB(B1, 0, 1); PG8_SCHED; PG8_LDA(At, 0, 0); PG8_STAGE(PG8_SA(1, 1), a1, aoc[1]);
;             PG8_WAIT_V(8); PG8_WAIT_L(0); PG8_BAR; PG8_MMA(0, 0, At, B0); PG8_MMA(0, 1, At, B1); PG8_BAR; PG8_SCHED;
;             PG8_LDA(At, 0, 1); PG8_STAGE(PG8_SB(0, 0), b2, ob); PG8_STAGE(PG8_SB(0, 1), b2 + hB2, ob); PG8_STAGE(PG8_SA(0, 0), a2, oa0);
;             PG8_WAIT_V(8); PG8_WAIT_L(0); PG8_BAR; PG8_MMA(1, 0, At, B0); PG8_MMA(1, 1, At, B1); PG8_BAR; PG8_SCHED;
;             PG8_LDB(B0, 1, 0); PG8_LDB(B1, 1, 1); PG8_SCHED; PG8_LDA(At, 1, 0); PG8_STAGE(PG8_SA(0, 1), a2, oa1);
;             PG8_WAIT_V(8); PG8_WAIT_L(0); PG8_BAR; PG8_MMA(0, 0, At, B0); PG8_MMA(0, 1, At, B1); PG8_BAR; PG8_SCHED;
.LBB0_1242:
	ds_read_b128 v[18:21], v187
	ds_read_b128 v[26:29], v187 offset:2048
	ds_read_b128 v[22:25], v188
	ds_read_b128 v[30:33], v188 offset:2048
	ds_read_b128 v[2:5], v189
	ds_read_b128 v[10:13], v189 offset:2048
	ds_read_b128 v[6:9], v190
	ds_read_b128 v[14:17], v190 offset:2048
	s_add_u32 s42, s6, 0x80
	s_addc_u32 s43, s7, 0
	s_cmp_eq_u32 s72, 12
	s_cselect_b32 s45, s39, s43
	s_cselect_b32 s44, s38, s42
	s_cselect_b32 s43, s41, s47
	s_cselect_b32 s42, s40, s46
	v_lshl_add_u64 v[224:225], s[6:7], 0, v[172:173]
	s_add_i32 m0, s56, 0xc000
	ds_read_b128 v[178:181], v191
	ds_read_b128 v[200:203], v191 offset:2048
	ds_read_b128 v[182:185], v192
	ds_read_b128 v[204:207], v192 offset:2048
	ds_read_b128 v[208:211], v191 offset:4096
	ds_read_b128 v[216:219], v191 offset:6144
	ds_read_b128 v[212:215], v192 offset:4096
	ds_read_b128 v[220:223], v192 offset:6144
	global_load_lds_dwordx4 v[224:225], off
	v_lshl_add_u64 v[224:225], s[6:7], 0, v[170:171]
	s_add_i32 m0, s56, 0xe000
	s_nop 0
	global_load_lds_dwordx4 v[224:225], off
	s_waitcnt vmcnt(8)
	s_waitcnt lgkmcnt(0)
	s_barrier
	s_setprio 0
	s_waitcnt lgkmcnt(0)
	v_mfma_scale_f32_16x16x128_f8f6f4 v[158:161], v[18:25], v[178:185], v[158:161], v193, v194 op_sel_hi:[0,0,0]
	v_mfma_scale_f32_16x16x128_f8f6f4 v[154:157], v[26:33], v[178:185], v[154:157], v193, v194 op_sel_hi:[0,0,0]
	v_mfma_scale_f32_16x16x128_f8f6f4 v[146:149], v[18:25], v[200:207], v[146:149], v193, v194 op_sel_hi:[0,0,0]
	v_mfma_scale_f32_16x16x128_f8f6f4 v[138:141], v[26:33], v[200:207], v[138:141], v193, v194 op_sel_hi:[0,0,0]
	v_mfma_scale_f32_16x16x128_f8f6f4 v[130:133], v[18:25], v[208:215], v[130:133], v193, v194 op_sel_hi:[0,0,0]
	v_mfma_scale_f32_16x16x128_f8f6f4 v[122:125], v[26:33], v[208:215], v[122:125], v193, v194 op_sel_hi:[0,0,0]
	v_mfma_scale_f32_16x16x128_f8f6f4 v[114:117], v[18:25], v[216:223], v[114:117], v193, v194 op_sel_hi:[0,0,0]
	v_mfma_scale_f32_16x16x128_f8f6f4 v[106:109], v[26:33], v[216:223], v[106:109], v193, v194 op_sel_hi:[0,0,0]
	s_nop 0
	s_setprio 0
	v_mfma_scale_f32_16x16x128_f8f6f4 v[150:153], v[2:9], v[178:185], v[150:153], v193, v194 op_sel_hi:[0,0,0]
	v_mfma_scale_f32_16x16x128_f8f6f4 v[142:145], v[10:17], v[178:185], v[142:145], v193, v194 op_sel_hi:[0,0,0]
	v_mfma_scale_f32_16x16x128_f8f6f4 v[134:137], v[2:9], v[200:207], v[134:137], v193, v194 op_sel_hi:[0,0,0]
	v_mfma_scale_f32_16x16x128_f8f6f4 v[126:129], v[10:17], v[200:207], v[126:129], v193, v194 op_sel_hi:[0,0,0]
	v_mfma_scale_f32_16x16x128_f8f6f4 v[118:121], v[2:9], v[208:215], v[118:121], v193, v194 op_sel_hi:[0,0,0]
	v_mfma_scale_f32_16x16x128_f8f6f4 v[110:113], v[10:17], v[208:215], v[110:113], v193, v194 op_sel_hi:[0,0,0]
	v_mfma_scale_f32_16x16x128_f8f6f4 v[102:105], v[2:9], v[216:223], v[102:105], v193, v194 op_sel_hi:[0,0,0]
	v_mfma_scale_f32_16x16x128_f8f6f4 v[94:97], v[10:17], v[216:223], v[94:97], v193, v194 op_sel_hi:[0,0,0]
	s_setprio 1
	s_barrier
	s_mov_b32 m0, s48
	v_lshl_add_u64 v[178:179], s[42:43], 0, v[162:163]
	s_add_u32 s74, s42, 0x40000
	ds_read_b128 v[200:203], v191 offset:16384
	ds_read_b128 v[208:211], v191 offset:18432
	ds_read_b128 v[204:207], v192 offset:16384
	ds_read_b128 v[212:215], v192 offset:18432
	ds_read_b128 v[216:219], v191 offset:20480
	ds_read_b128 v[224:227], v191 offset:22528
	ds_read_b128 v[220:223], v192 offset:20480
	ds_read_b128 v[228:231], v192 offset:22528
	global_load_lds_dwordx4 v[178:179], off
	v_lshl_add_u64 v[180:181], s[42:43], 0, v[166:167]
	s_mov_b32 m0, s49
	s_addc_u32 s75, s43, 0
	global_load_lds_dwordx4 v[180:181], off
	v_lshl_add_u64 v[182:183], s[74:75], 0, v[162:163]
	s_mov_b32 m0, s50
	v_lshl_add_u64 v[184:185], s[44:45], 0, v[166:167]
	global_load_lds_dwordx4 v[182:183], off
	v_lshl_add_u64 v[182:183], s[74:75], 0, v[166:167]
	s_mov_b32 m0, s51
	s_nop 0
	global_load_lds_dwordx4 v[182:183], off
	v_lshl_add_u64 v[182:183], s[44:45], 0, v[162:163]
	s_mov_b32 m0, s56
	s_nop 0
	global_load_lds_dwordx4 v[182:183], off
	s_mov_b32 m0, s57
	s_nop 0
	global_load_lds_dwordx4 v[184:185], off
	s_waitcnt vmcnt(8)
	s_waitcnt lgkmcnt(0)
	s_barrier
	s_setprio 0
	s_waitcnt lgkmcnt(0)
	v_mfma_scale_f32_16x16x128_f8f6f4 v[86:89], v[18:25], v[200:207], v[86:89], v193, v194 op_sel_hi:[0,0,0]
	v_mfma_scale_f32_16x16x128_f8f6f4 v[82:85], v[26:33], v[200:207], v[82:85], v193, v194 op_sel_hi:[0,0,0]
	v_mfma_scale_f32_16x16x128_f8f6f4 v[70:73], v[18:25], v[208:215], v[70:73], v193, v194 op_sel_hi:[0,0,0]
	v_mfma_scale_f32_16x16x128_f8f6f4 v[58:61], v[26:33], v[208:215], v[58:61], v193, v194 op_sel_hi:[0,0,0]
	v_mfma_scale_f32_16x16x128_f8f6f4 v[66:69], v[18:25], v[216:223], v[66:69], v193, v194 op_sel_hi:[0,0,0]
	v_mfma_scale_f32_16x16x128_f8f6f4 v[54:57], v[26:33], v[216:223], v[54:57], v193, v194 op_sel_hi:[0,0,0]
	v_mfma_scale_f32_16x16x128_f8f6f4 v[46:49], v[18:25], v[224:231], v[46:49], v193, v194 op_sel_hi:[0,0,0]
	v_mfma_scale_f32_16x16x128_f8f6f4 v[38:41], v[26:33], v[224:231], v[38:41], v193, v194 op_sel_hi:[0,0,0]
	s_nop 0
	s_setprio 0
	v_mfma_scale_f32_16x16x128_f8f6f4 v[98:101], v[2:9], v[200:207], v[98:101], v193, v194 op_sel_hi:[0,0,0]
	v_mfma_scale_f32_16x16x128_f8f6f4 v[90:93], v[10:17], v[200:207], v[90:93], v193, v194 op_sel_hi:[0,0,0]
	v_mfma_scale_f32_16x16x128_f8f6f4 v[78:81], v[2:9], v[208:215], v[78:81], v193, v194 op_sel_hi:[0,0,0]
	v_mfma_scale_f32_16x16x128_f8f6f4 v[74:77], v[10:17], v[208:215], v[74:77], v193, v194 op_sel_hi:[0,0,0]
	v_mfma_scale_f32_16x16x128_f8f6f4 v[62:65], v[2:9], v[216:223], v[62:65], v193, v194 op_sel_hi:[0,0,0]
	v_mfma_scale_f32_16x16x128_f8f6f4 v[50:53], v[10:17], v[216:223], v[50:53], v193, v194 op_sel_hi:[0,0,0]
	v_mfma_scale_f32_16x16x128_f8f6f4 v[42:45], v[2:9], v[224:231], v[42:45], v193, v194 op_sel_hi:[0,0,0]
	v_mfma_scale_f32_16x16x128_f8f6f4 v[34:37], v[10:17], v[224:231], v[34:37], v193, v194 op_sel_hi:[0,0,0]
	s_setprio 1
	s_barrier
; #define PG8_STAGE(bufoff, gbase, voff) do { _Pragma("unroll") for (int _i = 0; _i < 2; ++_i) \
;         __builtin_amdgcn_global_load_lds((const GAS unsigned*)((const GAS char*)(gbase) + (voff)[_i]), (LAS unsigned*)(lds + (bufoff) + ldsw + _i * 8192), 16, 0, 0); } while (0)
; #define PG8_LDA(dst, b, h) do { _Pragma("unroll") for (int m = 0; m < 4; ++m) { dst[m].lo = *(const LAS i32x4v*)(lds + PG8_SA(b, h) + (FP8 ? aoff8[0] : aoff) + m * 2048); dst[m].hi = *(const LAS i32x4v*)(lds + PG8_SA(b, h) + (FP8 ? aoff8[1] : aoff + 1024) + m * 2048); } } while (0)
; #define PG8_LDB(dst, b, h) do { _Pragma("unroll") for (int n = 0; n < 2; ++n) { dst[n].lo = *(const LAS i32x4v*)(lds + PG8_SB(b, h) + (FP8 ? boff8[0] : boff) + n * 2048); dst[n].hi = *(const LAS i32x4v*)(lds + PG8_SB(b, h) + (FP8 ? boff8[1] : boff + 1024) + n * 2048); } } while (0)
; #define PG8_WAIT_V(n) asm volatile("s_waitcnt vmcnt(" #n ")" ::: "memory")
; #define PG8_WAIT_L(n) asm volatile("s_waitcnt lgkmcnt(" #n ")" ::: "memory")
; #define PG8_BAR __builtin_amdgcn_s_barrier()
; #define PG8_SCHED __builtin_amdgcn_sched_barrier(0)
; template <class Epi, class Sched, bool GATHER, bool FP8 = false, bool UNI = false>
; __device__ __forceinline__ void gemm_phase(LAS unsigned char* lds, const Sched& S, const Epi& E) {
;     ...
;             PG8_LDB(B0, 1, 0); PG8_LDB(B1, 1, 1); PG8_SCHED; PG8_LDA(At, 1, 0); PG8_STAGE(PG8_SA(0, 1), a2, oa1);
;             PG8_WAIT_V(8); PG8_WAIT_L(0); PG8_BAR; PG8_MMA(0, 0, At, B0); PG8_MMA(0, 1, At, B1); PG8_BAR; PG8_SCHED;
;             PG8_LDA(At, 1, 1); PG8_STAGE(PG8_SB(1, 0), b3, ob); PG8_STAGE(PG8_SB(1, 1), b3 + hB2, ob); PG8_STAGE(PG8_SA(1, 0), a3, oa0);
;             PG8_WAIT_V(8); PG8_WAIT_L(0); PG8_BAR; PG8_MMA(1, 0, At, B0); PG8_MMA(1, 1, At, B1); PG8_BAR; PG8_SCHED;
;         }
;         if (wr == 0) PG8_BAR;
	ds_read_b128 v[2:5], v195
	ds_read_b128 v[10:13], v195 offset:2048
	ds_read_b128 v[6:9], v196
	ds_read_b128 v[14:17], v196 offset:2048
	ds_read_b128 v[18:21], v197
	ds_read_b128 v[26:29], v197 offset:2048
	ds_read_b128 v[22:25], v198
	ds_read_b128 v[30:33], v198 offset:2048
	s_mov_b32 m0, s58
	v_lshl_add_u64 v[232:233], s[44:45], 0, v[164:165]
	ds_read_b128 v[200:203], v191 offset:32768
	ds_read_b128 v[208:211], v191 offset:34816
	ds_read_b128 v[204:207], v192 offset:32768
	ds_read_b128 v[212:215], v192 offset:34816
	ds_read_b128 v[216:219], v191 offset:36864
	ds_read_b128 v[224:227], v191 offset:38912
	ds_read_b128 v[220:223], v192 offset:36864
	ds_read_b128 v[228:231], v192 offset:38912
	global_load_lds_dwordx4 v[232:233], off
	v_lshl_add_u64 v[232:233], s[44:45], 0, v[168:169]
	s_mov_b32 m0, s59
	s_nop 0
	global_load_lds_dwordx4 v[232:233], off
	s_waitcnt vmcnt(8)
	s_waitcnt lgkmcnt(0)
	s_barrier
	s_setprio 0
	s_waitcnt lgkmcnt(0)
	v_mfma_scale_f32_16x16x128_f8f6f4 v[158:161], v[2:9], v[200:207], v[158:161], v193, v194 op_sel_hi:[0,0,0]
	v_mfma_scale_f32_16x16x128_f8f6f4 v[154:157], v[10:17], v[200:207], v[154:157], v193, v194 op_sel_hi:[0,0,0]
	v_mfma_scale_f32_16x16x128_f8f6f4 v[146:149], v[2:9], v[208:215], v[146:149], v193, v194 op_sel_hi:[0,0,0]
	v_mfma_scale_f32_16x16x128_f8f6f4 v[138:141], v[10:17], v[208:215], v[138:141], v193, v194 op_sel_hi:[0,0,0]
	v_mfma_scale_f32_16x16x128_f8f6f4 v[130:133], v[2:9], v[216:223], v[130:133], v193, v194 op_sel_hi:[0,0,0]
	v_mfma_scale_f32_16x16x128_f8f6f4 v[122:125], v[10:17], v[216:223], v[122:125], v193, v194 op_sel_hi:[0,0,0]
	v_mfma_scale_f32_16x16x128_f8f6f4 v[114:117], v[2:9], v[224:231], v[114:117], v193, v194 op_sel_hi:[0,0,0]
	v_mfma_scale_f32_16x16x128_f8f6f4 v[106:109], v[10:17], v[224:231], v[106:109], v193, v194 op_sel_hi:[0,0,0]
	s_nop 0
	s_setprio 0
	v_mfma_scale_f32_16x16x128_f8f6f4 v[150:153], v[18:25], v[200:207], v[150:153], v193, v194 op_sel_hi:[0,0,0]
	v_mfma_scale_f32_16x16x128_f8f6f4 v[142:145], v[26:33], v[200:207], v[142:145], v193, v194 op_sel_hi:[0,0,0]
	v_mfma_scale_f32_16x16x128_f8f6f4 v[134:137], v[18:25], v[208:215], v[134:137], v193, v194 op_sel_hi:[0,0,0]
	v_mfma_scale_f32_16x16x128_f8f6f4 v[126:129], v[26:33], v[208:215], v[126:129], v193, v194 op_sel_hi:[0,0,0]
	v_mfma_scale_f32_16x16x128_f8f6f4 v[118:121], v[18:25], v[216:223], v[118:121], v193, v194 op_sel_hi:[0,0,0]
	v_mfma_scale_f32_16x16x128_f8f6f4 v[110:113], v[26:33], v[216:223], v[110:113], v193, v194 op_sel_hi:[0,0,0]
	v_mfma_scale_f32_16x16x128_f8f6f4 v[102:105], v[18:25], v[224:231], v[102:105], v193, v194 op_sel_hi:[0,0,0]
	v_mfma_scale_f32_16x16x128_f8f6f4 v[94:97], v[26:33], v[224:231], v[94:97], v193, v194 op_sel_hi:[0,0,0]
	s_setprio 1
	s_barrier
	s_mov_b32 m0, s60
	v_lshl_add_u64 v[178:179], v[178:179], 0, s[16:17]
	s_add_u32 s42, s42, 0x40080
	ds_read_b128 v[200:203], v191 offset:49152
	ds_read_b128 v[208:211], v191 offset:51200
	ds_read_b128 v[204:207], v192 offset:49152
	ds_read_b128 v[212:215], v192 offset:51200
	ds_read_b128 v[216:219], v191 offset:53248
	ds_read_b128 v[224:227], v191 offset:55296
	ds_read_b128 v[220:223], v192 offset:53248
	ds_read_b128 v[228:231], v192 offset:55296
	global_load_lds_dwordx4 v[178:179], off
	v_lshl_add_u64 v[178:179], v[180:181], 0, s[16:17]
	s_mov_b32 m0, s61
	s_addc_u32 s43, s43, 0
	global_load_lds_dwordx4 v[178:179], off
	v_lshl_add_u64 v[178:179], s[42:43], 0, v[162:163]
	s_mov_b32 m0, s64
	s_nop 0
	global_load_lds_dwordx4 v[178:179], off
	v_lshl_add_u64 v[178:179], s[42:43], 0, v[166:167]
	s_mov_b32 m0, s65
	s_nop 0
	global_load_lds_dwordx4 v[178:179], off
	v_lshl_add_u64 v[178:179], v[182:183], 0, s[16:17]
	s_mov_b32 m0, s62
	s_nop 0
	global_load_lds_dwordx4 v[178:179], off
	v_lshl_add_u64 v[178:179], v[184:185], 0, s[16:17]
	s_mov_b32 m0, s63
	s_nop 0
	global_load_lds_dwordx4 v[178:179], off
	s_waitcnt vmcnt(8)
	s_waitcnt lgkmcnt(0)
	s_barrier
	s_setprio 0
	s_waitcnt lgkmcnt(0)
	v_mfma_scale_f32_16x16x128_f8f6f4 v[86:89], v[2:9], v[200:207], v[86:89], v193, v194 op_sel_hi:[0,0,0]
	v_mfma_scale_f32_16x16x128_f8f6f4 v[82:85], v[10:17], v[200:207], v[82:85], v193, v194 op_sel_hi:[0,0,0]
	v_mfma_scale_f32_16x16x128_f8f6f4 v[70:73], v[2:9], v[208:215], v[70:73], v193, v194 op_sel_hi:[0,0,0]
	v_mfma_scale_f32_16x16x128_f8f6f4 v[58:61], v[10:17], v[208:215], v[58:61], v193, v194 op_sel_hi:[0,0,0]
	v_mfma_scale_f32_16x16x128_f8f6f4 v[66:69], v[2:9], v[216:223], v[66:69], v193, v194 op_sel_hi:[0,0,0]
	v_mfma_scale_f32_16x16x128_f8f6f4 v[54:57], v[10:17], v[216:223], v[54:57], v193, v194 op_sel_hi:[0,0,0]
	v_mfma_scale_f32_16x16x128_f8f6f4 v[46:49], v[2:9], v[224:231], v[46:49], v193, v194 op_sel_hi:[0,0,0]
	v_mfma_scale_f32_16x16x128_f8f6f4 v[38:41], v[10:17], v[224:231], v[38:41], v193, v194 op_sel_hi:[0,0,0]
	s_nop 0
	s_setprio 0
	v_mfma_scale_f32_16x16x128_f8f6f4 v[98:101], v[18:25], v[200:207], v[98:101], v193, v194 op_sel_hi:[0,0,0]
	v_mfma_scale_f32_16x16x128_f8f6f4 v[90:93], v[26:33], v[200:207], v[90:93], v193, v194 op_sel_hi:[0,0,0]
	v_mfma_scale_f32_16x16x128_f8f6f4 v[78:81], v[18:25], v[208:215], v[78:81], v193, v194 op_sel_hi:[0,0,0]
	v_mfma_scale_f32_16x16x128_f8f6f4 v[74:77], v[26:33], v[208:215], v[74:77], v193, v194 op_sel_hi:[0,0,0]
	v_mfma_scale_f32_16x16x128_f8f6f4 v[62:65], v[18:25], v[216:223], v[62:65], v193, v194 op_sel_hi:[0,0,0]
	v_mfma_scale_f32_16x16x128_f8f6f4 v[50:53], v[26:33], v[216:223], v[50:53], v193, v194 op_sel_hi:[0,0,0]
	v_mfma_scale_f32_16x16x128_f8f6f4 v[42:45], v[18:25], v[224:231], v[42:45], v193, v194 op_sel_hi:[0,0,0]
	v_mfma_scale_f32_16x16x128_f8f6f4 v[34:37], v[26:33], v[224:231], v[34:37], v193, v194 op_sel_hi:[0,0,0]
	s_setprio 1
	s_barrier
	s_add_i32 s72, s72, 2
	s_add_u32 s46, s46, 0x100
	s_addc_u32 s47, s47, 0
	s_add_u32 s6, s6, 0x100
	s_addc_u32 s7, s7, 0
	s_cmp_gt_u32 s72, 13
	s_cbranch_scc0 .LBB0_1242
	s_setprio 0
	s_and_b64 vcc, exec, s[18:19]
	s_cbranch_vccz .LBB0_1245
	s_barrier

; #define GAS __attribute__((address_space(1)))
; #define PG8_STAGE(bufoff, gbase, voff) do { _Pragma("unroll") for (int _i = 0; _i < 2; ++_i) \
;         __builtin_amdgcn_global_load_lds((const GAS unsigned*)((const GAS char*)(gbase) + (voff)[_i]), (LAS unsigned*)(lds + (bufoff) + ldsw + _i * 8192), 16, 0, 0); } while (0)
; #define PG8_LDA(dst, b, h) do { _Pragma("unroll") for (int m = 0; m < 4; ++m) { dst[m].lo = *(const LAS i32x4v*)(lds + PG8_SA(b, h) + (FP8 ? aoff8[0] : aoff) + m * 2048); dst[m].hi = *(const LAS i32x4v*)(lds + PG8_SA(b, h) + (FP8 ? aoff8[1] : aoff + 1024) + m * 2048); } } while (0)
; #define PG8_WAIT_V(n) asm volatile("s_waitcnt vmcnt(" #n ")" ::: "memory")
; #define PG8_BAR __builtin_amdgcn_s_barrier()
; template <class Epi, class Sched, bool GATHER, bool FP8 = false, bool UNI = false>
; __device__ __forceinline__ void gemm_phase(LAS unsigned char* lds, const Sched& S, const Epi& E) {
;     ...
;         for (int t = 0; t < nt; t += 2) {
;             const bool last = (t == nt - 2);
;             const GAS char* a1 = cA + (size_t)(t + 1) * 128;
;             const GAS char* a2 = last ? nA : cA + (size_t)(t + 2) * 128; const GAS char* b2 = last ? nB : cB + (size_t)(t + 2) * 128;
;             const GAS char* a3 = a2 + 128; const GAS char* b3 = b2 + 128;
;             const size_t hB2 = last ? hBn : hBc;
;             unsigned oa0[2], oa1[2], ob[2];
; #pragma unroll
;             for (int i = 0; i < 2; ++i) { if constexpr (UNI) { oa0[i] = aoc[0][i]; oa1[i] = aoc[1][i]; ob[i] = boc[i]; } else { oa0[i] = last ? aon[0][i] : aoc[0][i]; oa1[i] = last ? aon[1][i] : aoc[1][i]; ob[i] = last ? bon[i] : boc[i]; } }
;             PG8_LDB(B0, 0, 0); PG8_LDB(B1, 0, 1); PG8_SCHED; PG8_LDA(At, 0, 0); PG8_STAGE(PG8_SA(1, 1), a1, aoc[1]);
;             PG8_WAIT_V(8); PG8_WAIT_L(0); PG8_BAR; PG8_MMA(0, 0, At, B0); PG8_MMA(0, 1, At, B1); PG8_BAR; PG8_SCHED;
;             PG8_LDA(At, 0, 1); PG8_STAGE(PG8_SB(0, 0), b2, ob); PG8_STAGE(PG8_SB(0, 1), b2 + hB2, ob); PG8_STAGE(PG8_SA(0, 0), a2, oa0);
;             PG8_WAIT_V(8); PG8_WAIT_L(0); PG8_BAR; PG8_MMA(1, 0, At, B0); PG8_MMA(1, 1, At, B1); PG8_BAR; PG8_SCHED;
;             PG8_LDB(B0, 1, 0); PG8_LDB(B1, 1, 1); PG8_SCHED; PG8_LDA(At, 1, 0); PG8_STAGE(PG8_SA(0, 1), a2, oa1);
;             PG8_WAIT_V(8); PG8_WAIT_L(0); PG8_BAR; PG8_MMA(0, 0, At, B0); PG8_MMA(0, 1, At, B1); PG8_BAR; PG8_SCHED;
.LBB0_1558:
	s_add_u32 s84, s70, s78
	s_addc_u32 s85, s71, s79
	v_add_u32_e32 v2, s95, v179
	v_add_u32_e32 v3, s95, v203
	v_add_u32_e32 v6, s96, v179
	v_add_u32_e32 v14, s96, v203
	s_add_u32 s86, s84, 0x100
	ds_read_b128 v[18:21], v2
	ds_read_b128 v[26:29], v2 offset:2048
	ds_read_b128 v[22:25], v3
	ds_read_b128 v[30:33], v3 offset:2048
	ds_read_b128 v[2:5], v6
	ds_read_b128 v[10:13], v6 offset:2048
	ds_read_b128 v[6:9], v14
	ds_read_b128 v[14:17], v14 offset:2048
	s_addc_u32 s87, s85, 0
	s_add_u32 s2, s39, s78
	s_addc_u32 s63, s64, s79
	s_cmpk_eq_i32 s78, 0x700
	s_cselect_b64 vcc, -1, 0
	s_and_b64 s[84:85], vcc, exec
	v_cndmask_b32_e32 v162, v178, v210, vcc
	s_cselect_b32 s87, s77, s87
	s_cselect_b32 s86, s76, s86
	v_cndmask_b32_e32 v177, v176, v209, vcc
	v_cndmask_b32_e32 v244, v174, v208, vcc
	v_cndmask_b32_e32 v181, v180, v211, vcc
	s_cselect_b32 s85, s7, s63
	s_cselect_b32 s84, s6, s2
	v_lshl_add_u64 v[236:237], v[186:187], 0, s[78:79]
	s_add_i32 m0, s43, 0xc000
	ds_read_b128 v[188:191], v205
	ds_read_b128 v[212:215], v205 offset:2048
	ds_read_b128 v[192:195], v206
	ds_read_b128 v[216:219], v206 offset:2048
	ds_read_b128 v[220:223], v205 offset:4096
	ds_read_b128 v[228:231], v205 offset:6144
	ds_read_b128 v[224:227], v206 offset:4096
	ds_read_b128 v[232:235], v206 offset:6144
	global_load_lds_dwordx4 v[236:237], off
	v_lshl_add_u64 v[236:237], v[184:185], 0, s[78:79]
	s_add_i32 m0, s43, 0xe000
	s_nop 0
	global_load_lds_dwordx4 v[236:237], off
	s_waitcnt vmcnt(8)
	s_waitcnt lgkmcnt(0)
	s_barrier
	s_setprio 0
	s_waitcnt lgkmcnt(0)
	v_mfma_scale_f32_16x16x128_f8f6f4 v[134:137], v[18:25], v[188:195], v[134:137], v1, v196 op_sel_hi:[0,0,0]
	v_mfma_scale_f32_16x16x128_f8f6f4 v[130:133], v[26:33], v[188:195], v[130:133], v1, v196 op_sel_hi:[0,0,0]
	v_mfma_scale_f32_16x16x128_f8f6f4 v[126:129], v[18:25], v[212:219], v[126:129], v1, v196 op_sel_hi:[0,0,0]
	v_mfma_scale_f32_16x16x128_f8f6f4 v[122:125], v[26:33], v[212:219], v[122:125], v1, v196 op_sel_hi:[0,0,0]
	v_mfma_scale_f32_16x16x128_f8f6f4 v[118:121], v[18:25], v[220:227], v[118:121], v1, v196 op_sel_hi:[0,0,0]
	v_mfma_scale_f32_16x16x128_f8f6f4 v[114:117], v[26:33], v[220:227], v[114:117], v1, v196 op_sel_hi:[0,0,0]
	v_mfma_scale_f32_16x16x128_f8f6f4 v[110:113], v[18:25], v[228:235], v[110:113], v1, v196 op_sel_hi:[0,0,0]
	v_mfma_scale_f32_16x16x128_f8f6f4 v[106:109], v[26:33], v[228:235], v[106:109], v1, v196 op_sel_hi:[0,0,0]
	s_nop 0
	s_setprio 0
	v_mfma_scale_f32_16x16x128_f8f6f4 v[102:105], v[2:9], v[188:195], v[102:105], v1, v196 op_sel_hi:[0,0,0]
	v_mfma_scale_f32_16x16x128_f8f6f4 v[98:101], v[10:17], v[188:195], v[98:101], v1, v196 op_sel_hi:[0,0,0]
	v_mfma_scale_f32_16x16x128_f8f6f4 v[94:97], v[2:9], v[212:219], v[94:97], v1, v196 op_sel_hi:[0,0,0]
	v_mfma_scale_f32_16x16x128_f8f6f4 v[90:93], v[10:17], v[212:219], v[90:93], v1, v196 op_sel_hi:[0,0,0]
	v_mfma_scale_f32_16x16x128_f8f6f4 v[86:89], v[2:9], v[220:227], v[86:89], v1, v196 op_sel_hi:[0,0,0]
	v_mfma_scale_f32_16x16x128_f8f6f4 v[82:85], v[10:17], v[220:227], v[82:85], v1, v196 op_sel_hi:[0,0,0]
	v_mfma_scale_f32_16x16x128_f8f6f4 v[78:81], v[2:9], v[228:235], v[78:81], v1, v196 op_sel_hi:[0,0,0]
	v_mfma_scale_f32_16x16x128_f8f6f4 v[74:77], v[10:17], v[228:235], v[74:77], v1, v196 op_sel_hi:[0,0,0]
	s_setprio 1
	s_barrier
	s_mov_b32 m0, s8
	v_lshl_add_u64 v[188:189], s[84:85], 0, v[172:173]
	s_add_u32 vcc_lo, s84, 0x40000
	ds_read_b128 v[212:215], v205 offset:16384
	ds_read_b128 v[220:223], v205 offset:18432
	ds_read_b128 v[216:219], v206 offset:16384
	ds_read_b128 v[224:227], v206 offset:18432
	ds_read_b128 v[228:231], v205 offset:20480
	ds_read_b128 v[236:239], v205 offset:22528
	ds_read_b128 v[232:235], v206 offset:20480
	ds_read_b128 v[240:243], v206 offset:22528
	global_load_lds_dwordx4 v[188:189], off
	v_lshl_add_u64 v[190:191], s[84:85], 0, v[170:171]
	s_mov_b32 m0, s24
	s_addc_u32 vcc_hi, s85, 0
	global_load_lds_dwordx4 v[190:191], off
	v_lshl_add_u64 v[192:193], vcc, 0, v[172:173]
	s_mov_b32 m0, s9
	v_mov_b32_e32 v245, v163
	global_load_lds_dwordx4 v[192:193], off
	v_lshl_add_u64 v[192:193], vcc, 0, v[170:171]
	s_mov_b32 m0, s42
	v_lshl_add_u64 v[194:195], s[86:87], 0, v[162:163]
	global_load_lds_dwordx4 v[192:193], off
	s_mov_b32 m0, s43
	v_lshl_add_u64 v[192:193], s[86:87], 0, v[244:245]
	global_load_lds_dwordx4 v162, s[86:87]
	s_mov_b32 m0, s33
	s_nop 0
	global_load_lds_dwordx4 v244, s[86:87]
	s_waitcnt vmcnt(8)
	s_waitcnt lgkmcnt(0)
	s_barrier
	s_setprio 0
	s_waitcnt lgkmcnt(0)
	v_mfma_scale_f32_16x16x128_f8f6f4 v[70:73], v[18:25], v[212:219], v[70:73], v1, v196 op_sel_hi:[0,0,0]
	v_mfma_scale_f32_16x16x128_f8f6f4 v[66:69], v[26:33], v[212:219], v[66:69], v1, v196 op_sel_hi:[0,0,0]
	v_mfma_scale_f32_16x16x128_f8f6f4 v[62:65], v[18:25], v[220:227], v[62:65], v1, v196 op_sel_hi:[0,0,0]
	v_mfma_scale_f32_16x16x128_f8f6f4 v[58:61], v[26:33], v[220:227], v[58:61], v1, v196 op_sel_hi:[0,0,0]
	v_mfma_scale_f32_16x16x128_f8f6f4 v[54:57], v[18:25], v[228:235], v[54:57], v1, v196 op_sel_hi:[0,0,0]
	v_mfma_scale_f32_16x16x128_f8f6f4 v[50:53], v[26:33], v[228:235], v[50:53], v1, v196 op_sel_hi:[0,0,0]
	v_mfma_scale_f32_16x16x128_f8f6f4 v[46:49], v[18:25], v[236:243], v[46:49], v1, v196 op_sel_hi:[0,0,0]
	v_mfma_scale_f32_16x16x128_f8f6f4 v[42:45], v[26:33], v[236:243], v[42:45], v1, v196 op_sel_hi:[0,0,0]
	s_nop 0
	s_setprio 0
	v_mfma_scale_f32_16x16x128_f8f6f4 v[38:41], v[2:9], v[212:219], v[38:41], v1, v196 op_sel_hi:[0,0,0]
	v_mfma_scale_f32_16x16x128_f8f6f4 v[34:37], v[10:17], v[212:219], v[34:37], v1, v196 op_sel_hi:[0,0,0]
	v_mfma_scale_f32_16x16x128_f8f6f4 v[138:141], v[2:9], v[220:227], v[138:141], v1, v196 op_sel_hi:[0,0,0]
	v_mfma_scale_f32_16x16x128_f8f6f4 v[142:145], v[10:17], v[220:227], v[142:145], v1, v196 op_sel_hi:[0,0,0]
	v_mfma_scale_f32_16x16x128_f8f6f4 v[146:149], v[2:9], v[228:235], v[146:149], v1, v196 op_sel_hi:[0,0,0]
	v_mfma_scale_f32_16x16x128_f8f6f4 v[150:153], v[10:17], v[228:235], v[150:153], v1, v196 op_sel_hi:[0,0,0]
	v_mfma_scale_f32_16x16x128_f8f6f4 v[154:157], v[2:9], v[236:243], v[154:157], v1, v196 op_sel_hi:[0,0,0]
	v_mfma_scale_f32_16x16x128_f8f6f4 v[158:161], v[10:17], v[236:243], v[158:161], v1, v196 op_sel_hi:[0,0,0]
	s_setprio 1
	s_barrier
; #define PG8_STAGE(bufoff, gbase, voff) do { _Pragma("unroll") for (int _i = 0; _i < 2; ++_i) \
;         __builtin_amdgcn_global_load_lds((const GAS unsigned*)((const GAS char*)(gbase) + (voff)[_i]), (LAS unsigned*)(lds + (bufoff) + ldsw + _i * 8192), 16, 0, 0); } while (0)
; #define PG8_LDA(dst, b, h) do { _Pragma("unroll") for (int m = 0; m < 4; ++m) { dst[m].lo = *(const LAS i32x4v*)(lds + PG8_SA(b, h) + (FP8 ? aoff8[0] : aoff) + m * 2048); dst[m].hi = *(const LAS i32x4v*)(lds + PG8_SA(b, h) + (FP8 ? aoff8[1] : aoff + 1024) + m * 2048); } } while (0)
; #define PG8_LDB(dst, b, h) do { _Pragma("unroll") for (int n = 0; n < 2; ++n) { dst[n].lo = *(const LAS i32x4v*)(lds + PG8_SB(b, h) + (FP8 ? boff8[0] : boff) + n * 2048); dst[n].hi = *(const LAS i32x4v*)(lds + PG8_SB(b, h) + (FP8 ? boff8[1] : boff + 1024) + n * 2048); } } while (0)
; #define PG8_WAIT_V(n) asm volatile("s_waitcnt vmcnt(" #n ")" ::: "memory")
; #define PG8_WAIT_L(n) asm volatile("s_waitcnt lgkmcnt(" #n ")" ::: "memory")
; #define PG8_BAR __builtin_amdgcn_s_barrier()
; #define PG8_SCHED __builtin_amdgcn_sched_barrier(0)
; template <class Epi, class Sched, bool GATHER, bool FP8 = false, bool UNI = false>
; __device__ __forceinline__ void gemm_phase(LAS unsigned char* lds, const Sched& S, const Epi& E) {
;     ...
;             PG8_LDB(B0, 1, 0); PG8_LDB(B1, 1, 1); PG8_SCHED; PG8_LDA(At, 1, 0); PG8_STAGE(PG8_SA(0, 1), a2, oa1);
;             PG8_WAIT_V(8); PG8_WAIT_L(0); PG8_BAR; PG8_MMA(0, 0, At, B0); PG8_MMA(0, 1, At, B1); PG8_BAR; PG8_SCHED;
;             PG8_LDA(At, 1, 1); PG8_STAGE(PG8_SB(1, 0), b3, ob); PG8_STAGE(PG8_SB(1, 1), b3 + hB2, ob); PG8_STAGE(PG8_SA(1, 0), a3, oa0);
;             PG8_WAIT_V(8); PG8_WAIT_L(0); PG8_BAR; PG8_MMA(1, 0, At, B0); PG8_MMA(1, 1, At, B1); PG8_BAR; PG8_SCHED;
;         }
;         if (wr == 0) PG8_BAR;
	v_add_u32_e32 v6, s97, v179
	v_add_u32_e32 v14, s97, v203
	v_add_u32_e32 v22, s58, v179
	v_add_u32_e32 v30, s58, v203
	ds_read_b128 v[2:5], v6
	ds_read_b128 v[10:13], v6 offset:2048
	ds_read_b128 v[6:9], v14
	ds_read_b128 v[14:17], v14 offset:2048
	ds_read_b128 v[18:21], v22
	ds_read_b128 v[26:29], v22 offset:2048
	ds_read_b128 v[22:25], v30
	ds_read_b128 v[30:33], v30 offset:2048
	s_mov_b32 m0, s10
	ds_read_b128 v[212:215], v205 offset:32768
	ds_read_b128 v[220:223], v205 offset:34816
	ds_read_b128 v[216:219], v206 offset:32768
	ds_read_b128 v[224:227], v206 offset:34816
	ds_read_b128 v[228:231], v205 offset:36864
	ds_read_b128 v[236:239], v205 offset:38912
	ds_read_b128 v[232:235], v206 offset:36864
	ds_read_b128 v[240:243], v206 offset:38912
	global_load_lds_dwordx4 v177, s[86:87]
	s_mov_b32 m0, s11
	s_nop 0
	global_load_lds_dwordx4 v181, s[86:87]
	s_waitcnt vmcnt(8)
	s_waitcnt lgkmcnt(0)
	s_barrier
	s_setprio 0
	s_waitcnt lgkmcnt(0)
	v_mfma_scale_f32_16x16x128_f8f6f4 v[134:137], v[2:9], v[212:219], v[134:137], v1, v196 op_sel_hi:[0,0,0]
	v_mfma_scale_f32_16x16x128_f8f6f4 v[130:133], v[10:17], v[212:219], v[130:133], v1, v196 op_sel_hi:[0,0,0]
	v_mfma_scale_f32_16x16x128_f8f6f4 v[126:129], v[2:9], v[220:227], v[126:129], v1, v196 op_sel_hi:[0,0,0]
	v_mfma_scale_f32_16x16x128_f8f6f4 v[122:125], v[10:17], v[220:227], v[122:125], v1, v196 op_sel_hi:[0,0,0]
	v_mfma_scale_f32_16x16x128_f8f6f4 v[118:121], v[2:9], v[228:235], v[118:121], v1, v196 op_sel_hi:[0,0,0]
	v_mfma_scale_f32_16x16x128_f8f6f4 v[114:117], v[10:17], v[228:235], v[114:117], v1, v196 op_sel_hi:[0,0,0]
	v_mfma_scale_f32_16x16x128_f8f6f4 v[110:113], v[2:9], v[236:243], v[110:113], v1, v196 op_sel_hi:[0,0,0]
	v_mfma_scale_f32_16x16x128_f8f6f4 v[106:109], v[10:17], v[236:243], v[106:109], v1, v196 op_sel_hi:[0,0,0]
	s_nop 0
	s_setprio 0
	v_mfma_scale_f32_16x16x128_f8f6f4 v[102:105], v[18:25], v[212:219], v[102:105], v1, v196 op_sel_hi:[0,0,0]
	v_mfma_scale_f32_16x16x128_f8f6f4 v[98:101], v[26:33], v[212:219], v[98:101], v1, v196 op_sel_hi:[0,0,0]
	v_mfma_scale_f32_16x16x128_f8f6f4 v[94:97], v[18:25], v[220:227], v[94:97], v1, v196 op_sel_hi:[0,0,0]
	v_mfma_scale_f32_16x16x128_f8f6f4 v[90:93], v[26:33], v[220:227], v[90:93], v1, v196 op_sel_hi:[0,0,0]
	v_mfma_scale_f32_16x16x128_f8f6f4 v[86:89], v[18:25], v[228:235], v[86:89], v1, v196 op_sel_hi:[0,0,0]
	v_mfma_scale_f32_16x16x128_f8f6f4 v[82:85], v[26:33], v[228:235], v[82:85], v1, v196 op_sel_hi:[0,0,0]
	v_mfma_scale_f32_16x16x128_f8f6f4 v[78:81], v[18:25], v[236:243], v[78:81], v1, v196 op_sel_hi:[0,0,0]
	v_mfma_scale_f32_16x16x128_f8f6f4 v[74:77], v[26:33], v[236:243], v[74:77], v1, v196 op_sel_hi:[0,0,0]
	s_setprio 1
	s_barrier
	s_mov_b32 m0, s40
	v_lshl_add_u64 v[188:189], v[188:189], 0, s[66:67]
	s_add_u32 s84, s84, 0x40080
	ds_read_b128 v[212:215], v205 offset:49152
	ds_read_b128 v[220:223], v205 offset:51200
	ds_read_b128 v[216:219], v206 offset:49152
	ds_read_b128 v[224:227], v206 offset:51200
	ds_read_b128 v[228:231], v205 offset:53248
	ds_read_b128 v[236:239], v205 offset:55296
	ds_read_b128 v[232:235], v206 offset:53248
	ds_read_b128 v[240:243], v206 offset:55296
	global_load_lds_dwordx4 v[188:189], off
	v_lshl_add_u64 v[188:189], v[190:191], 0, s[66:67]
	s_mov_b32 m0, s41
	s_addc_u32 s85, s85, 0
	global_load_lds_dwordx4 v[188:189], off
	v_lshl_add_u64 v[188:189], s[84:85], 0, v[172:173]
	s_mov_b32 m0, s61
	s_nop 0
	global_load_lds_dwordx4 v[188:189], off
	v_lshl_add_u64 v[188:189], s[84:85], 0, v[170:171]
	s_mov_b32 m0, s50
	s_nop 0
	global_load_lds_dwordx4 v[188:189], off
	v_lshl_add_u64 v[188:189], v[194:195], 0, s[66:67]
	s_mov_b32 m0, s49
	s_nop 0
	global_load_lds_dwordx4 v[188:189], off
	v_lshl_add_u64 v[188:189], v[192:193], 0, s[66:67]
	s_mov_b32 m0, s25
	s_nop 0
	global_load_lds_dwordx4 v[188:189], off
	s_waitcnt vmcnt(8)
	s_waitcnt lgkmcnt(0)
	s_barrier
	s_setprio 0
	s_waitcnt lgkmcnt(0)
	v_mfma_scale_f32_16x16x128_f8f6f4 v[70:73], v[2:9], v[212:219], v[70:73], v1, v196 op_sel_hi:[0,0,0]
	v_mfma_scale_f32_16x16x128_f8f6f4 v[66:69], v[10:17], v[212:219], v[66:69], v1, v196 op_sel_hi:[0,0,0]
	v_mfma_scale_f32_16x16x128_f8f6f4 v[62:65], v[2:9], v[220:227], v[62:65], v1, v196 op_sel_hi:[0,0,0]
	v_mfma_scale_f32_16x16x128_f8f6f4 v[58:61], v[10:17], v[220:227], v[58:61], v1, v196 op_sel_hi:[0,0,0]
	v_mfma_scale_f32_16x16x128_f8f6f4 v[54:57], v[2:9], v[228:235], v[54:57], v1, v196 op_sel_hi:[0,0,0]
	v_mfma_scale_f32_16x16x128_f8f6f4 v[50:53], v[10:17], v[228:235], v[50:53], v1, v196 op_sel_hi:[0,0,0]
	v_mfma_scale_f32_16x16x128_f8f6f4 v[46:49], v[2:9], v[236:243], v[46:49], v1, v196 op_sel_hi:[0,0,0]
	v_mfma_scale_f32_16x16x128_f8f6f4 v[42:45], v[10:17], v[236:243], v[42:45], v1, v196 op_sel_hi:[0,0,0]
	s_nop 0
	s_setprio 0
	v_mfma_scale_f32_16x16x128_f8f6f4 v[38:41], v[18:25], v[212:219], v[38:41], v1, v196 op_sel_hi:[0,0,0]
	v_mfma_scale_f32_16x16x128_f8f6f4 v[34:37], v[26:33], v[212:219], v[34:37], v1, v196 op_sel_hi:[0,0,0]
	v_mfma_scale_f32_16x16x128_f8f6f4 v[138:141], v[18:25], v[220:227], v[138:141], v1, v196 op_sel_hi:[0,0,0]
	v_mfma_scale_f32_16x16x128_f8f6f4 v[142:145], v[26:33], v[220:227], v[142:145], v1, v196 op_sel_hi:[0,0,0]
	v_mfma_scale_f32_16x16x128_f8f6f4 v[146:149], v[18:25], v[228:235], v[146:149], v1, v196 op_sel_hi:[0,0,0]
	v_mfma_scale_f32_16x16x128_f8f6f4 v[150:153], v[26:33], v[228:235], v[150:153], v1, v196 op_sel_hi:[0,0,0]
	v_mfma_scale_f32_16x16x128_f8f6f4 v[154:157], v[18:25], v[236:243], v[154:157], v1, v196 op_sel_hi:[0,0,0]
	v_mfma_scale_f32_16x16x128_f8f6f4 v[158:161], v[26:33], v[236:243], v[158:161], v1, v196 op_sel_hi:[0,0,0]
	s_setprio 1
	s_barrier
	s_add_i32 s65, s65, 2
	s_add_u32 s78, s78, 0x100
	s_addc_u32 s79, s79, 0
	s_cmp_gt_u32 s65, 13
	s_cbranch_scc0 .LBB0_1558
	s_setprio 0
	s_and_b64 vcc, exec, s[74:75]
	s_cbranch_vccz .LBB0_1561
	s_barrier

; #define GAS __attribute__((address_space(1)))
; #define PG8_STAGE(bufoff, gbase, voff) do { _Pragma("unroll") for (int _i = 0; _i < 2; ++_i) \
;         __builtin_amdgcn_global_load_lds((const GAS unsigned*)((const GAS char*)(gbase) + (voff)[_i]), (LAS unsigned*)(lds + (bufoff) + ldsw + _i * 8192), 16, 0, 0); } while (0)
; #define PG8_LDA(dst, b, h) do { _Pragma("unroll") for (int m = 0; m < 4; ++m) { dst[m].lo = *(const LAS i32x4v*)(lds + PG8_SA(b, h) + (FP8 ? aoff8[0] : aoff) + m * 2048); dst[m].hi = *(const LAS i32x4v*)(lds + PG8_SA(b, h) + (FP8 ? aoff8[1] : aoff + 1024) + m * 2048); } } while (0)
; #define PG8_WAIT_V(n) asm volatile("s_waitcnt vmcnt(" #n ")" ::: "memory")
; #define PG8_BAR __builtin_amdgcn_s_barrier()
; template <class Epi, class Sched, bool GATHER, bool FP8 = false, bool UNI = false>
; __device__ __forceinline__ void gemm_phase(LAS unsigned char* lds, const Sched& S, const Epi& E) {
;     ...
;         for (int t = 0; t < nt; t += 2) {
;             const bool last = (t == nt - 2);
;             const GAS char* a1 = cA + (size_t)(t + 1) * 128;
;             const GAS char* a2 = last ? nA : cA + (size_t)(t + 2) * 128; const GAS char* b2 = last ? nB : cB + (size_t)(t + 2) * 128;
;             const GAS char* a3 = a2 + 128; const GAS char* b3 = b2 + 128;
;             const size_t hB2 = last ? hBn : hBc;
;             unsigned oa0[2], oa1[2], ob[2];
; #pragma unroll
;             for (int i = 0; i < 2; ++i) { if constexpr (UNI) { oa0[i] = aoc[0][i]; oa1[i] = aoc[1][i]; ob[i] = boc[i]; } else { oa0[i] = last ? aon[0][i] : aoc[0][i]; oa1[i] = last ? aon[1][i] : aoc[1][i]; ob[i] = last ? bon[i] : boc[i]; } }
;             PG8_LDB(B0, 0, 0); PG8_LDB(B1, 0, 1); PG8_SCHED; PG8_LDA(At, 0, 0); PG8_STAGE(PG8_SA(1, 1), a1, aoc[1]);
;             PG8_WAIT_V(8); PG8_WAIT_L(0); PG8_BAR; PG8_MMA(0, 0, At, B0); PG8_MMA(0, 1, At, B1); PG8_BAR; PG8_SCHED;
;             PG8_LDA(At, 0, 1); PG8_STAGE(PG8_SB(0, 0), b2, ob); PG8_STAGE(PG8_SB(0, 1), b2 + hB2, ob); PG8_STAGE(PG8_SA(0, 0), a2, oa0);
;             PG8_WAIT_V(8); PG8_WAIT_L(0); PG8_BAR; PG8_MMA(1, 0, At, B0); PG8_MMA(1, 1, At, B1); PG8_BAR; PG8_SCHED;
;             PG8_LDB(B0, 1, 0); PG8_LDB(B1, 1, 1); PG8_SCHED; PG8_LDA(At, 1, 0); PG8_STAGE(PG8_SA(0, 1), a2, oa1);
;             PG8_WAIT_V(8); PG8_WAIT_L(0); PG8_BAR; PG8_MMA(0, 0, At, B0); PG8_MMA(0, 1, At, B1); PG8_BAR; PG8_SCHED;
.LBB0_1961:
	s_add_u32 s40, s20, s36
	s_addc_u32 s41, s21, 0
	s_add_u32 s37, s40, 0x100
	s_addc_u32 s38, s41, 0
	s_and_b64 s[34:35], s[30:31], exec
	ds_read_b128 v[18:21], v1
	ds_read_b128 v[26:29], v1 offset:2048
	ds_read_b128 v[22:25], v186
	ds_read_b128 v[30:33], v186 offset:2048
	s_waitcnt lgkmcnt(0)
	ds_read_b128 v[2:5], v187
	ds_read_b128 v[10:13], v187 offset:2048
	ds_read_b128 v[6:9], v188
	ds_read_b128 v[14:17], v188 offset:2048
	s_cselect_b32 s34, s16, s37
	s_cselect_b32 s35, s17, s38
	s_add_u32 s36, s22, s36
	s_addc_u32 s37, s23, 0
	s_add_u32 s36, s36, 0x100
	s_addc_u32 s37, s37, 0
	s_and_b64 s[30:31], s[30:31], exec
	s_cselect_b32 s37, s19, s37
	s_cselect_b32 s36, s18, s36
	s_add_i32 m0, s45, 0xc000
	s_add_i32 s70, s45, 0xe000
	s_add_u32 s38, s36, 0x4000
	s_addc_u32 s39, s37, 0
	s_add_u32 s30, s36, 0x4080
	s_addc_u32 s31, s37, 0
	v_lshl_add_u64 v[224:225], s[40:41], 0, v[166:167]
	v_lshl_add_u64 v[224:225], v[224:225], 0, s[10:11]
	ds_read_b128 v[178:181], v189
	ds_read_b128 v[200:203], v189 offset:2048
	ds_read_b128 v[182:185], v190
	ds_read_b128 v[204:207], v190 offset:2048
	ds_read_b128 v[208:211], v189 offset:4096
	ds_read_b128 v[216:219], v189 offset:6144
	ds_read_b128 v[212:215], v190 offset:4096
	ds_read_b128 v[220:223], v190 offset:6144
	global_load_lds_dwordx4 v[224:225], off
	v_lshl_add_u64 v[224:225], s[40:41], 0, v[172:173]
	v_lshl_add_u64 v[224:225], v[224:225], 0, s[10:11]
	s_mov_b32 m0, s70
	s_nop 0
	global_load_lds_dwordx4 v[224:225], off
	s_waitcnt vmcnt(8)
	s_waitcnt lgkmcnt(0)
	s_barrier
	s_setprio 0
	s_waitcnt lgkmcnt(0)
	v_mfma_scale_f32_16x16x128_f8f6f4 v[158:161], v[18:25], v[178:185], v[158:161], v191, v192 op_sel_hi:[0,0,0]
	v_mfma_scale_f32_16x16x128_f8f6f4 v[154:157], v[26:33], v[178:185], v[154:157], v191, v192 op_sel_hi:[0,0,0]
	v_mfma_scale_f32_16x16x128_f8f6f4 v[142:145], v[18:25], v[200:207], v[142:145], v191, v192 op_sel_hi:[0,0,0]
	v_mfma_scale_f32_16x16x128_f8f6f4 v[138:141], v[26:33], v[200:207], v[138:141], v191, v192 op_sel_hi:[0,0,0]
	v_mfma_scale_f32_16x16x128_f8f6f4 v[126:129], v[18:25], v[208:215], v[126:129], v191, v192 op_sel_hi:[0,0,0]
	v_mfma_scale_f32_16x16x128_f8f6f4 v[122:125], v[26:33], v[208:215], v[122:125], v191, v192 op_sel_hi:[0,0,0]
	v_mfma_scale_f32_16x16x128_f8f6f4 v[106:109], v[18:25], v[216:223], v[106:109], v191, v192 op_sel_hi:[0,0,0]
	v_mfma_scale_f32_16x16x128_f8f6f4 v[98:101], v[26:33], v[216:223], v[98:101], v191, v192 op_sel_hi:[0,0,0]
	s_nop 0
	s_setprio 0
	v_mfma_scale_f32_16x16x128_f8f6f4 v[150:153], v[2:9], v[178:185], v[150:153], v191, v192 op_sel_hi:[0,0,0]
	v_mfma_scale_f32_16x16x128_f8f6f4 v[146:149], v[10:17], v[178:185], v[146:149], v191, v192 op_sel_hi:[0,0,0]
	v_mfma_scale_f32_16x16x128_f8f6f4 v[134:137], v[2:9], v[200:207], v[134:137], v191, v192 op_sel_hi:[0,0,0]
	v_mfma_scale_f32_16x16x128_f8f6f4 v[130:133], v[10:17], v[200:207], v[130:133], v191, v192 op_sel_hi:[0,0,0]
	v_mfma_scale_f32_16x16x128_f8f6f4 v[118:121], v[2:9], v[208:215], v[118:121], v191, v192 op_sel_hi:[0,0,0]
	v_mfma_scale_f32_16x16x128_f8f6f4 v[114:117], v[10:17], v[208:215], v[114:117], v191, v192 op_sel_hi:[0,0,0]
	v_mfma_scale_f32_16x16x128_f8f6f4 v[86:89], v[2:9], v[216:223], v[86:89], v191, v192 op_sel_hi:[0,0,0]
	v_mfma_scale_f32_16x16x128_f8f6f4 v[82:85], v[10:17], v[216:223], v[82:85], v191, v192 op_sel_hi:[0,0,0]
	s_setprio 1
	s_barrier
	s_mov_b32 m0, s33
	v_lshl_add_u64 v[178:179], s[36:37], 0, v[162:163]
	ds_read_b128 v[200:203], v189 offset:16384
	ds_read_b128 v[208:211], v189 offset:18432
	ds_read_b128 v[204:207], v190 offset:16384
	ds_read_b128 v[212:215], v190 offset:18432
	ds_read_b128 v[216:219], v189 offset:20480
	ds_read_b128 v[224:227], v189 offset:22528
	ds_read_b128 v[220:223], v190 offset:20480
	ds_read_b128 v[228:231], v190 offset:22528
	global_load_lds_dwordx4 v[178:179], off
	v_lshl_add_u64 v[180:181], s[36:37], 0, v[168:169]
	s_mov_b32 m0, s42
	v_lshl_add_u64 v[182:183], s[38:39], 0, v[162:163]
	global_load_lds_dwordx4 v[180:181], off
	s_mov_b32 m0, s43
	v_lshl_add_u64 v[184:185], s[34:35], 0, v[170:171]
	global_load_lds_dwordx4 v[182:183], off
	v_lshl_add_u64 v[182:183], s[38:39], 0, v[168:169]
	s_mov_b32 m0, s44
	s_nop 0
	global_load_lds_dwordx4 v[182:183], off
	v_lshl_add_u64 v[182:183], s[34:35], 0, v[164:165]
	s_mov_b32 m0, s45
	s_nop 0
	global_load_lds_dwordx4 v[182:183], off
	s_mov_b32 m0, s46
	s_nop 0
	global_load_lds_dwordx4 v[184:185], off
	s_waitcnt vmcnt(8)
	s_waitcnt lgkmcnt(0)
	s_barrier
	s_setprio 0
	s_waitcnt lgkmcnt(0)
	v_mfma_scale_f32_16x16x128_f8f6f4 v[70:73], v[18:25], v[200:207], v[70:73], v191, v192 op_sel_hi:[0,0,0]
	v_mfma_scale_f32_16x16x128_f8f6f4 v[66:69], v[26:33], v[200:207], v[66:69], v191, v192 op_sel_hi:[0,0,0]
	v_mfma_scale_f32_16x16x128_f8f6f4 v[38:41], v[18:25], v[208:215], v[38:41], v191, v192 op_sel_hi:[0,0,0]
	v_mfma_scale_f32_16x16x128_f8f6f4 v[34:37], v[26:33], v[208:215], v[34:37], v191, v192 op_sel_hi:[0,0,0]
	v_mfma_scale_f32_16x16x128_f8f6f4 v[54:57], v[18:25], v[216:223], v[54:57], v191, v192 op_sel_hi:[0,0,0]
	v_mfma_scale_f32_16x16x128_f8f6f4 v[62:65], v[26:33], v[216:223], v[62:65], v191, v192 op_sel_hi:[0,0,0]
	v_mfma_scale_f32_16x16x128_f8f6f4 v[42:45], v[18:25], v[224:231], v[42:45], v191, v192 op_sel_hi:[0,0,0]
	v_mfma_scale_f32_16x16x128_f8f6f4 v[46:49], v[26:33], v[224:231], v[46:49], v191, v192 op_sel_hi:[0,0,0]
	s_nop 0
	s_setprio 0
	v_mfma_scale_f32_16x16x128_f8f6f4 v[102:105], v[2:9], v[200:207], v[102:105], v191, v192 op_sel_hi:[0,0,0]
	v_mfma_scale_f32_16x16x128_f8f6f4 v[110:113], v[10:17], v[200:207], v[110:113], v191, v192 op_sel_hi:[0,0,0]
	v_mfma_scale_f32_16x16x128_f8f6f4 v[90:93], v[2:9], v[208:215], v[90:93], v191, v192 op_sel_hi:[0,0,0]
	v_mfma_scale_f32_16x16x128_f8f6f4 v[94:97], v[10:17], v[208:215], v[94:97], v191, v192 op_sel_hi:[0,0,0]
	v_mfma_scale_f32_16x16x128_f8f6f4 v[74:77], v[2:9], v[216:223], v[74:77], v191, v192 op_sel_hi:[0,0,0]
	v_mfma_scale_f32_16x16x128_f8f6f4 v[78:81], v[10:17], v[216:223], v[78:81], v191, v192 op_sel_hi:[0,0,0]
	v_mfma_scale_f32_16x16x128_f8f6f4 v[50:53], v[2:9], v[224:231], v[50:53], v191, v192 op_sel_hi:[0,0,0]
	v_mfma_scale_f32_16x16x128_f8f6f4 v[58:61], v[10:17], v[224:231], v[58:61], v191, v192 op_sel_hi:[0,0,0]
	s_setprio 1
	s_barrier
; #define PG8_STAGE(bufoff, gbase, voff) do { _Pragma("unroll") for (int _i = 0; _i < 2; ++_i) \
;         __builtin_amdgcn_global_load_lds((const GAS unsigned*)((const GAS char*)(gbase) + (voff)[_i]), (LAS unsigned*)(lds + (bufoff) + ldsw + _i * 8192), 16, 0, 0); } while (0)
; #define PG8_LDA(dst, b, h) do { _Pragma("unroll") for (int m = 0; m < 4; ++m) { dst[m].lo = *(const LAS i32x4v*)(lds + PG8_SA(b, h) + (FP8 ? aoff8[0] : aoff) + m * 2048); dst[m].hi = *(const LAS i32x4v*)(lds + PG8_SA(b, h) + (FP8 ? aoff8[1] : aoff + 1024) + m * 2048); } } while (0)
; #define PG8_LDB(dst, b, h) do { _Pragma("unroll") for (int n = 0; n < 2; ++n) { dst[n].lo = *(const LAS i32x4v*)(lds + PG8_SB(b, h) + (FP8 ? boff8[0] : boff) + n * 2048); dst[n].hi = *(const LAS i32x4v*)(lds + PG8_SB(b, h) + (FP8 ? boff8[1] : boff + 1024) + n * 2048); } } while (0)
; #define PG8_WAIT_V(n) asm volatile("s_waitcnt vmcnt(" #n ")" ::: "memory")
; #define PG8_WAIT_L(n) asm volatile("s_waitcnt lgkmcnt(" #n ")" ::: "memory")
; #define PG8_BAR __builtin_amdgcn_s_barrier()
; #define PG8_SCHED __builtin_amdgcn_sched_barrier(0)
; template <class Epi, class Sched, bool GATHER, bool FP8 = false, bool UNI = false>
; __device__ __forceinline__ void gemm_phase(LAS unsigned char* lds, const Sched& S, const Epi& E) {
;     ...
;             PG8_LDB(B0, 1, 0); PG8_LDB(B1, 1, 1); PG8_SCHED; PG8_LDA(At, 1, 0); PG8_STAGE(PG8_SA(0, 1), a2, oa1);
;             PG8_WAIT_V(8); PG8_WAIT_L(0); PG8_BAR; PG8_MMA(0, 0, At, B0); PG8_MMA(0, 1, At, B1); PG8_BAR; PG8_SCHED;
;             PG8_LDA(At, 1, 1); PG8_STAGE(PG8_SB(1, 0), b3, ob); PG8_STAGE(PG8_SB(1, 1), b3 + hB2, ob); PG8_STAGE(PG8_SA(1, 0), a3, oa0);
;             PG8_WAIT_V(8); PG8_WAIT_L(0); PG8_BAR; PG8_MMA(1, 0, At, B0); PG8_MMA(1, 1, At, B1); PG8_BAR; PG8_SCHED;
;         }
;         if (wr == 0) PG8_BAR;
	ds_read_b128 v[2:5], v193
	ds_read_b128 v[10:13], v193 offset:2048
	ds_read_b128 v[6:9], v194
	ds_read_b128 v[14:17], v194 offset:2048
	ds_read_b128 v[18:21], v195
	ds_read_b128 v[26:29], v195 offset:2048
	ds_read_b128 v[22:25], v196
	ds_read_b128 v[30:33], v196 offset:2048
	s_mov_b32 m0, s47
	v_lshl_add_u64 v[232:233], s[34:35], 0, v[166:167]
	ds_read_b128 v[200:203], v189 offset:32768
	ds_read_b128 v[208:211], v189 offset:34816
	ds_read_b128 v[204:207], v190 offset:32768
	ds_read_b128 v[212:215], v190 offset:34816
	ds_read_b128 v[216:219], v189 offset:36864
	ds_read_b128 v[224:227], v189 offset:38912
	ds_read_b128 v[220:223], v190 offset:36864
	ds_read_b128 v[228:231], v190 offset:38912
	global_load_lds_dwordx4 v[232:233], off
	v_lshl_add_u64 v[232:233], s[34:35], 0, v[172:173]
	s_mov_b32 m0, s48
	s_nop 0
	global_load_lds_dwordx4 v[232:233], off
	s_waitcnt vmcnt(8)
	s_waitcnt lgkmcnt(0)
	s_barrier
	s_setprio 0
	s_waitcnt lgkmcnt(0)
	v_mfma_scale_f32_16x16x128_f8f6f4 v[158:161], v[2:9], v[200:207], v[158:161], v191, v192 op_sel_hi:[0,0,0]
	v_mfma_scale_f32_16x16x128_f8f6f4 v[154:157], v[10:17], v[200:207], v[154:157], v191, v192 op_sel_hi:[0,0,0]
	v_mfma_scale_f32_16x16x128_f8f6f4 v[142:145], v[2:9], v[208:215], v[142:145], v191, v192 op_sel_hi:[0,0,0]
	v_mfma_scale_f32_16x16x128_f8f6f4 v[138:141], v[10:17], v[208:215], v[138:141], v191, v192 op_sel_hi:[0,0,0]
	v_mfma_scale_f32_16x16x128_f8f6f4 v[126:129], v[2:9], v[216:223], v[126:129], v191, v192 op_sel_hi:[0,0,0]
	v_mfma_scale_f32_16x16x128_f8f6f4 v[122:125], v[10:17], v[216:223], v[122:125], v191, v192 op_sel_hi:[0,0,0]
	v_mfma_scale_f32_16x16x128_f8f6f4 v[106:109], v[2:9], v[224:231], v[106:109], v191, v192 op_sel_hi:[0,0,0]
	v_mfma_scale_f32_16x16x128_f8f6f4 v[98:101], v[10:17], v[224:231], v[98:101], v191, v192 op_sel_hi:[0,0,0]
	s_nop 0
	s_setprio 0
	v_mfma_scale_f32_16x16x128_f8f6f4 v[150:153], v[18:25], v[200:207], v[150:153], v191, v192 op_sel_hi:[0,0,0]
	v_mfma_scale_f32_16x16x128_f8f6f4 v[146:149], v[26:33], v[200:207], v[146:149], v191, v192 op_sel_hi:[0,0,0]
	v_mfma_scale_f32_16x16x128_f8f6f4 v[134:137], v[18:25], v[208:215], v[134:137], v191, v192 op_sel_hi:[0,0,0]
	v_mfma_scale_f32_16x16x128_f8f6f4 v[130:133], v[26:33], v[208:215], v[130:133], v191, v192 op_sel_hi:[0,0,0]
	v_mfma_scale_f32_16x16x128_f8f6f4 v[118:121], v[18:25], v[216:223], v[118:121], v191, v192 op_sel_hi:[0,0,0]
	v_mfma_scale_f32_16x16x128_f8f6f4 v[114:117], v[26:33], v[216:223], v[114:117], v191, v192 op_sel_hi:[0,0,0]
	v_mfma_scale_f32_16x16x128_f8f6f4 v[86:89], v[18:25], v[224:231], v[86:89], v191, v192 op_sel_hi:[0,0,0]
	v_mfma_scale_f32_16x16x128_f8f6f4 v[82:85], v[26:33], v[224:231], v[82:85], v191, v192 op_sel_hi:[0,0,0]
	s_setprio 1
	s_barrier
	s_mov_b32 m0, s50
	v_lshl_add_u64 v[178:179], v[178:179], 0, s[10:11]
	ds_read_b128 v[200:203], v189 offset:49152
	ds_read_b128 v[208:211], v189 offset:51200
	ds_read_b128 v[204:207], v190 offset:49152
	ds_read_b128 v[212:215], v190 offset:51200
	ds_read_b128 v[216:219], v189 offset:53248
	ds_read_b128 v[224:227], v189 offset:55296
	ds_read_b128 v[220:223], v190 offset:53248
	ds_read_b128 v[228:231], v190 offset:55296
	global_load_lds_dwordx4 v[178:179], off
	v_lshl_add_u64 v[178:179], v[180:181], 0, s[10:11]
	s_mov_b32 m0, s51
	s_nop 0
	global_load_lds_dwordx4 v[178:179], off
	v_lshl_add_u64 v[178:179], s[30:31], 0, v[162:163]
	s_mov_b32 m0, s58
	s_nop 0
	global_load_lds_dwordx4 v[178:179], off
	v_lshl_add_u64 v[178:179], s[30:31], 0, v[168:169]
	s_mov_b32 m0, s59
	s_nop 0
	global_load_lds_dwordx4 v[178:179], off
	v_lshl_add_u64 v[178:179], v[182:183], 0, s[10:11]
	s_mov_b32 m0, s56
	s_nop 0
	global_load_lds_dwordx4 v[178:179], off
	v_lshl_add_u64 v[178:179], v[184:185], 0, s[10:11]
	s_mov_b32 m0, s57
	s_nop 0
	global_load_lds_dwordx4 v[178:179], off
	s_waitcnt vmcnt(8)
	s_waitcnt lgkmcnt(0)
	s_barrier
	s_setprio 0
	s_waitcnt lgkmcnt(0)
	v_mfma_scale_f32_16x16x128_f8f6f4 v[70:73], v[2:9], v[200:207], v[70:73], v191, v192 op_sel_hi:[0,0,0]
	v_mfma_scale_f32_16x16x128_f8f6f4 v[66:69], v[10:17], v[200:207], v[66:69], v191, v192 op_sel_hi:[0,0,0]
	v_mfma_scale_f32_16x16x128_f8f6f4 v[38:41], v[2:9], v[208:215], v[38:41], v191, v192 op_sel_hi:[0,0,0]
	v_mfma_scale_f32_16x16x128_f8f6f4 v[34:37], v[10:17], v[208:215], v[34:37], v191, v192 op_sel_hi:[0,0,0]
	v_mfma_scale_f32_16x16x128_f8f6f4 v[54:57], v[2:9], v[216:223], v[54:57], v191, v192 op_sel_hi:[0,0,0]
	v_mfma_scale_f32_16x16x128_f8f6f4 v[62:65], v[10:17], v[216:223], v[62:65], v191, v192 op_sel_hi:[0,0,0]
	v_mfma_scale_f32_16x16x128_f8f6f4 v[42:45], v[2:9], v[224:231], v[42:45], v191, v192 op_sel_hi:[0,0,0]
	v_mfma_scale_f32_16x16x128_f8f6f4 v[46:49], v[10:17], v[224:231], v[46:49], v191, v192 op_sel_hi:[0,0,0]
	s_nop 0
	s_setprio 0
	v_mfma_scale_f32_16x16x128_f8f6f4 v[102:105], v[18:25], v[200:207], v[102:105], v191, v192 op_sel_hi:[0,0,0]
	v_mfma_scale_f32_16x16x128_f8f6f4 v[110:113], v[26:33], v[200:207], v[110:113], v191, v192 op_sel_hi:[0,0,0]
	v_mfma_scale_f32_16x16x128_f8f6f4 v[90:93], v[18:25], v[208:215], v[90:93], v191, v192 op_sel_hi:[0,0,0]
	v_mfma_scale_f32_16x16x128_f8f6f4 v[94:97], v[26:33], v[208:215], v[94:97], v191, v192 op_sel_hi:[0,0,0]
	v_mfma_scale_f32_16x16x128_f8f6f4 v[74:77], v[18:25], v[216:223], v[74:77], v191, v192 op_sel_hi:[0,0,0]
	v_mfma_scale_f32_16x16x128_f8f6f4 v[78:81], v[26:33], v[216:223], v[78:81], v191, v192 op_sel_hi:[0,0,0]
	v_mfma_scale_f32_16x16x128_f8f6f4 v[50:53], v[18:25], v[224:231], v[50:53], v191, v192 op_sel_hi:[0,0,0]
	v_mfma_scale_f32_16x16x128_f8f6f4 v[58:61], v[26:33], v[224:231], v[58:61], v191, v192 op_sel_hi:[0,0,0]
	s_setprio 1
	s_barrier
	s_movk_i32 s36, 0x100
	s_andn2_b64 vcc, exec, s[28:29]
	s_mov_b64 s[30:31], -1
	s_mov_b64 s[28:29], 0
	s_cbranch_vccz .LBB0_1961
	s_setprio 0
	s_and_b64 vcc, exec, s[12:13]
	s_cbranch_vccz .LBB0_1964
	s_barrier

; #define GAS __attribute__((address_space(1)))
; #define PG8_STAGE(bufoff, gbase, voff) do { _Pragma("unroll") for (int _i = 0; _i < 2; ++_i) \
;         __builtin_amdgcn_global_load_lds((const GAS unsigned*)((const GAS char*)(gbase) + (voff)[_i]), (LAS unsigned*)(lds + (bufoff) + ldsw + _i * 8192), 16, 0, 0); } while (0)
; #define PG8_LDA(dst, b, h) do { _Pragma("unroll") for (int m = 0; m < 4; ++m) { dst[m].lo = *(const LAS i32x4v*)(lds + PG8_SA(b, h) + (FP8 ? aoff8[0] : aoff) + m * 2048); dst[m].hi = *(const LAS i32x4v*)(lds + PG8_SA(b, h) + (FP8 ? aoff8[1] : aoff + 1024) + m * 2048); } } while (0)
; #define PG8_LDB(dst, b, h) do { _Pragma("unroll") for (int n = 0; n < 2; ++n) { dst[n].lo = *(const LAS i32x4v*)(lds + PG8_SB(b, h) + (FP8 ? boff8[0] : boff) + n * 2048); dst[n].hi = *(const LAS i32x4v*)(lds + PG8_SB(b, h) + (FP8 ? boff8[1] : boff + 1024) + n * 2048); } } while (0)
; #define PG8_WAIT_V(n) asm volatile("s_waitcnt vmcnt(" #n ")" ::: "memory")
; template <class Epi, class Sched, bool GATHER, bool FP8 = false, bool UNI = false>
; __device__ __forceinline__ void gemm_phase(LAS unsigned char* lds, const Sched& S, const Epi& E) {
;     ...
;         for (int t = 0; t < nt; t += 2) {
;             const bool last = (t == nt - 2);
;             const GAS char* a1 = cA + (size_t)(t + 1) * 128;
;             const GAS char* a2 = last ? nA : cA + (size_t)(t + 2) * 128; const GAS char* b2 = last ? nB : cB + (size_t)(t + 2) * 128;
;             const GAS char* a3 = a2 + 128; const GAS char* b3 = b2 + 128;
;             const size_t hB2 = last ? hBn : hBc;
;             unsigned oa0[2], oa1[2], ob[2];
; #pragma unroll
;             for (int i = 0; i < 2; ++i) { if constexpr (UNI) { oa0[i] = aoc[0][i]; oa1[i] = aoc[1][i]; ob[i] = boc[i]; } else { oa0[i] = last ? aon[0][i] : aoc[0][i]; oa1[i] = last ? aon[1][i] : aoc[1][i]; ob[i] = last ? bon[i] : boc[i]; } }
;             PG8_LDB(B0, 0, 0); PG8_LDB(B1, 0, 1); PG8_SCHED; PG8_LDA(At, 0, 0); PG8_STAGE(PG8_SA(1, 1), a1, aoc[1]);
;             PG8_WAIT_V(8); PG8_WAIT_L(0); PG8_BAR; PG8_MMA(0, 0, At, B0); PG8_MMA(0, 1, At, B1); PG8_BAR; PG8_SCHED;
;             PG8_LDA(At, 0, 1); PG8_STAGE(PG8_SB(0, 0), b2, ob); PG8_STAGE(PG8_SB(0, 1), b2 + hB2, ob); PG8_STAGE(PG8_SA(0, 0), a2, oa0);
;             PG8_WAIT_V(8); PG8_WAIT_L(0); PG8_BAR; PG8_MMA(1, 0, At, B0); PG8_MMA(1, 1, At, B1); PG8_BAR; PG8_SCHED;
.LBB0_2113:
	ds_read_b128 v[130:133], v161
	ds_read_b128 v[134:137], v161 offset:1024
	ds_read_b128 v[138:141], v161 offset:2048
	ds_read_b128 v[142:145], v161 offset:3072
	ds_read_b128 v[174:177], v182
	ds_read_b128 v[178:181], v182 offset:1024
	ds_read_b128 v[188:191], v182 offset:2048
	ds_read_b128 v[192:195], v182 offset:3072
	s_add_u32 s8, s6, 0x80
	s_addc_u32 s9, s7, 0
	s_cmp_eq_u32 s60, 28
	s_cselect_b32 s49, s45, s9
	s_cselect_b32 s48, s44, s8
	s_cselect_b32 s9, s47, s59
	s_cselect_b32 s8, s46, s58
	v_lshl_add_u64 v[228:229], s[6:7], 0, v[168:169]
	s_add_i32 m0, s68, 0xc000
	ds_read_b128 v[196:199], v183
	ds_read_b128 v[200:203], v183 offset:1024
	ds_read_b128 v[204:207], v183 offset:2048
	ds_read_b128 v[208:211], v183 offset:3072
	ds_read_b128 v[212:215], v183 offset:4096
	ds_read_b128 v[216:219], v183 offset:5120
	ds_read_b128 v[220:223], v183 offset:6144
	ds_read_b128 v[224:227], v183 offset:7168
	global_load_lds_dwordx4 v[228:229], off
	v_lshl_add_u64 v[228:229], s[6:7], 0, v[166:167]
	s_add_i32 m0, s68, 0xe000
	s_nop 0
	global_load_lds_dwordx4 v[228:229], off
	s_waitcnt vmcnt(8)
	s_waitcnt lgkmcnt(0)
	s_barrier
	s_setprio 0
	s_waitcnt lgkmcnt(0)
	v_mfma_f32_16x16x32_bf16 v[126:129], v[130:133], v[196:199], v[126:129]
	v_mfma_f32_16x16x32_bf16 v[122:125], v[138:141], v[196:199], v[122:125]
	v_mfma_f32_16x16x32_bf16 v[110:113], v[130:133], v[204:207], v[110:113]
	v_mfma_f32_16x16x32_bf16 v[106:109], v[138:141], v[204:207], v[106:109]
	v_mfma_f32_16x16x32_bf16 v[94:97], v[130:133], v[212:215], v[94:97]
	v_mfma_f32_16x16x32_bf16 v[90:93], v[138:141], v[212:215], v[90:93]
	v_mfma_f32_16x16x32_bf16 v[78:81], v[130:133], v[220:223], v[78:81]
	v_mfma_f32_16x16x32_bf16 v[74:77], v[138:141], v[220:223], v[74:77]
	v_mfma_f32_16x16x32_bf16 v[126:129], v[134:137], v[200:203], v[126:129]
	v_mfma_f32_16x16x32_bf16 v[122:125], v[142:145], v[200:203], v[122:125]
	v_mfma_f32_16x16x32_bf16 v[110:113], v[134:137], v[208:211], v[110:113]
	v_mfma_f32_16x16x32_bf16 v[106:109], v[142:145], v[208:211], v[106:109]
	v_mfma_f32_16x16x32_bf16 v[94:97], v[134:137], v[216:219], v[94:97]
	v_mfma_f32_16x16x32_bf16 v[90:93], v[142:145], v[216:219], v[90:93]
	v_mfma_f32_16x16x32_bf16 v[78:81], v[134:137], v[224:227], v[78:81]
	v_mfma_f32_16x16x32_bf16 v[74:77], v[142:145], v[224:227], v[74:77]
	s_nop 0
	s_setprio 0
	v_mfma_f32_16x16x32_bf16 v[118:121], v[174:177], v[196:199], v[118:121]
	v_mfma_f32_16x16x32_bf16 v[114:117], v[188:191], v[196:199], v[114:117]
	v_mfma_f32_16x16x32_bf16 v[102:105], v[174:177], v[204:207], v[102:105]
	v_mfma_f32_16x16x32_bf16 v[98:101], v[188:191], v[204:207], v[98:101]
	v_mfma_f32_16x16x32_bf16 v[86:89], v[174:177], v[212:215], v[86:89]
	v_mfma_f32_16x16x32_bf16 v[82:85], v[188:191], v[212:215], v[82:85]
	v_mfma_f32_16x16x32_bf16 v[70:73], v[174:177], v[220:223], v[70:73]
	v_mfma_f32_16x16x32_bf16 v[66:69], v[188:191], v[220:223], v[66:69]
	v_mfma_f32_16x16x32_bf16 v[118:121], v[178:181], v[200:203], v[118:121]
	v_mfma_f32_16x16x32_bf16 v[114:117], v[192:195], v[200:203], v[114:117]
	v_mfma_f32_16x16x32_bf16 v[102:105], v[178:181], v[208:211], v[102:105]
	v_mfma_f32_16x16x32_bf16 v[98:101], v[192:195], v[208:211], v[98:101]
	v_mfma_f32_16x16x32_bf16 v[86:89], v[178:181], v[216:219], v[86:89]
	v_mfma_f32_16x16x32_bf16 v[82:85], v[192:195], v[216:219], v[82:85]
	v_mfma_f32_16x16x32_bf16 v[70:73], v[178:181], v[224:227], v[70:73]
	v_mfma_f32_16x16x32_bf16 v[66:69], v[192:195], v[224:227], v[66:69]
	s_setprio 1
	s_barrier
	s_mov_b32 m0, s50
	v_lshl_add_u64 v[228:229], s[8:9], 0, v[146:147]
	s_add_u32 s90, s8, 0x80000
	ds_read_b128 v[196:199], v183 offset:16384
	ds_read_b128 v[200:203], v183 offset:17408
	ds_read_b128 v[204:207], v183 offset:18432
	ds_read_b128 v[208:211], v183 offset:19456
	ds_read_b128 v[212:215], v183 offset:20480
	ds_read_b128 v[216:219], v183 offset:21504
	ds_read_b128 v[220:223], v183 offset:22528
	ds_read_b128 v[224:227], v183 offset:23552
	global_load_lds_dwordx4 v[228:229], off
	v_lshl_add_u64 v[230:231], s[8:9], 0, v[152:153]
	s_mov_b32 m0, s51
	s_addc_u32 s91, s9, 0
	global_load_lds_dwordx4 v[230:231], off
	v_lshl_add_u64 v[232:233], s[90:91], 0, v[146:147]
	s_mov_b32 m0, s56
	v_lshl_add_u64 v[234:235], s[48:49], 0, v[154:155]
	global_load_lds_dwordx4 v[232:233], off
	v_lshl_add_u64 v[232:233], s[90:91], 0, v[152:153]
	s_mov_b32 m0, s57
	s_nop 0
	global_load_lds_dwordx4 v[232:233], off
	v_lshl_add_u64 v[232:233], s[48:49], 0, v[148:149]
	s_mov_b32 m0, s68
	s_nop 0
	global_load_lds_dwordx4 v[232:233], off
	s_mov_b32 m0, s69
	s_nop 0
	global_load_lds_dwordx4 v[234:235], off
	s_waitcnt vmcnt(8)
	s_waitcnt lgkmcnt(0)
	s_barrier
; #define PG8_STAGE(bufoff, gbase, voff) do { _Pragma("unroll") for (int _i = 0; _i < 2; ++_i) \
;         __builtin_amdgcn_global_load_lds((const GAS unsigned*)((const GAS char*)(gbase) + (voff)[_i]), (LAS unsigned*)(lds + (bufoff) + ldsw + _i * 8192), 16, 0, 0); } while (0)
; #define PG8_LDA(dst, b, h) do { _Pragma("unroll") for (int m = 0; m < 4; ++m) { dst[m].lo = *(const LAS i32x4v*)(lds + PG8_SA(b, h) + (FP8 ? aoff8[0] : aoff) + m * 2048); dst[m].hi = *(const LAS i32x4v*)(lds + PG8_SA(b, h) + (FP8 ? aoff8[1] : aoff + 1024) + m * 2048); } } while (0)
; #define PG8_LDB(dst, b, h) do { _Pragma("unroll") for (int n = 0; n < 2; ++n) { dst[n].lo = *(const LAS i32x4v*)(lds + PG8_SB(b, h) + (FP8 ? boff8[0] : boff) + n * 2048); dst[n].hi = *(const LAS i32x4v*)(lds + PG8_SB(b, h) + (FP8 ? boff8[1] : boff + 1024) + n * 2048); } } while (0)
; #define PG8_WAIT_V(n) asm volatile("s_waitcnt vmcnt(" #n ")" ::: "memory")
; #define PG8_WAIT_L(n) asm volatile("s_waitcnt lgkmcnt(" #n ")" ::: "memory")
; #define PG8_BAR __builtin_amdgcn_s_barrier()
; #define PG8_SCHED __builtin_amdgcn_sched_barrier(0)
; template <class Epi, class Sched, bool GATHER, bool FP8 = false, bool UNI = false>
; __device__ __forceinline__ void gemm_phase(LAS unsigned char* lds, const Sched& S, const Epi& E) {
;     ...
;             PG8_WAIT_V(8); PG8_WAIT_L(0); PG8_BAR; PG8_MMA(1, 0, At, B0); PG8_MMA(1, 1, At, B1); PG8_BAR; PG8_SCHED;
;             PG8_LDB(B0, 1, 0); PG8_LDB(B1, 1, 1); PG8_SCHED; PG8_LDA(At, 1, 0); PG8_STAGE(PG8_SA(0, 1), a2, oa1);
;             PG8_WAIT_V(8); PG8_WAIT_L(0); PG8_BAR; PG8_MMA(0, 0, At, B0); PG8_MMA(0, 1, At, B1); PG8_BAR; PG8_SCHED;
	s_setprio 0
	s_waitcnt lgkmcnt(0)
	v_mfma_f32_16x16x32_bf16 v[54:57], v[130:133], v[196:199], v[54:57]
	v_mfma_f32_16x16x32_bf16 v[50:53], v[138:141], v[196:199], v[50:53]
	v_mfma_f32_16x16x32_bf16 v[38:41], v[130:133], v[204:207], v[38:41]
	v_mfma_f32_16x16x32_bf16 v[34:37], v[138:141], v[204:207], v[34:37]
	v_mfma_f32_16x16x32_bf16 v[18:21], v[130:133], v[212:215], v[18:21]
	v_mfma_f32_16x16x32_bf16 v[22:25], v[138:141], v[212:215], v[22:25]
	v_mfma_f32_16x16x32_bf16 v[2:5], v[130:133], v[220:223], v[2:5]
	v_mfma_f32_16x16x32_bf16 v[6:9], v[138:141], v[220:223], v[6:9]
	v_mfma_f32_16x16x32_bf16 v[54:57], v[134:137], v[200:203], v[54:57]
	v_mfma_f32_16x16x32_bf16 v[50:53], v[142:145], v[200:203], v[50:53]
	v_mfma_f32_16x16x32_bf16 v[38:41], v[134:137], v[208:211], v[38:41]
	v_mfma_f32_16x16x32_bf16 v[34:37], v[142:145], v[208:211], v[34:37]
	v_mfma_f32_16x16x32_bf16 v[18:21], v[134:137], v[216:219], v[18:21]
	v_mfma_f32_16x16x32_bf16 v[22:25], v[142:145], v[216:219], v[22:25]
	v_mfma_f32_16x16x32_bf16 v[2:5], v[134:137], v[224:227], v[2:5]
	v_mfma_f32_16x16x32_bf16 v[6:9], v[142:145], v[224:227], v[6:9]
	s_nop 0
	s_setprio 0
	v_mfma_f32_16x16x32_bf16 v[58:61], v[174:177], v[196:199], v[58:61]
	v_mfma_f32_16x16x32_bf16 v[62:65], v[188:191], v[196:199], v[62:65]
	v_mfma_f32_16x16x32_bf16 v[42:45], v[174:177], v[204:207], v[42:45]
	v_mfma_f32_16x16x32_bf16 v[46:49], v[188:191], v[204:207], v[46:49]
	v_mfma_f32_16x16x32_bf16 v[26:29], v[174:177], v[212:215], v[26:29]
	v_mfma_f32_16x16x32_bf16 v[30:33], v[188:191], v[212:215], v[30:33]
	v_mfma_f32_16x16x32_bf16 v[10:13], v[174:177], v[220:223], v[10:13]
	v_mfma_f32_16x16x32_bf16 v[14:17], v[188:191], v[220:223], v[14:17]
	v_mfma_f32_16x16x32_bf16 v[58:61], v[178:181], v[200:203], v[58:61]
	v_mfma_f32_16x16x32_bf16 v[62:65], v[192:195], v[200:203], v[62:65]
	v_mfma_f32_16x16x32_bf16 v[42:45], v[178:181], v[208:211], v[42:45]
	v_mfma_f32_16x16x32_bf16 v[46:49], v[192:195], v[208:211], v[46:49]
	v_mfma_f32_16x16x32_bf16 v[26:29], v[178:181], v[216:219], v[26:29]
	v_mfma_f32_16x16x32_bf16 v[30:33], v[192:195], v[216:219], v[30:33]
	v_mfma_f32_16x16x32_bf16 v[10:13], v[178:181], v[224:227], v[10:13]
	v_mfma_f32_16x16x32_bf16 v[14:17], v[192:195], v[224:227], v[14:17]
	s_setprio 1
	s_barrier
	ds_read_b128 v[130:133], v184
	ds_read_b128 v[134:137], v184 offset:1024
	ds_read_b128 v[138:141], v184 offset:2048
	ds_read_b128 v[142:145], v184 offset:3072
	ds_read_b128 v[174:177], v185
	ds_read_b128 v[178:181], v185 offset:1024
	ds_read_b128 v[188:191], v185 offset:2048
	ds_read_b128 v[192:195], v185 offset:3072
	s_mov_b32 m0, s70
	v_lshl_add_u64 v[236:237], s[48:49], 0, v[150:151]
	ds_read_b128 v[196:199], v183 offset:32768
	ds_read_b128 v[200:203], v183 offset:33792
	ds_read_b128 v[204:207], v183 offset:34816
	ds_read_b128 v[208:211], v183 offset:35840
	ds_read_b128 v[212:215], v183 offset:36864
	ds_read_b128 v[216:219], v183 offset:37888
	ds_read_b128 v[220:223], v183 offset:38912
	ds_read_b128 v[224:227], v183 offset:39936
	global_load_lds_dwordx4 v[236:237], off
	v_lshl_add_u64 v[236:237], s[48:49], 0, v[156:157]
	s_mov_b32 m0, s71
	s_nop 0
	global_load_lds_dwordx4 v[236:237], off
	s_waitcnt vmcnt(8)
	s_waitcnt lgkmcnt(0)
	s_barrier
	s_setprio 0
	s_waitcnt lgkmcnt(0)
	v_mfma_f32_16x16x32_bf16 v[126:129], v[130:133], v[196:199], v[126:129]
	v_mfma_f32_16x16x32_bf16 v[122:125], v[138:141], v[196:199], v[122:125]
	v_mfma_f32_16x16x32_bf16 v[110:113], v[130:133], v[204:207], v[110:113]
	v_mfma_f32_16x16x32_bf16 v[106:109], v[138:141], v[204:207], v[106:109]
	v_mfma_f32_16x16x32_bf16 v[94:97], v[130:133], v[212:215], v[94:97]
	v_mfma_f32_16x16x32_bf16 v[90:93], v[138:141], v[212:215], v[90:93]
	v_mfma_f32_16x16x32_bf16 v[78:81], v[130:133], v[220:223], v[78:81]
	v_mfma_f32_16x16x32_bf16 v[74:77], v[138:141], v[220:223], v[74:77]
	v_mfma_f32_16x16x32_bf16 v[126:129], v[134:137], v[200:203], v[126:129]
	v_mfma_f32_16x16x32_bf16 v[122:125], v[142:145], v[200:203], v[122:125]
	v_mfma_f32_16x16x32_bf16 v[110:113], v[134:137], v[208:211], v[110:113]
	v_mfma_f32_16x16x32_bf16 v[106:109], v[142:145], v[208:211], v[106:109]
	v_mfma_f32_16x16x32_bf16 v[94:97], v[134:137], v[216:219], v[94:97]
	v_mfma_f32_16x16x32_bf16 v[90:93], v[142:145], v[216:219], v[90:93]
	v_mfma_f32_16x16x32_bf16 v[78:81], v[134:137], v[224:227], v[78:81]
	v_mfma_f32_16x16x32_bf16 v[74:77], v[142:145], v[224:227], v[74:77]
	s_nop 0
	s_setprio 0
	v_mfma_f32_16x16x32_bf16 v[118:121], v[174:177], v[196:199], v[118:121]
	v_mfma_f32_16x16x32_bf16 v[114:117], v[188:191], v[196:199], v[114:117]
	v_mfma_f32_16x16x32_bf16 v[102:105], v[174:177], v[204:207], v[102:105]
	v_mfma_f32_16x16x32_bf16 v[98:101], v[188:191], v[204:207], v[98:101]
	v_mfma_f32_16x16x32_bf16 v[86:89], v[174:177], v[212:215], v[86:89]
	v_mfma_f32_16x16x32_bf16 v[82:85], v[188:191], v[212:215], v[82:85]
	v_mfma_f32_16x16x32_bf16 v[70:73], v[174:177], v[220:223], v[70:73]
	v_mfma_f32_16x16x32_bf16 v[66:69], v[188:191], v[220:223], v[66:69]
	v_mfma_f32_16x16x32_bf16 v[118:121], v[178:181], v[200:203], v[118:121]
	v_mfma_f32_16x16x32_bf16 v[114:117], v[192:195], v[200:203], v[114:117]
	v_mfma_f32_16x16x32_bf16 v[102:105], v[178:181], v[208:211], v[102:105]
	v_mfma_f32_16x16x32_bf16 v[98:101], v[192:195], v[208:211], v[98:101]
	v_mfma_f32_16x16x32_bf16 v[86:89], v[178:181], v[216:219], v[86:89]
	v_mfma_f32_16x16x32_bf16 v[82:85], v[192:195], v[216:219], v[82:85]
	v_mfma_f32_16x16x32_bf16 v[70:73], v[178:181], v[224:227], v[70:73]
	v_mfma_f32_16x16x32_bf16 v[66:69], v[192:195], v[224:227], v[66:69]
	s_setprio 1
	s_barrier
; #define PG8_STAGE(bufoff, gbase, voff) do { _Pragma("unroll") for (int _i = 0; _i < 2; ++_i) \
;         __builtin_amdgcn_global_load_lds((const GAS unsigned*)((const GAS char*)(gbase) + (voff)[_i]), (LAS unsigned*)(lds + (bufoff) + ldsw + _i * 8192), 16, 0, 0); } while (0)
; #define PG8_LDA(dst, b, h) do { _Pragma("unroll") for (int m = 0; m < 4; ++m) { dst[m].lo = *(const LAS i32x4v*)(lds + PG8_SA(b, h) + (FP8 ? aoff8[0] : aoff) + m * 2048); dst[m].hi = *(const LAS i32x4v*)(lds + PG8_SA(b, h) + (FP8 ? aoff8[1] : aoff + 1024) + m * 2048); } } while (0)
; #define PG8_WAIT_V(n) asm volatile("s_waitcnt vmcnt(" #n ")" ::: "memory")
; #define PG8_WAIT_L(n) asm volatile("s_waitcnt lgkmcnt(" #n ")" ::: "memory")
; #define PG8_BAR __builtin_amdgcn_s_barrier()
; #define PG8_SCHED __builtin_amdgcn_sched_barrier(0)
; template <class Epi, class Sched, bool GATHER, bool FP8 = false, bool UNI = false>
; __device__ __forceinline__ void gemm_phase(LAS unsigned char* lds, const Sched& S, const Epi& E) {
;     ...
;             PG8_LDA(At, 1, 1); PG8_STAGE(PG8_SB(1, 0), b3, ob); PG8_STAGE(PG8_SB(1, 1), b3 + hB2, ob); PG8_STAGE(PG8_SA(1, 0), a3, oa0);
;             PG8_WAIT_V(8); PG8_WAIT_L(0); PG8_BAR; PG8_MMA(1, 0, At, B0); PG8_MMA(1, 1, At, B1); PG8_BAR; PG8_SCHED;
;         }
;         if (wr == 0) PG8_BAR;
	s_mov_b32 m0, s72
	v_lshl_add_u64 v[228:229], v[228:229], 0, s[22:23]
	s_add_u32 s8, s8, 0x80080
	ds_read_b128 v[196:199], v183 offset:49152
	ds_read_b128 v[200:203], v183 offset:50176
	ds_read_b128 v[204:207], v183 offset:51200
	ds_read_b128 v[208:211], v183 offset:52224
	ds_read_b128 v[212:215], v183 offset:53248
	ds_read_b128 v[216:219], v183 offset:54272
	ds_read_b128 v[220:223], v183 offset:55296
	ds_read_b128 v[224:227], v183 offset:56320
	global_load_lds_dwordx4 v[228:229], off
	v_lshl_add_u64 v[228:229], v[230:231], 0, s[22:23]
	s_mov_b32 m0, s73
	s_addc_u32 s9, s9, 0
	global_load_lds_dwordx4 v[228:229], off
	v_lshl_add_u64 v[228:229], s[8:9], 0, v[146:147]
	s_mov_b32 m0, s76
	s_nop 0
	global_load_lds_dwordx4 v[228:229], off
	v_lshl_add_u64 v[228:229], s[8:9], 0, v[152:153]
	s_mov_b32 m0, s77
	s_nop 0
	global_load_lds_dwordx4 v[228:229], off
	v_lshl_add_u64 v[228:229], v[232:233], 0, s[22:23]
	s_mov_b32 m0, s74
	s_nop 0
	global_load_lds_dwordx4 v[228:229], off
	v_lshl_add_u64 v[228:229], v[234:235], 0, s[22:23]
	s_mov_b32 m0, s75
	s_nop 0
	global_load_lds_dwordx4 v[228:229], off
	s_waitcnt vmcnt(8)
	s_waitcnt lgkmcnt(0)
	s_barrier
	s_setprio 0
	s_waitcnt lgkmcnt(0)
	v_mfma_f32_16x16x32_bf16 v[54:57], v[130:133], v[196:199], v[54:57]
	v_mfma_f32_16x16x32_bf16 v[50:53], v[138:141], v[196:199], v[50:53]
	v_mfma_f32_16x16x32_bf16 v[38:41], v[130:133], v[204:207], v[38:41]
	v_mfma_f32_16x16x32_bf16 v[34:37], v[138:141], v[204:207], v[34:37]
	v_mfma_f32_16x16x32_bf16 v[18:21], v[130:133], v[212:215], v[18:21]
	v_mfma_f32_16x16x32_bf16 v[22:25], v[138:141], v[212:215], v[22:25]
	v_mfma_f32_16x16x32_bf16 v[2:5], v[130:133], v[220:223], v[2:5]
	v_mfma_f32_16x16x32_bf16 v[6:9], v[138:141], v[220:223], v[6:9]
	v_mfma_f32_16x16x32_bf16 v[54:57], v[134:137], v[200:203], v[54:57]
	v_mfma_f32_16x16x32_bf16 v[50:53], v[142:145], v[200:203], v[50:53]
	v_mfma_f32_16x16x32_bf16 v[38:41], v[134:137], v[208:211], v[38:41]
	v_mfma_f32_16x16x32_bf16 v[34:37], v[142:145], v[208:211], v[34:37]
	v_mfma_f32_16x16x32_bf16 v[18:21], v[134:137], v[216:219], v[18:21]
	v_mfma_f32_16x16x32_bf16 v[22:25], v[142:145], v[216:219], v[22:25]
	v_mfma_f32_16x16x32_bf16 v[2:5], v[134:137], v[224:227], v[2:5]
	v_mfma_f32_16x16x32_bf16 v[6:9], v[142:145], v[224:227], v[6:9]
	s_nop 0
	s_setprio 0
	v_mfma_f32_16x16x32_bf16 v[58:61], v[174:177], v[196:199], v[58:61]
	v_mfma_f32_16x16x32_bf16 v[62:65], v[188:191], v[196:199], v[62:65]
	v_mfma_f32_16x16x32_bf16 v[42:45], v[174:177], v[204:207], v[42:45]
	v_mfma_f32_16x16x32_bf16 v[46:49], v[188:191], v[204:207], v[46:49]
	v_mfma_f32_16x16x32_bf16 v[26:29], v[174:177], v[212:215], v[26:29]
	v_mfma_f32_16x16x32_bf16 v[30:33], v[188:191], v[212:215], v[30:33]
	v_mfma_f32_16x16x32_bf16 v[10:13], v[174:177], v[220:223], v[10:13]
	v_mfma_f32_16x16x32_bf16 v[14:17], v[188:191], v[220:223], v[14:17]
	v_mfma_f32_16x16x32_bf16 v[58:61], v[178:181], v[200:203], v[58:61]
	v_mfma_f32_16x16x32_bf16 v[62:65], v[192:195], v[200:203], v[62:65]
	v_mfma_f32_16x16x32_bf16 v[42:45], v[178:181], v[208:211], v[42:45]
	v_mfma_f32_16x16x32_bf16 v[46:49], v[192:195], v[208:211], v[46:49]
	v_mfma_f32_16x16x32_bf16 v[26:29], v[178:181], v[216:219], v[26:29]
	v_mfma_f32_16x16x32_bf16 v[30:33], v[192:195], v[216:219], v[30:33]
	v_mfma_f32_16x16x32_bf16 v[10:13], v[178:181], v[224:227], v[10:13]
	v_mfma_f32_16x16x32_bf16 v[14:17], v[192:195], v[224:227], v[14:17]
	s_setprio 1
	s_barrier
	s_add_i32 s60, s60, 2
	s_add_u32 s58, s58, 0x100
	s_addc_u32 s59, s59, 0
	s_add_u32 s6, s6, 0x100
	s_addc_u32 s7, s7, 0
	s_cmp_gt_u32 s60, 29
	s_cbranch_scc0 .LBB0_2113
	s_setprio 0
	s_and_b64 vcc, exec, s[26:27]
	s_cbranch_vccz .LBB0_2116
	s_barrier

; #define PG8_STAGE(bufoff, gbase, voff) do { _Pragma("unroll") for (int _i = 0; _i < 2; ++_i) \
;         __builtin_amdgcn_global_load_lds((const GAS unsigned*)((const GAS char*)(gbase) + (voff)[_i]), (LAS unsigned*)(lds + (bufoff) + ldsw + _i * 8192), 16, 0, 0); } while (0)
; #define PG8_LDA(dst, b, h) do { _Pragma("unroll") for (int m = 0; m < 4; ++m) { dst[m].lo = *(const LAS i32x4v*)(lds + PG8_SA(b, h) + (FP8 ? aoff8[0] : aoff) + m * 2048); dst[m].hi = *(const LAS i32x4v*)(lds + PG8_SA(b, h) + (FP8 ? aoff8[1] : aoff + 1024) + m * 2048); } } while (0)
; #define PG8_LDB(dst, b, h) do { _Pragma("unroll") for (int n = 0; n < 2; ++n) { dst[n].lo = *(const LAS i32x4v*)(lds + PG8_SB(b, h) + (FP8 ? boff8[0] : boff) + n * 2048); dst[n].hi = *(const LAS i32x4v*)(lds + PG8_SB(b, h) + (FP8 ? boff8[1] : boff + 1024) + n * 2048); } } while (0)
; #define PG8_WAIT_V(n) asm volatile("s_waitcnt vmcnt(" #n ")" ::: "memory")
; #define PG8_WAIT_L(n) asm volatile("s_waitcnt lgkmcnt(" #n ")" ::: "memory")
; #define PG8_BAR __builtin_amdgcn_s_barrier()
; #define PG8_SCHED __builtin_amdgcn_sched_barrier(0)
; template <class Epi, class Sched, bool GATHER, bool FP8 = false, bool UNI = false>
; __device__ __forceinline__ void gemm_phase(LAS unsigned char* lds, const Sched& S, const Epi& E) {
;     ...
;             PG8_LDB(B0, 0, 0); PG8_LDB(B1, 0, 1); PG8_SCHED; PG8_LDA(At, 0, 0); PG8_STAGE(PG8_SA(1, 1), a1, aoc[1]);
;             PG8_WAIT_V(8); PG8_WAIT_L(0); PG8_BAR; PG8_MMA(0, 0, At, B0); PG8_MMA(0, 1, At, B1); PG8_BAR; PG8_SCHED;
;             PG8_LDA(At, 0, 1); PG8_STAGE(PG8_SB(0, 0), b2, ob); PG8_STAGE(PG8_SB(0, 1), b2 + hB2, ob); PG8_STAGE(PG8_SA(0, 0), a2, oa0);
;             PG8_WAIT_V(8); PG8_WAIT_L(0); PG8_BAR; PG8_MMA(1, 0, At, B0); PG8_MMA(1, 1, At, B1); PG8_BAR; PG8_SCHED;
.LBB0_2182:
	ds_read_b128 v[18:21], v177
	ds_read_b128 v[26:29], v177 offset:2048
	ds_read_b128 v[22:25], v198
	ds_read_b128 v[30:33], v198 offset:2048
	ds_read_b128 v[2:5], v199
	ds_read_b128 v[10:13], v199 offset:2048
	ds_read_b128 v[6:9], v200
	ds_read_b128 v[14:17], v200 offset:2048
	s_add_u32 s8, s6, 0x80
	s_addc_u32 s9, s7, 0
	s_cmp_eq_u32 s46, 12
	s_cselect_b32 s43, s39, s9
	s_cselect_b32 s42, s38, s8
	s_cselect_b32 s9, s41, s45
	s_cselect_b32 s8, s40, s44
	v_lshl_add_u64 v[234:235], s[6:7], 0, v[184:185]
	s_add_i32 m0, s56, 0xc000
	ds_read_b128 v[190:193], v201
	ds_read_b128 v[210:213], v201 offset:2048
	ds_read_b128 v[194:197], v202
	ds_read_b128 v[214:217], v202 offset:2048
	ds_read_b128 v[218:221], v201 offset:4096
	ds_read_b128 v[226:229], v201 offset:6144
	ds_read_b128 v[222:225], v202 offset:4096
	ds_read_b128 v[230:233], v202 offset:6144
	global_load_lds_dwordx4 v[234:235], off
	v_lshl_add_u64 v[234:235], s[6:7], 0, v[182:183]
	s_add_i32 m0, s56, 0xe000
	s_nop 0
	global_load_lds_dwordx4 v[234:235], off
	s_waitcnt vmcnt(8)
	s_waitcnt lgkmcnt(0)
	s_barrier
	s_setprio 0
	s_waitcnt lgkmcnt(0)
	v_mfma_scale_f32_16x16x128_f8f6f4 v[158:161], v[18:25], v[190:197], v[158:161], v203, v204 op_sel_hi:[0,0,0]
	v_mfma_scale_f32_16x16x128_f8f6f4 v[154:157], v[26:33], v[190:197], v[154:157], v203, v204 op_sel_hi:[0,0,0]
	v_mfma_scale_f32_16x16x128_f8f6f4 v[142:145], v[18:25], v[210:217], v[142:145], v203, v204 op_sel_hi:[0,0,0]
	v_mfma_scale_f32_16x16x128_f8f6f4 v[138:141], v[26:33], v[210:217], v[138:141], v203, v204 op_sel_hi:[0,0,0]
	v_mfma_scale_f32_16x16x128_f8f6f4 v[126:129], v[18:25], v[218:225], v[126:129], v203, v204 op_sel_hi:[0,0,0]
	v_mfma_scale_f32_16x16x128_f8f6f4 v[122:125], v[26:33], v[218:225], v[122:125], v203, v204 op_sel_hi:[0,0,0]
	v_mfma_scale_f32_16x16x128_f8f6f4 v[110:113], v[18:25], v[226:233], v[110:113], v203, v204 op_sel_hi:[0,0,0]
	v_mfma_scale_f32_16x16x128_f8f6f4 v[106:109], v[26:33], v[226:233], v[106:109], v203, v204 op_sel_hi:[0,0,0]
	s_nop 0
	s_setprio 0
	v_mfma_scale_f32_16x16x128_f8f6f4 v[150:153], v[2:9], v[190:197], v[150:153], v203, v204 op_sel_hi:[0,0,0]
	v_mfma_scale_f32_16x16x128_f8f6f4 v[146:149], v[10:17], v[190:197], v[146:149], v203, v204 op_sel_hi:[0,0,0]
	v_mfma_scale_f32_16x16x128_f8f6f4 v[134:137], v[2:9], v[210:217], v[134:137], v203, v204 op_sel_hi:[0,0,0]
	v_mfma_scale_f32_16x16x128_f8f6f4 v[130:133], v[10:17], v[210:217], v[130:133], v203, v204 op_sel_hi:[0,0,0]
	v_mfma_scale_f32_16x16x128_f8f6f4 v[118:121], v[2:9], v[218:225], v[118:121], v203, v204 op_sel_hi:[0,0,0]
	v_mfma_scale_f32_16x16x128_f8f6f4 v[114:117], v[10:17], v[218:225], v[114:117], v203, v204 op_sel_hi:[0,0,0]
	v_mfma_scale_f32_16x16x128_f8f6f4 v[102:105], v[2:9], v[226:233], v[102:105], v203, v204 op_sel_hi:[0,0,0]
	v_mfma_scale_f32_16x16x128_f8f6f4 v[98:101], v[10:17], v[226:233], v[98:101], v203, v204 op_sel_hi:[0,0,0]
	s_setprio 1
	s_barrier
	s_mov_b32 m0, s48
	v_lshl_add_u64 v[190:191], s[8:9], 0, v[162:163]
	s_add_u32 s88, s8, 0x40000
	ds_read_b128 v[210:213], v201 offset:16384
	ds_read_b128 v[218:221], v201 offset:18432
	ds_read_b128 v[214:217], v202 offset:16384
	ds_read_b128 v[222:225], v202 offset:18432
	ds_read_b128 v[226:229], v201 offset:20480
	ds_read_b128 v[234:237], v201 offset:22528
	ds_read_b128 v[230:233], v202 offset:20480
	ds_read_b128 v[238:241], v202 offset:22528
	global_load_lds_dwordx4 v[190:191], off
	v_lshl_add_u64 v[192:193], s[8:9], 0, v[168:169]
	s_mov_b32 m0, s49
	s_addc_u32 s89, s9, 0
	global_load_lds_dwordx4 v[192:193], off
	v_lshl_add_u64 v[194:195], s[88:89], 0, v[162:163]
	s_mov_b32 m0, s50
	v_lshl_add_u64 v[196:197], s[42:43], 0, v[170:171]
	global_load_lds_dwordx4 v[194:195], off
	v_lshl_add_u64 v[194:195], s[88:89], 0, v[168:169]
	s_mov_b32 m0, s51
	s_nop 0
	global_load_lds_dwordx4 v[194:195], off
	v_lshl_add_u64 v[194:195], s[42:43], 0, v[164:165]
	s_mov_b32 m0, s56
	s_nop 0
	global_load_lds_dwordx4 v[194:195], off
	s_mov_b32 m0, s57
	s_nop 0
	global_load_lds_dwordx4 v[196:197], off
	s_waitcnt vmcnt(8)
	s_waitcnt lgkmcnt(0)
	s_barrier
	s_setprio 0
	s_waitcnt lgkmcnt(0)
	v_mfma_scale_f32_16x16x128_f8f6f4 v[86:89], v[18:25], v[210:217], v[86:89], v203, v204 op_sel_hi:[0,0,0]
	v_mfma_scale_f32_16x16x128_f8f6f4 v[82:85], v[26:33], v[210:217], v[82:85], v203, v204 op_sel_hi:[0,0,0]
	v_mfma_scale_f32_16x16x128_f8f6f4 v[70:73], v[18:25], v[218:225], v[70:73], v203, v204 op_sel_hi:[0,0,0]
	v_mfma_scale_f32_16x16x128_f8f6f4 v[66:69], v[26:33], v[218:225], v[66:69], v203, v204 op_sel_hi:[0,0,0]
	v_mfma_scale_f32_16x16x128_f8f6f4 v[54:57], v[18:25], v[226:233], v[54:57], v203, v204 op_sel_hi:[0,0,0]
	v_mfma_scale_f32_16x16x128_f8f6f4 v[50:53], v[26:33], v[226:233], v[50:53], v203, v204 op_sel_hi:[0,0,0]
	v_mfma_scale_f32_16x16x128_f8f6f4 v[38:41], v[18:25], v[234:241], v[38:41], v203, v204 op_sel_hi:[0,0,0]
	v_mfma_scale_f32_16x16x128_f8f6f4 v[34:37], v[26:33], v[234:241], v[34:37], v203, v204 op_sel_hi:[0,0,0]
	s_nop 0
	s_setprio 0
	v_mfma_scale_f32_16x16x128_f8f6f4 v[94:97], v[2:9], v[210:217], v[94:97], v203, v204 op_sel_hi:[0,0,0]
	v_mfma_scale_f32_16x16x128_f8f6f4 v[90:93], v[10:17], v[210:217], v[90:93], v203, v204 op_sel_hi:[0,0,0]
	v_mfma_scale_f32_16x16x128_f8f6f4 v[78:81], v[2:9], v[218:225], v[78:81], v203, v204 op_sel_hi:[0,0,0]
	v_mfma_scale_f32_16x16x128_f8f6f4 v[74:77], v[10:17], v[218:225], v[74:77], v203, v204 op_sel_hi:[0,0,0]
	v_mfma_scale_f32_16x16x128_f8f6f4 v[62:65], v[2:9], v[226:233], v[62:65], v203, v204 op_sel_hi:[0,0,0]
	v_mfma_scale_f32_16x16x128_f8f6f4 v[58:61], v[10:17], v[226:233], v[58:61], v203, v204 op_sel_hi:[0,0,0]
	v_mfma_scale_f32_16x16x128_f8f6f4 v[46:49], v[2:9], v[234:241], v[46:49], v203, v204 op_sel_hi:[0,0,0]
	v_mfma_scale_f32_16x16x128_f8f6f4 v[42:45], v[10:17], v[234:241], v[42:45], v203, v204 op_sel_hi:[0,0,0]
	s_setprio 1
	s_barrier
; #define PG8_STAGE(bufoff, gbase, voff) do { _Pragma("unroll") for (int _i = 0; _i < 2; ++_i) \
;         __builtin_amdgcn_global_load_lds((const GAS unsigned*)((const GAS char*)(gbase) + (voff)[_i]), (LAS unsigned*)(lds + (bufoff) + ldsw + _i * 8192), 16, 0, 0); } while (0)
; #define PG8_LDA(dst, b, h) do { _Pragma("unroll") for (int m = 0; m < 4; ++m) { dst[m].lo = *(const LAS i32x4v*)(lds + PG8_SA(b, h) + (FP8 ? aoff8[0] : aoff) + m * 2048); dst[m].hi = *(const LAS i32x4v*)(lds + PG8_SA(b, h) + (FP8 ? aoff8[1] : aoff + 1024) + m * 2048); } } while (0)
; #define PG8_LDB(dst, b, h) do { _Pragma("unroll") for (int n = 0; n < 2; ++n) { dst[n].lo = *(const LAS i32x4v*)(lds + PG8_SB(b, h) + (FP8 ? boff8[0] : boff) + n * 2048); dst[n].hi = *(const LAS i32x4v*)(lds + PG8_SB(b, h) + (FP8 ? boff8[1] : boff + 1024) + n * 2048); } } while (0)
; #define PG8_WAIT_V(n) asm volatile("s_waitcnt vmcnt(" #n ")" ::: "memory")
; #define PG8_WAIT_L(n) asm volatile("s_waitcnt lgkmcnt(" #n ")" ::: "memory")
; #define PG8_BAR __builtin_amdgcn_s_barrier()
; #define PG8_SCHED __builtin_amdgcn_sched_barrier(0)
; template <class Epi, class Sched, bool GATHER, bool FP8 = false, bool UNI = false>
; __device__ __forceinline__ void gemm_phase(LAS unsigned char* lds, const Sched& S, const Epi& E) {
;     ...
;             PG8_LDB(B0, 1, 0); PG8_LDB(B1, 1, 1); PG8_SCHED; PG8_LDA(At, 1, 0); PG8_STAGE(PG8_SA(0, 1), a2, oa1);
;             PG8_WAIT_V(8); PG8_WAIT_L(0); PG8_BAR; PG8_MMA(0, 0, At, B0); PG8_MMA(0, 1, At, B1); PG8_BAR; PG8_SCHED;
;             PG8_LDA(At, 1, 1); PG8_STAGE(PG8_SB(1, 0), b3, ob); PG8_STAGE(PG8_SB(1, 1), b3 + hB2, ob); PG8_STAGE(PG8_SA(1, 0), a3, oa0);
;             PG8_WAIT_V(8); PG8_WAIT_L(0); PG8_BAR; PG8_MMA(1, 0, At, B0); PG8_MMA(1, 1, At, B1); PG8_BAR; PG8_SCHED;
;         }
	ds_read_b128 v[2:5], v205
	ds_read_b128 v[10:13], v205 offset:2048
	ds_read_b128 v[6:9], v206
	ds_read_b128 v[14:17], v206 offset:2048
	ds_read_b128 v[18:21], v207
	ds_read_b128 v[26:29], v207 offset:2048
	ds_read_b128 v[22:25], v208
	ds_read_b128 v[30:33], v208 offset:2048
	s_mov_b32 m0, s58
	v_lshl_add_u64 v[242:243], s[42:43], 0, v[166:167]
	ds_read_b128 v[210:213], v201 offset:32768
	ds_read_b128 v[218:221], v201 offset:34816
	ds_read_b128 v[214:217], v202 offset:32768
	ds_read_b128 v[222:225], v202 offset:34816
	ds_read_b128 v[226:229], v201 offset:36864
	ds_read_b128 v[234:237], v201 offset:38912
	ds_read_b128 v[230:233], v202 offset:36864
	ds_read_b128 v[238:241], v202 offset:38912
	global_load_lds_dwordx4 v[242:243], off
	v_lshl_add_u64 v[242:243], s[42:43], 0, v[172:173]
	s_mov_b32 m0, s59
	s_nop 0
	global_load_lds_dwordx4 v[242:243], off
	s_waitcnt vmcnt(8)
	s_waitcnt lgkmcnt(0)
	s_barrier
	s_setprio 0
	s_waitcnt lgkmcnt(0)
	v_mfma_scale_f32_16x16x128_f8f6f4 v[158:161], v[2:9], v[210:217], v[158:161], v203, v204 op_sel_hi:[0,0,0]
	v_mfma_scale_f32_16x16x128_f8f6f4 v[154:157], v[10:17], v[210:217], v[154:157], v203, v204 op_sel_hi:[0,0,0]
	v_mfma_scale_f32_16x16x128_f8f6f4 v[142:145], v[2:9], v[218:225], v[142:145], v203, v204 op_sel_hi:[0,0,0]
	v_mfma_scale_f32_16x16x128_f8f6f4 v[138:141], v[10:17], v[218:225], v[138:141], v203, v204 op_sel_hi:[0,0,0]
	v_mfma_scale_f32_16x16x128_f8f6f4 v[126:129], v[2:9], v[226:233], v[126:129], v203, v204 op_sel_hi:[0,0,0]
	v_mfma_scale_f32_16x16x128_f8f6f4 v[122:125], v[10:17], v[226:233], v[122:125], v203, v204 op_sel_hi:[0,0,0]
	v_mfma_scale_f32_16x16x128_f8f6f4 v[110:113], v[2:9], v[234:241], v[110:113], v203, v204 op_sel_hi:[0,0,0]
	v_mfma_scale_f32_16x16x128_f8f6f4 v[106:109], v[10:17], v[234:241], v[106:109], v203, v204 op_sel_hi:[0,0,0]
	s_nop 0
	s_setprio 0
	v_mfma_scale_f32_16x16x128_f8f6f4 v[150:153], v[18:25], v[210:217], v[150:153], v203, v204 op_sel_hi:[0,0,0]
	v_mfma_scale_f32_16x16x128_f8f6f4 v[146:149], v[26:33], v[210:217], v[146:149], v203, v204 op_sel_hi:[0,0,0]
	v_mfma_scale_f32_16x16x128_f8f6f4 v[134:137], v[18:25], v[218:225], v[134:137], v203, v204 op_sel_hi:[0,0,0]
	v_mfma_scale_f32_16x16x128_f8f6f4 v[130:133], v[26:33], v[218:225], v[130:133], v203, v204 op_sel_hi:[0,0,0]
	v_mfma_scale_f32_16x16x128_f8f6f4 v[118:121], v[18:25], v[226:233], v[118:121], v203, v204 op_sel_hi:[0,0,0]
	v_mfma_scale_f32_16x16x128_f8f6f4 v[114:117], v[26:33], v[226:233], v[114:117], v203, v204 op_sel_hi:[0,0,0]
	v_mfma_scale_f32_16x16x128_f8f6f4 v[102:105], v[18:25], v[234:241], v[102:105], v203, v204 op_sel_hi:[0,0,0]
	v_mfma_scale_f32_16x16x128_f8f6f4 v[98:101], v[26:33], v[234:241], v[98:101], v203, v204 op_sel_hi:[0,0,0]
	s_setprio 1
	s_barrier
	s_mov_b32 m0, s61
	v_lshl_add_u64 v[190:191], v[190:191], 0, s[20:21]
	s_add_u32 s8, s8, 0x40080
	ds_read_b128 v[210:213], v201 offset:49152
	ds_read_b128 v[218:221], v201 offset:51200
	ds_read_b128 v[214:217], v202 offset:49152
	ds_read_b128 v[222:225], v202 offset:51200
	ds_read_b128 v[226:229], v201 offset:53248
	ds_read_b128 v[234:237], v201 offset:55296
	ds_read_b128 v[230:233], v202 offset:53248
	ds_read_b128 v[238:241], v202 offset:55296
	global_load_lds_dwordx4 v[190:191], off
	v_lshl_add_u64 v[190:191], v[192:193], 0, s[20:21]
	s_mov_b32 m0, s68
	s_addc_u32 s9, s9, 0
	global_load_lds_dwordx4 v[190:191], off
	v_lshl_add_u64 v[190:191], s[8:9], 0, v[162:163]
	s_mov_b32 m0, s71
	s_nop 0
	global_load_lds_dwordx4 v[190:191], off
	v_lshl_add_u64 v[190:191], s[8:9], 0, v[168:169]
	s_mov_b32 m0, s72
	s_nop 0
	global_load_lds_dwordx4 v[190:191], off
	v_lshl_add_u64 v[190:191], v[194:195], 0, s[20:21]
	s_mov_b32 m0, s69
	s_nop 0
	global_load_lds_dwordx4 v[190:191], off
	v_lshl_add_u64 v[190:191], v[196:197], 0, s[20:21]
	s_mov_b32 m0, s70
	s_nop 0
	global_load_lds_dwordx4 v[190:191], off
	s_waitcnt vmcnt(8)
	s_waitcnt lgkmcnt(0)
	s_barrier
	s_setprio 0
	s_waitcnt lgkmcnt(0)
	v_mfma_scale_f32_16x16x128_f8f6f4 v[86:89], v[2:9], v[210:217], v[86:89], v203, v204 op_sel_hi:[0,0,0]
	v_mfma_scale_f32_16x16x128_f8f6f4 v[82:85], v[10:17], v[210:217], v[82:85], v203, v204 op_sel_hi:[0,0,0]
	v_mfma_scale_f32_16x16x128_f8f6f4 v[70:73], v[2:9], v[218:225], v[70:73], v203, v204 op_sel_hi:[0,0,0]
	v_mfma_scale_f32_16x16x128_f8f6f4 v[66:69], v[10:17], v[218:225], v[66:69], v203, v204 op_sel_hi:[0,0,0]
	v_mfma_scale_f32_16x16x128_f8f6f4 v[54:57], v[2:9], v[226:233], v[54:57], v203, v204 op_sel_hi:[0,0,0]
	v_mfma_scale_f32_16x16x128_f8f6f4 v[50:53], v[10:17], v[226:233], v[50:53], v203, v204 op_sel_hi:[0,0,0]
	v_mfma_scale_f32_16x16x128_f8f6f4 v[38:41], v[2:9], v[234:241], v[38:41], v203, v204 op_sel_hi:[0,0,0]
	v_mfma_scale_f32_16x16x128_f8f6f4 v[34:37], v[10:17], v[234:241], v[34:37], v203, v204 op_sel_hi:[0,0,0]
	s_nop 0
	s_setprio 0
	v_mfma_scale_f32_16x16x128_f8f6f4 v[94:97], v[18:25], v[210:217], v[94:97], v203, v204 op_sel_hi:[0,0,0]
	v_mfma_scale_f32_16x16x128_f8f6f4 v[90:93], v[26:33], v[210:217], v[90:93], v203, v204 op_sel_hi:[0,0,0]
	v_mfma_scale_f32_16x16x128_f8f6f4 v[78:81], v[18:25], v[218:225], v[78:81], v203, v204 op_sel_hi:[0,0,0]
	v_mfma_scale_f32_16x16x128_f8f6f4 v[74:77], v[26:33], v[218:225], v[74:77], v203, v204 op_sel_hi:[0,0,0]
	v_mfma_scale_f32_16x16x128_f8f6f4 v[62:65], v[18:25], v[226:233], v[62:65], v203, v204 op_sel_hi:[0,0,0]
	v_mfma_scale_f32_16x16x128_f8f6f4 v[58:61], v[26:33], v[226:233], v[58:61], v203, v204 op_sel_hi:[0,0,0]
	v_mfma_scale_f32_16x16x128_f8f6f4 v[46:49], v[18:25], v[234:241], v[46:49], v203, v204 op_sel_hi:[0,0,0]
	v_mfma_scale_f32_16x16x128_f8f6f4 v[42:45], v[26:33], v[234:241], v[42:45], v203, v204 op_sel_hi:[0,0,0]
	s_setprio 1
	s_barrier
	s_add_i32 s46, s46, 2
	s_add_u32 s44, s44, 0x100
	s_addc_u32 s45, s45, 0
	s_add_u32 s6, s6, 0x100
	s_addc_u32 s7, s7, 0
	s_cmp_gt_u32 s46, 13
	s_cbranch_scc0 .LBB0_2182
	s_setprio 0
	s_and_b64 vcc, exec, s[22:23]
	s_cbranch_vccz .LBB0_2185
	s_barrier

; #define GAS __attribute__((address_space(1)))
; #define PG8_STAGE(bufoff, gbase, voff) do { _Pragma("unroll") for (int _i = 0; _i < 2; ++_i) \
;         __builtin_amdgcn_global_load_lds((const GAS unsigned*)((const GAS char*)(gbase) + (voff)[_i]), (LAS unsigned*)(lds + (bufoff) + ldsw + _i * 8192), 16, 0, 0); } while (0)
; #define PG8_LDA(dst, b, h) do { _Pragma("unroll") for (int m = 0; m < 4; ++m) { dst[m].lo = *(const LAS i32x4v*)(lds + PG8_SA(b, h) + (FP8 ? aoff8[0] : aoff) + m * 2048); dst[m].hi = *(const LAS i32x4v*)(lds + PG8_SA(b, h) + (FP8 ? aoff8[1] : aoff + 1024) + m * 2048); } } while (0)
; #define PG8_LDB(dst, b, h) do { _Pragma("unroll") for (int n = 0; n < 2; ++n) { dst[n].lo = *(const LAS i32x4v*)(lds + PG8_SB(b, h) + (FP8 ? boff8[0] : boff) + n * 2048); dst[n].hi = *(const LAS i32x4v*)(lds + PG8_SB(b, h) + (FP8 ? boff8[1] : boff + 1024) + n * 2048); } } while (0)
; #define PG8_WAIT_V(n) asm volatile("s_waitcnt vmcnt(" #n ")" ::: "memory")
; template <class Epi, class Sched, bool GATHER, bool FP8 = false, bool UNI = false>
; __device__ __forceinline__ void gemm_phase(LAS unsigned char* lds, const Sched& S, const Epi& E) {
;     ...
;         for (int t = 0; t < nt; t += 2) {
;             const bool last = (t == nt - 2);
;             const GAS char* a1 = cA + (size_t)(t + 1) * 128;
;             const GAS char* a2 = last ? nA : cA + (size_t)(t + 2) * 128; const GAS char* b2 = last ? nB : cB + (size_t)(t + 2) * 128;
;             const GAS char* a3 = a2 + 128; const GAS char* b3 = b2 + 128;
;             const size_t hB2 = last ? hBn : hBc;
;             unsigned oa0[2], oa1[2], ob[2];
; #pragma unroll
;             for (int i = 0; i < 2; ++i) { if constexpr (UNI) { oa0[i] = aoc[0][i]; oa1[i] = aoc[1][i]; ob[i] = boc[i]; } else { oa0[i] = last ? aon[0][i] : aoc[0][i]; oa1[i] = last ? aon[1][i] : aoc[1][i]; ob[i] = last ? bon[i] : boc[i]; } }
;             PG8_LDB(B0, 0, 0); PG8_LDB(B1, 0, 1); PG8_SCHED; PG8_LDA(At, 0, 0); PG8_STAGE(PG8_SA(1, 1), a1, aoc[1]);
;             PG8_WAIT_V(8); PG8_WAIT_L(0); PG8_BAR; PG8_MMA(0, 0, At, B0); PG8_MMA(0, 1, At, B1); PG8_BAR; PG8_SCHED;
;             PG8_LDA(At, 0, 1); PG8_STAGE(PG8_SB(0, 0), b2, ob); PG8_STAGE(PG8_SB(0, 1), b2 + hB2, ob); PG8_STAGE(PG8_SA(0, 0), a2, oa0);
;             PG8_WAIT_V(8); PG8_WAIT_L(0); PG8_BAR; PG8_MMA(1, 0, At, B0); PG8_MMA(1, 1, At, B1); PG8_BAR; PG8_SCHED;
.LBB0_3098:
	s_add_u32 s40, s16, s6
	s_addc_u32 s41, s17, s7
	v_add_u32_e32 v2, s33, v194
	v_add_u32_e32 v3, s33, v195
	v_add_u32_e32 v6, s56, v194
	v_add_u32_e32 v14, s56, v195
	s_add_u32 s44, s40, 0x100
	ds_read_b128 v[18:21], v2
	ds_read_b128 v[26:29], v2 offset:2048
	ds_read_b128 v[22:25], v3
	ds_read_b128 v[30:33], v3 offset:2048
	ds_read_b128 v[2:5], v6
	ds_read_b128 v[10:13], v6 offset:2048
	ds_read_b128 v[6:9], v14
	ds_read_b128 v[14:17], v14 offset:2048
	s_addc_u32 s45, s41, 0
	s_add_u32 s88, s46, s6
	s_addc_u32 s89, s47, s7
	s_cmpk_eq_i32 s6, 0x700
	s_cselect_b64 vcc, -1, 0
	s_and_b64 s[40:41], vcc, exec
	v_cndmask_b32_e32 v170, v176, v205, vcc
	s_cselect_b32 s45, s39, s45
	s_cselect_b32 s44, s38, s44
	v_cndmask_b32_e32 v175, v174, v204, vcc
	v_cndmask_b32_e32 v240, v172, v203, vcc
	v_cndmask_b32_e32 v179, v178, v206, vcc
	s_cselect_b32 s41, s37, s89
	s_cselect_b32 s40, s36, s88
	v_lshl_add_u64 v[232:233], v[182:183], 0, s[6:7]
	s_add_i32 m0, s59, 0xc000
	ds_read_b128 v[184:187], v197
	ds_read_b128 v[208:211], v197 offset:2048
	ds_read_b128 v[188:191], v198
	ds_read_b128 v[212:215], v198 offset:2048
	ds_read_b128 v[216:219], v197 offset:4096
	ds_read_b128 v[224:227], v197 offset:6144
	ds_read_b128 v[220:223], v198 offset:4096
	ds_read_b128 v[228:231], v198 offset:6144
	global_load_lds_dwordx4 v[232:233], off
	v_lshl_add_u64 v[232:233], v[180:181], 0, s[6:7]
	s_add_i32 m0, s59, 0xe000
	s_nop 0
	global_load_lds_dwordx4 v[232:233], off
	s_waitcnt vmcnt(8)
	s_waitcnt lgkmcnt(0)
	s_barrier
	s_setprio 0
	s_waitcnt lgkmcnt(0)
	v_mfma_scale_f32_16x16x128_f8f6f4 v[134:137], v[18:25], v[184:191], v[134:137], v199, v200 op_sel_hi:[0,0,0]
	v_mfma_scale_f32_16x16x128_f8f6f4 v[130:133], v[26:33], v[184:191], v[130:133], v199, v200 op_sel_hi:[0,0,0]
	v_mfma_scale_f32_16x16x128_f8f6f4 v[126:129], v[18:25], v[208:215], v[126:129], v199, v200 op_sel_hi:[0,0,0]
	v_mfma_scale_f32_16x16x128_f8f6f4 v[122:125], v[26:33], v[208:215], v[122:125], v199, v200 op_sel_hi:[0,0,0]
	v_mfma_scale_f32_16x16x128_f8f6f4 v[118:121], v[18:25], v[216:223], v[118:121], v199, v200 op_sel_hi:[0,0,0]
	v_mfma_scale_f32_16x16x128_f8f6f4 v[114:117], v[26:33], v[216:223], v[114:117], v199, v200 op_sel_hi:[0,0,0]
	v_mfma_scale_f32_16x16x128_f8f6f4 v[110:113], v[18:25], v[224:231], v[110:113], v199, v200 op_sel_hi:[0,0,0]
	v_mfma_scale_f32_16x16x128_f8f6f4 v[106:109], v[26:33], v[224:231], v[106:109], v199, v200 op_sel_hi:[0,0,0]
	s_nop 0
	s_setprio 0
	v_mfma_scale_f32_16x16x128_f8f6f4 v[102:105], v[2:9], v[184:191], v[102:105], v199, v200 op_sel_hi:[0,0,0]
	v_mfma_scale_f32_16x16x128_f8f6f4 v[98:101], v[10:17], v[184:191], v[98:101], v199, v200 op_sel_hi:[0,0,0]
	v_mfma_scale_f32_16x16x128_f8f6f4 v[94:97], v[2:9], v[208:215], v[94:97], v199, v200 op_sel_hi:[0,0,0]
	v_mfma_scale_f32_16x16x128_f8f6f4 v[90:93], v[10:17], v[208:215], v[90:93], v199, v200 op_sel_hi:[0,0,0]
	v_mfma_scale_f32_16x16x128_f8f6f4 v[86:89], v[2:9], v[216:223], v[86:89], v199, v200 op_sel_hi:[0,0,0]
	v_mfma_scale_f32_16x16x128_f8f6f4 v[82:85], v[10:17], v[216:223], v[82:85], v199, v200 op_sel_hi:[0,0,0]
	v_mfma_scale_f32_16x16x128_f8f6f4 v[78:81], v[2:9], v[224:231], v[78:81], v199, v200 op_sel_hi:[0,0,0]
	v_mfma_scale_f32_16x16x128_f8f6f4 v[74:77], v[10:17], v[224:231], v[74:77], v199, v200 op_sel_hi:[0,0,0]
	s_setprio 1
	s_barrier
	s_mov_b32 m0, s50
	v_lshl_add_u64 v[184:185], s[40:41], 0, v[168:169]
	s_add_u32 s88, s40, 0x40000
	ds_read_b128 v[208:211], v197 offset:16384
	ds_read_b128 v[216:219], v197 offset:18432
	ds_read_b128 v[212:215], v198 offset:16384
	ds_read_b128 v[220:223], v198 offset:18432
	ds_read_b128 v[224:227], v197 offset:20480
	ds_read_b128 v[232:235], v197 offset:22528
	ds_read_b128 v[228:231], v198 offset:20480
	ds_read_b128 v[236:239], v198 offset:22528
	global_load_lds_dwordx4 v[184:185], off
	v_lshl_add_u64 v[186:187], s[40:41], 0, v[166:167]
	s_mov_b32 m0, s51
	s_addc_u32 s89, s41, 0
	global_load_lds_dwordx4 v[186:187], off
	v_lshl_add_u64 v[188:189], s[88:89], 0, v[168:169]
	s_mov_b32 m0, s57
	v_mov_b32_e32 v241, v171
	global_load_lds_dwordx4 v[188:189], off
	v_lshl_add_u64 v[188:189], s[88:89], 0, v[166:167]
	s_mov_b32 m0, s58
	v_lshl_add_u64 v[190:191], s[44:45], 0, v[170:171]
	global_load_lds_dwordx4 v[188:189], off
	s_mov_b32 m0, s59
	v_lshl_add_u64 v[188:189], s[44:45], 0, v[240:241]
	global_load_lds_dwordx4 v170, s[44:45]
	s_mov_b32 m0, s60
	s_nop 0
	global_load_lds_dwordx4 v240, s[44:45]
	s_waitcnt vmcnt(8)
	s_waitcnt lgkmcnt(0)
	s_barrier
	s_setprio 0
	s_waitcnt lgkmcnt(0)
	v_mfma_scale_f32_16x16x128_f8f6f4 v[70:73], v[18:25], v[208:215], v[70:73], v199, v200 op_sel_hi:[0,0,0]
	v_mfma_scale_f32_16x16x128_f8f6f4 v[66:69], v[26:33], v[208:215], v[66:69], v199, v200 op_sel_hi:[0,0,0]
	v_mfma_scale_f32_16x16x128_f8f6f4 v[62:65], v[18:25], v[216:223], v[62:65], v199, v200 op_sel_hi:[0,0,0]
	v_mfma_scale_f32_16x16x128_f8f6f4 v[58:61], v[26:33], v[216:223], v[58:61], v199, v200 op_sel_hi:[0,0,0]
	v_mfma_scale_f32_16x16x128_f8f6f4 v[54:57], v[18:25], v[224:231], v[54:57], v199, v200 op_sel_hi:[0,0,0]
	v_mfma_scale_f32_16x16x128_f8f6f4 v[50:53], v[26:33], v[224:231], v[50:53], v199, v200 op_sel_hi:[0,0,0]
	v_mfma_scale_f32_16x16x128_f8f6f4 v[46:49], v[18:25], v[232:239], v[46:49], v199, v200 op_sel_hi:[0,0,0]
	v_mfma_scale_f32_16x16x128_f8f6f4 v[42:45], v[26:33], v[232:239], v[42:45], v199, v200 op_sel_hi:[0,0,0]
	s_nop 0
	s_setprio 0
	v_mfma_scale_f32_16x16x128_f8f6f4 v[38:41], v[2:9], v[208:215], v[38:41], v199, v200 op_sel_hi:[0,0,0]
	v_mfma_scale_f32_16x16x128_f8f6f4 v[34:37], v[10:17], v[208:215], v[34:37], v199, v200 op_sel_hi:[0,0,0]
	v_mfma_scale_f32_16x16x128_f8f6f4 v[138:141], v[2:9], v[216:223], v[138:141], v199, v200 op_sel_hi:[0,0,0]
	v_mfma_scale_f32_16x16x128_f8f6f4 v[142:145], v[10:17], v[216:223], v[142:145], v199, v200 op_sel_hi:[0,0,0]
	v_mfma_scale_f32_16x16x128_f8f6f4 v[146:149], v[2:9], v[224:231], v[146:149], v199, v200 op_sel_hi:[0,0,0]
	v_mfma_scale_f32_16x16x128_f8f6f4 v[150:153], v[10:17], v[224:231], v[150:153], v199, v200 op_sel_hi:[0,0,0]
	v_mfma_scale_f32_16x16x128_f8f6f4 v[154:157], v[2:9], v[232:239], v[154:157], v199, v200 op_sel_hi:[0,0,0]
	v_mfma_scale_f32_16x16x128_f8f6f4 v[158:161], v[10:17], v[232:239], v[158:161], v199, v200 op_sel_hi:[0,0,0]
	s_setprio 1
	s_barrier
; #define PG8_STAGE(bufoff, gbase, voff) do { _Pragma("unroll") for (int _i = 0; _i < 2; ++_i) \
;         __builtin_amdgcn_global_load_lds((const GAS unsigned*)((const GAS char*)(gbase) + (voff)[_i]), (LAS unsigned*)(lds + (bufoff) + ldsw + _i * 8192), 16, 0, 0); } while (0)
; #define PG8_LDA(dst, b, h) do { _Pragma("unroll") for (int m = 0; m < 4; ++m) { dst[m].lo = *(const LAS i32x4v*)(lds + PG8_SA(b, h) + (FP8 ? aoff8[0] : aoff) + m * 2048); dst[m].hi = *(const LAS i32x4v*)(lds + PG8_SA(b, h) + (FP8 ? aoff8[1] : aoff + 1024) + m * 2048); } } while (0)
; #define PG8_LDB(dst, b, h) do { _Pragma("unroll") for (int n = 0; n < 2; ++n) { dst[n].lo = *(const LAS i32x4v*)(lds + PG8_SB(b, h) + (FP8 ? boff8[0] : boff) + n * 2048); dst[n].hi = *(const LAS i32x4v*)(lds + PG8_SB(b, h) + (FP8 ? boff8[1] : boff + 1024) + n * 2048); } } while (0)
; #define PG8_WAIT_V(n) asm volatile("s_waitcnt vmcnt(" #n ")" ::: "memory")
; #define PG8_WAIT_L(n) asm volatile("s_waitcnt lgkmcnt(" #n ")" ::: "memory")
; #define PG8_BAR __builtin_amdgcn_s_barrier()
; #define PG8_SCHED __builtin_amdgcn_sched_barrier(0)
; template <class Epi, class Sched, bool GATHER, bool FP8 = false, bool UNI = false>
; __device__ __forceinline__ void gemm_phase(LAS unsigned char* lds, const Sched& S, const Epi& E) {
;     ...
;             PG8_LDB(B0, 1, 0); PG8_LDB(B1, 1, 1); PG8_SCHED; PG8_LDA(At, 1, 0); PG8_STAGE(PG8_SA(0, 1), a2, oa1);
;             PG8_WAIT_V(8); PG8_WAIT_L(0); PG8_BAR; PG8_MMA(0, 0, At, B0); PG8_MMA(0, 1, At, B1); PG8_BAR; PG8_SCHED;
;             PG8_LDA(At, 1, 1); PG8_STAGE(PG8_SB(1, 0), b3, ob); PG8_STAGE(PG8_SB(1, 1), b3 + hB2, ob); PG8_STAGE(PG8_SA(1, 0), a3, oa0);
;             PG8_WAIT_V(8); PG8_WAIT_L(0); PG8_BAR; PG8_MMA(1, 0, At, B0); PG8_MMA(1, 1, At, B1); PG8_BAR; PG8_SCHED;
;         }
	v_add_u32_e32 v6, s67, v194
	v_add_u32_e32 v14, s67, v195
	v_add_u32_e32 v22, s72, v194
	v_add_u32_e32 v30, s72, v195
	ds_read_b128 v[2:5], v6
	ds_read_b128 v[10:13], v6 offset:2048
	ds_read_b128 v[6:9], v14
	ds_read_b128 v[14:17], v14 offset:2048
	ds_read_b128 v[18:21], v22
	ds_read_b128 v[26:29], v22 offset:2048
	ds_read_b128 v[22:25], v30
	ds_read_b128 v[30:33], v30 offset:2048
	s_mov_b32 m0, s61
	ds_read_b128 v[208:211], v197 offset:32768
	ds_read_b128 v[216:219], v197 offset:34816
	ds_read_b128 v[212:215], v198 offset:32768
	ds_read_b128 v[220:223], v198 offset:34816
	ds_read_b128 v[224:227], v197 offset:36864
	ds_read_b128 v[232:235], v197 offset:38912
	ds_read_b128 v[228:231], v198 offset:36864
	ds_read_b128 v[236:239], v198 offset:38912
	global_load_lds_dwordx4 v175, s[44:45]
	s_mov_b32 m0, s62
	s_nop 0
	global_load_lds_dwordx4 v179, s[44:45]
	s_waitcnt vmcnt(8)
	s_waitcnt lgkmcnt(0)
	s_barrier
	s_setprio 0
	s_waitcnt lgkmcnt(0)
	v_mfma_scale_f32_16x16x128_f8f6f4 v[134:137], v[2:9], v[208:215], v[134:137], v199, v200 op_sel_hi:[0,0,0]
	v_mfma_scale_f32_16x16x128_f8f6f4 v[130:133], v[10:17], v[208:215], v[130:133], v199, v200 op_sel_hi:[0,0,0]
	v_mfma_scale_f32_16x16x128_f8f6f4 v[126:129], v[2:9], v[216:223], v[126:129], v199, v200 op_sel_hi:[0,0,0]
	v_mfma_scale_f32_16x16x128_f8f6f4 v[122:125], v[10:17], v[216:223], v[122:125], v199, v200 op_sel_hi:[0,0,0]
	v_mfma_scale_f32_16x16x128_f8f6f4 v[118:121], v[2:9], v[224:231], v[118:121], v199, v200 op_sel_hi:[0,0,0]
	v_mfma_scale_f32_16x16x128_f8f6f4 v[114:117], v[10:17], v[224:231], v[114:117], v199, v200 op_sel_hi:[0,0,0]
	v_mfma_scale_f32_16x16x128_f8f6f4 v[110:113], v[2:9], v[232:239], v[110:113], v199, v200 op_sel_hi:[0,0,0]
	v_mfma_scale_f32_16x16x128_f8f6f4 v[106:109], v[10:17], v[232:239], v[106:109], v199, v200 op_sel_hi:[0,0,0]
	s_nop 0
	s_setprio 0
	v_mfma_scale_f32_16x16x128_f8f6f4 v[102:105], v[18:25], v[208:215], v[102:105], v199, v200 op_sel_hi:[0,0,0]
	v_mfma_scale_f32_16x16x128_f8f6f4 v[98:101], v[26:33], v[208:215], v[98:101], v199, v200 op_sel_hi:[0,0,0]
	v_mfma_scale_f32_16x16x128_f8f6f4 v[94:97], v[18:25], v[216:223], v[94:97], v199, v200 op_sel_hi:[0,0,0]
	v_mfma_scale_f32_16x16x128_f8f6f4 v[90:93], v[26:33], v[216:223], v[90:93], v199, v200 op_sel_hi:[0,0,0]
	v_mfma_scale_f32_16x16x128_f8f6f4 v[86:89], v[18:25], v[224:231], v[86:89], v199, v200 op_sel_hi:[0,0,0]
	v_mfma_scale_f32_16x16x128_f8f6f4 v[82:85], v[26:33], v[224:231], v[82:85], v199, v200 op_sel_hi:[0,0,0]
	v_mfma_scale_f32_16x16x128_f8f6f4 v[78:81], v[18:25], v[232:239], v[78:81], v199, v200 op_sel_hi:[0,0,0]
	v_mfma_scale_f32_16x16x128_f8f6f4 v[74:77], v[26:33], v[232:239], v[74:77], v199, v200 op_sel_hi:[0,0,0]
	s_setprio 1
	s_barrier
	s_mov_b32 m0, s68
	v_lshl_add_u64 v[184:185], v[184:185], 0, s[22:23]
	s_add_u32 s40, s40, 0x40080
	ds_read_b128 v[208:211], v197 offset:49152
	ds_read_b128 v[216:219], v197 offset:51200
	ds_read_b128 v[212:215], v198 offset:49152
	ds_read_b128 v[220:223], v198 offset:51200
	ds_read_b128 v[224:227], v197 offset:53248
	ds_read_b128 v[232:235], v197 offset:55296
	ds_read_b128 v[228:231], v198 offset:53248
	ds_read_b128 v[236:239], v198 offset:55296
	global_load_lds_dwordx4 v[184:185], off
	v_lshl_add_u64 v[184:185], v[186:187], 0, s[22:23]
	s_mov_b32 m0, s69
	s_addc_u32 s41, s41, 0
	global_load_lds_dwordx4 v[184:185], off
	v_lshl_add_u64 v[184:185], s[40:41], 0, v[168:169]
	s_mov_b32 m0, s73
	s_nop 0
	global_load_lds_dwordx4 v[184:185], off
	v_lshl_add_u64 v[184:185], s[40:41], 0, v[166:167]
	s_mov_b32 m0, s74
	s_nop 0
	global_load_lds_dwordx4 v[184:185], off
	v_lshl_add_u64 v[184:185], v[190:191], 0, s[22:23]
	s_mov_b32 m0, s70
	s_nop 0
	global_load_lds_dwordx4 v[184:185], off
	v_lshl_add_u64 v[184:185], v[188:189], 0, s[22:23]
	s_mov_b32 m0, s71
	s_nop 0
	global_load_lds_dwordx4 v[184:185], off
	s_waitcnt vmcnt(8)
	s_waitcnt lgkmcnt(0)
	s_barrier
	s_setprio 0
	s_waitcnt lgkmcnt(0)
	v_mfma_scale_f32_16x16x128_f8f6f4 v[70:73], v[2:9], v[208:215], v[70:73], v199, v200 op_sel_hi:[0,0,0]
	v_mfma_scale_f32_16x16x128_f8f6f4 v[66:69], v[10:17], v[208:215], v[66:69], v199, v200 op_sel_hi:[0,0,0]
	v_mfma_scale_f32_16x16x128_f8f6f4 v[62:65], v[2:9], v[216:223], v[62:65], v199, v200 op_sel_hi:[0,0,0]
	v_mfma_scale_f32_16x16x128_f8f6f4 v[58:61], v[10:17], v[216:223], v[58:61], v199, v200 op_sel_hi:[0,0,0]
	v_mfma_scale_f32_16x16x128_f8f6f4 v[54:57], v[2:9], v[224:231], v[54:57], v199, v200 op_sel_hi:[0,0,0]
	v_mfma_scale_f32_16x16x128_f8f6f4 v[50:53], v[10:17], v[224:231], v[50:53], v199, v200 op_sel_hi:[0,0,0]
	v_mfma_scale_f32_16x16x128_f8f6f4 v[46:49], v[2:9], v[232:239], v[46:49], v199, v200 op_sel_hi:[0,0,0]
	v_mfma_scale_f32_16x16x128_f8f6f4 v[42:45], v[10:17], v[232:239], v[42:45], v199, v200 op_sel_hi:[0,0,0]
	s_nop 0
	s_setprio 0
	v_mfma_scale_f32_16x16x128_f8f6f4 v[38:41], v[18:25], v[208:215], v[38:41], v199, v200 op_sel_hi:[0,0,0]
	v_mfma_scale_f32_16x16x128_f8f6f4 v[34:37], v[26:33], v[208:215], v[34:37], v199, v200 op_sel_hi:[0,0,0]
	v_mfma_scale_f32_16x16x128_f8f6f4 v[138:141], v[18:25], v[216:223], v[138:141], v199, v200 op_sel_hi:[0,0,0]
	v_mfma_scale_f32_16x16x128_f8f6f4 v[142:145], v[26:33], v[216:223], v[142:145], v199, v200 op_sel_hi:[0,0,0]
	v_mfma_scale_f32_16x16x128_f8f6f4 v[146:149], v[18:25], v[224:231], v[146:149], v199, v200 op_sel_hi:[0,0,0]
	v_mfma_scale_f32_16x16x128_f8f6f4 v[150:153], v[26:33], v[224:231], v[150:153], v199, v200 op_sel_hi:[0,0,0]
	v_mfma_scale_f32_16x16x128_f8f6f4 v[154:157], v[18:25], v[232:239], v[154:157], v199, v200 op_sel_hi:[0,0,0]
	v_mfma_scale_f32_16x16x128_f8f6f4 v[158:161], v[26:33], v[232:239], v[158:161], v199, v200 op_sel_hi:[0,0,0]
	s_setprio 1
	s_barrier
	s_add_i32 s87, s87, 2
	s_add_u32 s6, s6, 0x100
	s_addc_u32 s7, s7, 0
	s_cmp_gt_u32 s87, 13
	s_cbranch_scc0 .LBB0_3098
	s_setprio 0
	s_and_b64 vcc, exec, s[26:27]
	s_cbranch_vccz .LBB0_3101
	s_barrier
